# GEMM K-loops: first iteration peeled with srcC=0, accumulator zeroing v_movs removed
# baseline (speedup 1.0000x reference)
.LBB0_210:
	s_ashr_i32 s49, s48, 31
	s_lshl_b64 s[4:5], s[48:49], 19
	s_add_u32 s50, s6, s4
	s_addc_u32 s51, s7, s5
	s_and_b64 s[4:5], s[38:39], exec
	s_cselect_b32 s49, s51, s41
	s_cselect_b32 s64, s50, s40
	s_ashr_i32 s45, s44, 31
	s_lshl_b64 s[4:5], s[44:45], 19
	s_add_u32 s52, s8, s4
	s_addc_u32 s53, s9, s5
	s_and_b64 s[4:5], s[38:39], exec
	s_cselect_b32 s45, s53, s43
	s_cselect_b32 s65, s52, s42
	s_add_u32 s70, s64, 0x80
	s_addc_u32 s71, s49, 0
	s_add_u32 s4, s40, 0x40080
	s_addc_u32 s5, s41, 0
	s_add_u32 s78, s42, 0x100
	v_lshl_add_u64 v[144:145], s[4:5], 0, v[140:141]
	v_lshl_add_u64 v[146:147], s[4:5], 0, v[142:143]
	s_addc_u32 s79, s43, 0
	s_mov_b32 s80, -2
	s_mov_b64 s[42:43], 0
	s_waitcnt lgkmcnt(0)
	s_add_u32 s4, s40, s42
	s_addc_u32 s5, s41, s43
	s_add_u32 s81, s4, 0x100
	s_addc_u32 s82, s5, 0
	s_add_u32 s60, s78, s42
	s_addc_u32 s61, s79, s43
	s_add_u32 s4, s4, 0x180
	s_addc_u32 s5, s5, 0
	s_add_i32 s83, 0, 0x10000
	s_add_i32 s84, 0, 0x14000
	v_add_u32_e32 v2, s83, v151
	s_waitcnt vmcnt(0)
	ds_read_b128 v[154:157], v2
	ds_read_b128 v[158:161], v2 offset:1024
	ds_read_b128 v[162:165], v2 offset:2048
	ds_read_b128 v[166:169], v2 offset:3072
	v_add_u32_e32 v2, s84, v151
	ds_read_b128 v[170:173], v2
	ds_read_b128 v[174:177], v2 offset:1024
	ds_read_b128 v[178:181], v2 offset:2048
	ds_read_b128 v[182:185], v2 offset:3072
	s_cmpk_eq_i32 s42, 0x700
	s_cselect_b32 s13, s71, s5
	s_cselect_b32 s12, s70, s4
	s_cselect_b32 s61, s45, s61
	s_cselect_b32 s60, s65, s60
	s_cselect_b32 s5, s49, s82
	s_cselect_b32 s4, s64, s81
	v_lshl_add_u64 v[148:149], v[144:145], 0, s[42:43]
	s_add_i32 m0, s17, 0xc000
	ds_read_b128 v[186:189], v153
	ds_read_b128 v[190:193], v153 offset:1024
	ds_read_b128 v[204:207], v153 offset:2048
	ds_read_b128 v[208:211], v153 offset:3072
	ds_read_b128 v[212:215], v153 offset:4096
	ds_read_b128 v[216:219], v153 offset:5120
	ds_read_b128 v[220:223], v153 offset:6144
	ds_read_b128 v[224:227], v153 offset:7168
	global_load_lds_dwordx4 v[148:149], off
	v_lshl_add_u64 v[148:149], v[146:147], 0, s[42:43]
	s_add_i32 m0, s17, 0xe000
	s_nop 0
	global_load_lds_dwordx4 v[148:149], off
	s_waitcnt vmcnt(8)
	s_waitcnt lgkmcnt(0)
	s_barrier
	s_setprio 1
	s_waitcnt lgkmcnt(0)
	v_mfma_f32_16x16x32_bf16 v[128:131], v[154:157], v[186:189], 0
	v_mfma_f32_16x16x32_bf16 v[124:127], v[162:165], v[186:189], 0
	v_mfma_f32_16x16x32_bf16 v[112:115], v[154:157], v[204:207], 0
	v_mfma_f32_16x16x32_bf16 v[108:111], v[162:165], v[204:207], 0
	v_mfma_f32_16x16x32_bf16 v[96:99], v[154:157], v[212:215], 0
	v_mfma_f32_16x16x32_bf16 v[92:95], v[162:165], v[212:215], 0
	v_mfma_f32_16x16x32_bf16 v[80:83], v[154:157], v[220:223], 0
	v_mfma_f32_16x16x32_bf16 v[76:79], v[162:165], v[220:223], 0
	v_mfma_f32_16x16x32_bf16 v[128:131], v[158:161], v[190:193], v[128:131]
	v_mfma_f32_16x16x32_bf16 v[124:127], v[166:169], v[190:193], v[124:127]
	v_mfma_f32_16x16x32_bf16 v[112:115], v[158:161], v[208:211], v[112:115]
	v_mfma_f32_16x16x32_bf16 v[108:111], v[166:169], v[208:211], v[108:111]
	v_mfma_f32_16x16x32_bf16 v[96:99], v[158:161], v[216:219], v[96:99]
	v_mfma_f32_16x16x32_bf16 v[92:95], v[166:169], v[216:219], v[92:95]
	v_mfma_f32_16x16x32_bf16 v[80:83], v[158:161], v[224:227], v[80:83]
	v_mfma_f32_16x16x32_bf16 v[76:79], v[166:169], v[224:227], v[76:79]
	s_setprio 0
	s_setprio 1
	v_mfma_f32_16x16x32_bf16 v[120:123], v[170:173], v[186:189], 0
	v_mfma_f32_16x16x32_bf16 v[116:119], v[178:181], v[186:189], 0
	v_mfma_f32_16x16x32_bf16 v[104:107], v[170:173], v[204:207], 0
	v_mfma_f32_16x16x32_bf16 v[100:103], v[178:181], v[204:207], 0
	v_mfma_f32_16x16x32_bf16 v[88:91], v[170:173], v[212:215], 0
	v_mfma_f32_16x16x32_bf16 v[84:87], v[178:181], v[212:215], 0
	v_mfma_f32_16x16x32_bf16 v[72:75], v[170:173], v[220:223], 0
	v_mfma_f32_16x16x32_bf16 v[68:71], v[178:181], v[220:223], 0
	v_mfma_f32_16x16x32_bf16 v[120:123], v[174:177], v[190:193], v[120:123]
	v_mfma_f32_16x16x32_bf16 v[116:119], v[182:185], v[190:193], v[116:119]
	v_mfma_f32_16x16x32_bf16 v[104:107], v[174:177], v[208:211], v[104:107]
	v_mfma_f32_16x16x32_bf16 v[100:103], v[182:185], v[208:211], v[100:103]
	v_mfma_f32_16x16x32_bf16 v[88:91], v[174:177], v[216:219], v[88:91]
	v_mfma_f32_16x16x32_bf16 v[84:87], v[182:185], v[216:219], v[84:87]
	v_mfma_f32_16x16x32_bf16 v[72:75], v[174:177], v[224:227], v[72:75]
	v_mfma_f32_16x16x32_bf16 v[68:71], v[182:185], v[224:227], v[68:71]
	s_setprio 0
	s_barrier
	s_add_i32 s81, s83, s16
	v_lshl_add_u64 v[148:149], s[60:61], 0, v[136:137]
	s_mov_b32 m0, s81
	ds_read_b128 v[186:189], v153 offset:16384
	ds_read_b128 v[190:193], v153 offset:17408
	ds_read_b128 v[204:207], v153 offset:18432
	ds_read_b128 v[208:211], v153 offset:19456
	ds_read_b128 v[212:215], v153 offset:20480
	ds_read_b128 v[216:219], v153 offset:21504
	ds_read_b128 v[220:223], v153 offset:22528
	ds_read_b128 v[224:227], v153 offset:23552
	global_load_lds_dwordx4 v[148:149], off
	s_add_i32 m0, s81, 0x2000
	s_add_u32 s82, s60, 0x40000
	v_lshl_add_u64 v[194:195], s[60:61], 0, v[132:133]
	s_addc_u32 s83, s61, 0
	s_add_i32 s81, s84, s16
	global_load_lds_dwordx4 v[194:195], off
	v_lshl_add_u64 v[196:197], s[82:83], 0, v[136:137]
	s_mov_b32 m0, s81
	s_nop 0
	global_load_lds_dwordx4 v[196:197], off
	v_lshl_add_u64 v[196:197], s[82:83], 0, v[132:133]
	s_add_i32 m0, s81, 0x2000
	s_nop 0
	global_load_lds_dwordx4 v[196:197], off
	v_lshl_add_u64 v[196:197], s[4:5], 0, v[138:139]
	s_mov_b32 m0, s17
	s_nop 0
	global_load_lds_dwordx4 v[196:197], off
	v_lshl_add_u64 v[196:197], s[4:5], 0, v[134:135]
	s_mov_b32 m0, s46
	s_nop 0
	global_load_lds_dwordx4 v[196:197], off
	s_waitcnt vmcnt(8)
	s_waitcnt lgkmcnt(0)
	s_barrier
	s_setprio 1
	s_waitcnt lgkmcnt(0)
	v_mfma_f32_16x16x32_bf16 v[64:67], v[154:157], v[186:189], 0
	v_mfma_f32_16x16x32_bf16 v[60:63], v[162:165], v[186:189], 0
	v_mfma_f32_16x16x32_bf16 v[48:51], v[154:157], v[204:207], 0
	v_mfma_f32_16x16x32_bf16 v[44:47], v[162:165], v[204:207], 0
	v_mfma_f32_16x16x32_bf16 v[32:35], v[154:157], v[212:215], 0
	v_mfma_f32_16x16x32_bf16 v[28:31], v[162:165], v[212:215], 0
	v_mfma_f32_16x16x32_bf16 v[16:19], v[154:157], v[220:223], 0
	v_mfma_f32_16x16x32_bf16 v[12:15], v[162:165], v[220:223], 0
	v_mfma_f32_16x16x32_bf16 v[64:67], v[158:161], v[190:193], v[64:67]
	v_mfma_f32_16x16x32_bf16 v[60:63], v[166:169], v[190:193], v[60:63]
	v_mfma_f32_16x16x32_bf16 v[48:51], v[158:161], v[208:211], v[48:51]
	v_mfma_f32_16x16x32_bf16 v[44:47], v[166:169], v[208:211], v[44:47]
	v_mfma_f32_16x16x32_bf16 v[32:35], v[158:161], v[216:219], v[32:35]
	v_mfma_f32_16x16x32_bf16 v[28:31], v[166:169], v[216:219], v[28:31]
	v_mfma_f32_16x16x32_bf16 v[16:19], v[158:161], v[224:227], v[16:19]
	v_mfma_f32_16x16x32_bf16 v[12:15], v[166:169], v[224:227], v[12:15]
	s_setprio 0
	s_setprio 1
	v_mfma_f32_16x16x32_bf16 v[56:59], v[170:173], v[186:189], 0
	v_mfma_f32_16x16x32_bf16 v[52:55], v[178:181], v[186:189], 0
	v_mfma_f32_16x16x32_bf16 v[40:43], v[170:173], v[204:207], 0
	v_mfma_f32_16x16x32_bf16 v[36:39], v[178:181], v[204:207], 0
	v_mfma_f32_16x16x32_bf16 v[24:27], v[170:173], v[212:215], 0
	v_mfma_f32_16x16x32_bf16 v[20:23], v[178:181], v[212:215], 0
	v_mfma_f32_16x16x32_bf16 v[8:11], v[170:173], v[220:223], 0
	v_mfma_f32_16x16x32_bf16 v[4:7], v[178:181], v[220:223], 0
	v_mfma_f32_16x16x32_bf16 v[56:59], v[174:177], v[190:193], v[56:59]
	v_mfma_f32_16x16x32_bf16 v[52:55], v[182:185], v[190:193], v[52:55]
	v_mfma_f32_16x16x32_bf16 v[40:43], v[174:177], v[208:211], v[40:43]
	v_mfma_f32_16x16x32_bf16 v[36:39], v[182:185], v[208:211], v[36:39]
	v_mfma_f32_16x16x32_bf16 v[24:27], v[174:177], v[216:219], v[24:27]
	v_mfma_f32_16x16x32_bf16 v[20:23], v[182:185], v[216:219], v[20:23]
	v_mfma_f32_16x16x32_bf16 v[8:11], v[174:177], v[224:227], v[8:11]
	v_mfma_f32_16x16x32_bf16 v[4:7], v[182:185], v[224:227], v[4:7]
	s_setprio 0
	s_barrier
	s_add_i32 s81, 0, 0x18000
	v_add_u32_e32 v2, s81, v151
	s_add_i32 s82, 0, 0x1c000
	ds_read_b128 v[154:157], v2
	ds_read_b128 v[158:161], v2 offset:1024
	ds_read_b128 v[162:165], v2 offset:2048
	ds_read_b128 v[166:169], v2 offset:3072
	v_add_u32_e32 v2, s82, v151
	ds_read_b128 v[170:173], v2
	ds_read_b128 v[174:177], v2 offset:1024
	ds_read_b128 v[178:181], v2 offset:2048
	ds_read_b128 v[182:185], v2 offset:3072
	s_add_u32 s4, s4, 0x40000
	s_addc_u32 s5, s5, 0
	s_mov_b32 m0, s47
	v_lshl_add_u64 v[196:197], s[4:5], 0, v[138:139]
	ds_read_b128 v[186:189], v153 offset:32768
	ds_read_b128 v[190:193], v153 offset:33792
	ds_read_b128 v[204:207], v153 offset:34816
	ds_read_b128 v[208:211], v153 offset:35840
	ds_read_b128 v[212:215], v153 offset:36864
	ds_read_b128 v[216:219], v153 offset:37888
	ds_read_b128 v[220:223], v153 offset:38912
	ds_read_b128 v[224:227], v153 offset:39936
	global_load_lds_dwordx4 v[196:197], off
	v_lshl_add_u64 v[196:197], s[4:5], 0, v[134:135]
	s_mov_b32 m0, s58
	s_nop 0
	global_load_lds_dwordx4 v[196:197], off
	s_waitcnt vmcnt(8)
	s_waitcnt lgkmcnt(0)
	s_barrier
	s_setprio 1
	s_waitcnt lgkmcnt(0)
	v_mfma_f32_16x16x32_bf16 v[128:131], v[154:157], v[186:189], v[128:131]
	v_mfma_f32_16x16x32_bf16 v[124:127], v[162:165], v[186:189], v[124:127]
	v_mfma_f32_16x16x32_bf16 v[112:115], v[154:157], v[204:207], v[112:115]
	v_mfma_f32_16x16x32_bf16 v[108:111], v[162:165], v[204:207], v[108:111]
	v_mfma_f32_16x16x32_bf16 v[96:99], v[154:157], v[212:215], v[96:99]
	v_mfma_f32_16x16x32_bf16 v[92:95], v[162:165], v[212:215], v[92:95]
	v_mfma_f32_16x16x32_bf16 v[80:83], v[154:157], v[220:223], v[80:83]
	v_mfma_f32_16x16x32_bf16 v[76:79], v[162:165], v[220:223], v[76:79]
	v_mfma_f32_16x16x32_bf16 v[128:131], v[158:161], v[190:193], v[128:131]
	v_mfma_f32_16x16x32_bf16 v[124:127], v[166:169], v[190:193], v[124:127]
	v_mfma_f32_16x16x32_bf16 v[112:115], v[158:161], v[208:211], v[112:115]
	v_mfma_f32_16x16x32_bf16 v[108:111], v[166:169], v[208:211], v[108:111]
	v_mfma_f32_16x16x32_bf16 v[96:99], v[158:161], v[216:219], v[96:99]
	v_mfma_f32_16x16x32_bf16 v[92:95], v[166:169], v[216:219], v[92:95]
	v_mfma_f32_16x16x32_bf16 v[80:83], v[158:161], v[224:227], v[80:83]
	v_mfma_f32_16x16x32_bf16 v[76:79], v[166:169], v[224:227], v[76:79]
	s_setprio 0
	s_setprio 1
	v_mfma_f32_16x16x32_bf16 v[120:123], v[170:173], v[186:189], v[120:123]
	v_mfma_f32_16x16x32_bf16 v[116:119], v[178:181], v[186:189], v[116:119]
	v_mfma_f32_16x16x32_bf16 v[104:107], v[170:173], v[204:207], v[104:107]
	v_mfma_f32_16x16x32_bf16 v[100:103], v[178:181], v[204:207], v[100:103]
	v_mfma_f32_16x16x32_bf16 v[88:91], v[170:173], v[212:215], v[88:91]
	v_mfma_f32_16x16x32_bf16 v[84:87], v[178:181], v[212:215], v[84:87]
	v_mfma_f32_16x16x32_bf16 v[72:75], v[170:173], v[220:223], v[72:75]
	v_mfma_f32_16x16x32_bf16 v[68:71], v[178:181], v[220:223], v[68:71]
	v_mfma_f32_16x16x32_bf16 v[120:123], v[174:177], v[190:193], v[120:123]
	v_mfma_f32_16x16x32_bf16 v[116:119], v[182:185], v[190:193], v[116:119]
	v_mfma_f32_16x16x32_bf16 v[104:107], v[174:177], v[208:211], v[104:107]
	v_mfma_f32_16x16x32_bf16 v[100:103], v[182:185], v[208:211], v[100:103]
	v_mfma_f32_16x16x32_bf16 v[88:91], v[174:177], v[216:219], v[88:91]
	v_mfma_f32_16x16x32_bf16 v[84:87], v[182:185], v[216:219], v[84:87]
	v_mfma_f32_16x16x32_bf16 v[72:75], v[174:177], v[224:227], v[72:75]
	v_mfma_f32_16x16x32_bf16 v[68:71], v[182:185], v[224:227], v[68:71]
	s_setprio 0
	s_barrier
	s_add_i32 s4, s81, s16
	v_lshl_add_u64 v[148:149], v[148:149], 0, s[34:35]
	s_mov_b32 m0, s4
	ds_read_b128 v[186:189], v153 offset:49152
	ds_read_b128 v[190:193], v153 offset:50176
	ds_read_b128 v[204:207], v153 offset:51200
	ds_read_b128 v[208:211], v153 offset:52224
	ds_read_b128 v[212:215], v153 offset:53248
	ds_read_b128 v[216:219], v153 offset:54272
	ds_read_b128 v[220:223], v153 offset:55296
	ds_read_b128 v[224:227], v153 offset:56320
	global_load_lds_dwordx4 v[148:149], off
	s_add_i32 m0, s4, 0x2000
	s_add_u32 s4, s60, 0x40080
	v_lshl_add_u64 v[148:149], v[194:195], 0, s[34:35]
	s_addc_u32 s5, s61, 0
	s_add_i32 s60, s82, s16
	global_load_lds_dwordx4 v[148:149], off
	v_lshl_add_u64 v[148:149], s[4:5], 0, v[136:137]
	s_mov_b32 m0, s60
	s_nop 0
	global_load_lds_dwordx4 v[148:149], off
	v_lshl_add_u64 v[148:149], s[4:5], 0, v[132:133]
	s_add_i32 m0, s60, 0x2000
	s_nop 0
	global_load_lds_dwordx4 v[148:149], off
	v_lshl_add_u64 v[148:149], s[12:13], 0, v[138:139]
	s_mov_b32 m0, s74
	s_nop 0
	global_load_lds_dwordx4 v[148:149], off
	v_lshl_add_u64 v[148:149], s[12:13], 0, v[134:135]
	s_mov_b32 m0, s75
	s_nop 0
	global_load_lds_dwordx4 v[148:149], off
	s_waitcnt vmcnt(8)
	s_waitcnt lgkmcnt(0)
	s_barrier
	s_setprio 1
	s_waitcnt lgkmcnt(0)
	v_mfma_f32_16x16x32_bf16 v[64:67], v[154:157], v[186:189], v[64:67]
	v_mfma_f32_16x16x32_bf16 v[60:63], v[162:165], v[186:189], v[60:63]
	v_mfma_f32_16x16x32_bf16 v[48:51], v[154:157], v[204:207], v[48:51]
	v_mfma_f32_16x16x32_bf16 v[44:47], v[162:165], v[204:207], v[44:47]
	v_mfma_f32_16x16x32_bf16 v[32:35], v[154:157], v[212:215], v[32:35]
	v_mfma_f32_16x16x32_bf16 v[28:31], v[162:165], v[212:215], v[28:31]
	v_mfma_f32_16x16x32_bf16 v[16:19], v[154:157], v[220:223], v[16:19]
	v_mfma_f32_16x16x32_bf16 v[12:15], v[162:165], v[220:223], v[12:15]
	v_mfma_f32_16x16x32_bf16 v[64:67], v[158:161], v[190:193], v[64:67]
	v_mfma_f32_16x16x32_bf16 v[60:63], v[166:169], v[190:193], v[60:63]
	v_mfma_f32_16x16x32_bf16 v[48:51], v[158:161], v[208:211], v[48:51]
	v_mfma_f32_16x16x32_bf16 v[44:47], v[166:169], v[208:211], v[44:47]
	v_mfma_f32_16x16x32_bf16 v[32:35], v[158:161], v[216:219], v[32:35]
	v_mfma_f32_16x16x32_bf16 v[28:31], v[166:169], v[216:219], v[28:31]
	v_mfma_f32_16x16x32_bf16 v[16:19], v[158:161], v[224:227], v[16:19]
	v_mfma_f32_16x16x32_bf16 v[12:15], v[166:169], v[224:227], v[12:15]
	s_setprio 0
	s_setprio 1
	v_mfma_f32_16x16x32_bf16 v[56:59], v[170:173], v[186:189], v[56:59]
	v_mfma_f32_16x16x32_bf16 v[52:55], v[178:181], v[186:189], v[52:55]
	v_mfma_f32_16x16x32_bf16 v[40:43], v[170:173], v[204:207], v[40:43]
	v_mfma_f32_16x16x32_bf16 v[36:39], v[178:181], v[204:207], v[36:39]
	v_mfma_f32_16x16x32_bf16 v[24:27], v[170:173], v[212:215], v[24:27]
	v_mfma_f32_16x16x32_bf16 v[20:23], v[178:181], v[212:215], v[20:23]
	v_mfma_f32_16x16x32_bf16 v[8:11], v[170:173], v[220:223], v[8:11]
	v_mfma_f32_16x16x32_bf16 v[4:7], v[178:181], v[220:223], v[4:7]
	v_mfma_f32_16x16x32_bf16 v[56:59], v[174:177], v[190:193], v[56:59]
	v_mfma_f32_16x16x32_bf16 v[52:55], v[182:185], v[190:193], v[52:55]
	v_mfma_f32_16x16x32_bf16 v[40:43], v[174:177], v[208:211], v[40:43]
	v_mfma_f32_16x16x32_bf16 v[36:39], v[182:185], v[208:211], v[36:39]
	v_mfma_f32_16x16x32_bf16 v[24:27], v[174:177], v[216:219], v[24:27]
	v_mfma_f32_16x16x32_bf16 v[20:23], v[182:185], v[216:219], v[20:23]
	v_mfma_f32_16x16x32_bf16 v[8:11], v[174:177], v[224:227], v[8:11]
	v_mfma_f32_16x16x32_bf16 v[4:7], v[182:185], v[224:227], v[4:7]
	s_setprio 0
	s_barrier
	s_add_i32 s80, s80, 2
	s_add_u32 s42, s42, 0x100
	s_addc_u32 s43, s43, 0
	s_cmp_gt_u32 s80, 13

.LBB0_288:
	s_ashr_i32 s41, s40, 31
	s_lshl_b64 s[4:5], s[40:41], 19
	s_add_u32 s42, s6, s4
	s_addc_u32 s43, s7, s5
	s_and_b64 s[4:5], s[22:23], exec
	s_cselect_b32 s41, s43, s37
	s_cselect_b32 s61, s42, s36
	s_ashr_i32 s39, s38, 31
	s_lshl_b64 s[4:5], s[38:39], 19
	s_add_u32 s44, s8, s4
	s_addc_u32 s45, s9, s5
	s_and_b64 s[4:5], s[22:23], exec
	s_cselect_b32 s39, s45, s49
	s_cselect_b32 s62, s44, s48
	s_add_u32 s63, s61, 0x80
	s_addc_u32 s64, s41, 0
	s_add_u32 s4, s36, 0x40080
	s_addc_u32 s5, s37, 0
	s_add_u32 s65, s48, 0x100
	v_lshl_add_u64 v[142:143], s[4:5], 0, v[138:139]
	v_lshl_add_u64 v[144:145], s[4:5], 0, v[140:141]
	s_addc_u32 s68, s49, 0
	s_mov_b32 s69, -2
	s_mov_b64 s[48:49], 0
	s_add_u32 s4, s36, s48
	s_addc_u32 s5, s37, s49
	s_add_u32 s70, s4, 0x100
	s_addc_u32 s71, s5, 0
	s_add_u32 s50, s65, s48
	s_addc_u32 s51, s68, s49
	s_add_u32 s4, s4, 0x180
	s_addc_u32 s5, s5, 0
	s_add_i32 s72, 0, 0x10000
	s_add_i32 s73, 0, 0x14000
	v_add_u32_e32 v160, s72, v146
	s_waitcnt vmcnt(0)
	v_add_u32_e32 v176, s73, v146
	ds_read_b128 v[148:151], v160
	ds_read_b128 v[152:155], v160 offset:1024
	ds_read_b128 v[156:159], v160 offset:2048
	ds_read_b128 v[160:163], v160 offset:3072
	ds_read_b128 v[164:167], v176
	ds_read_b128 v[168:171], v176 offset:1024
	ds_read_b128 v[172:175], v176 offset:2048
	ds_read_b128 v[176:179], v176 offset:3072
	s_cmpk_eq_i32 s48, 0x700
	s_cselect_b32 s13, s64, s5
	s_cselect_b32 s12, s63, s4
	s_cselect_b32 s51, s39, s51
	s_cselect_b32 s50, s62, s50
	s_cselect_b32 s5, s41, s71
	s_cselect_b32 s4, s61, s70
	v_lshl_add_u64 v[196:197], v[142:143], 0, s[48:49]
	s_add_i32 m0, s17, 0xc000
	ds_read_b128 v[180:183], v147
	ds_read_b128 v[184:187], v147 offset:1024
	ds_read_b128 v[188:191], v147 offset:2048
	ds_read_b128 v[192:195], v147 offset:3072
	ds_read_b128 v[204:207], v147 offset:4096
	ds_read_b128 v[208:211], v147 offset:5120
	ds_read_b128 v[212:215], v147 offset:6144
	ds_read_b128 v[216:219], v147 offset:7168
	global_load_lds_dwordx4 v[196:197], off
	v_lshl_add_u64 v[196:197], v[144:145], 0, s[48:49]
	s_add_i32 m0, s17, 0xe000
	s_nop 0
	global_load_lds_dwordx4 v[196:197], off
	s_waitcnt vmcnt(8)
	s_waitcnt lgkmcnt(0)
	s_barrier
	s_setprio 1
	s_waitcnt lgkmcnt(0)
	v_mfma_f32_16x16x32_bf16 v[128:131], v[148:151], v[180:183], 0
	v_mfma_f32_16x16x32_bf16 v[124:127], v[156:159], v[180:183], 0
	v_mfma_f32_16x16x32_bf16 v[120:123], v[148:151], v[188:191], 0
	v_mfma_f32_16x16x32_bf16 v[116:119], v[156:159], v[188:191], 0
	v_mfma_f32_16x16x32_bf16 v[104:107], v[148:151], v[204:207], 0
	v_mfma_f32_16x16x32_bf16 v[100:103], v[156:159], v[204:207], 0
	v_mfma_f32_16x16x32_bf16 v[88:91], v[148:151], v[212:215], 0
	v_mfma_f32_16x16x32_bf16 v[84:87], v[156:159], v[212:215], 0
	v_mfma_f32_16x16x32_bf16 v[128:131], v[152:155], v[184:187], v[128:131]
	v_mfma_f32_16x16x32_bf16 v[124:127], v[160:163], v[184:187], v[124:127]
	v_mfma_f32_16x16x32_bf16 v[120:123], v[152:155], v[192:195], v[120:123]
	v_mfma_f32_16x16x32_bf16 v[116:119], v[160:163], v[192:195], v[116:119]
	v_mfma_f32_16x16x32_bf16 v[104:107], v[152:155], v[208:211], v[104:107]
	v_mfma_f32_16x16x32_bf16 v[100:103], v[160:163], v[208:211], v[100:103]
	v_mfma_f32_16x16x32_bf16 v[88:91], v[152:155], v[216:219], v[88:91]
	v_mfma_f32_16x16x32_bf16 v[84:87], v[160:163], v[216:219], v[84:87]
	s_setprio 0
	s_setprio 1
	v_mfma_f32_16x16x32_bf16 v[112:115], v[164:167], v[180:183], 0
	v_mfma_f32_16x16x32_bf16 v[108:111], v[172:175], v[180:183], 0
	v_mfma_f32_16x16x32_bf16 v[96:99], v[164:167], v[188:191], 0
	v_mfma_f32_16x16x32_bf16 v[92:95], v[172:175], v[188:191], 0
	v_mfma_f32_16x16x32_bf16 v[80:83], v[164:167], v[204:207], 0
	v_mfma_f32_16x16x32_bf16 v[76:79], v[172:175], v[204:207], 0
	v_mfma_f32_16x16x32_bf16 v[72:75], v[164:167], v[212:215], 0
	v_mfma_f32_16x16x32_bf16 v[68:71], v[172:175], v[212:215], 0
	v_mfma_f32_16x16x32_bf16 v[112:115], v[168:171], v[184:187], v[112:115]
	v_mfma_f32_16x16x32_bf16 v[108:111], v[176:179], v[184:187], v[108:111]
	v_mfma_f32_16x16x32_bf16 v[96:99], v[168:171], v[192:195], v[96:99]
	v_mfma_f32_16x16x32_bf16 v[92:95], v[176:179], v[192:195], v[92:95]
	v_mfma_f32_16x16x32_bf16 v[80:83], v[168:171], v[208:211], v[80:83]
	v_mfma_f32_16x16x32_bf16 v[76:79], v[176:179], v[208:211], v[76:79]
	v_mfma_f32_16x16x32_bf16 v[72:75], v[168:171], v[216:219], v[72:75]
	v_mfma_f32_16x16x32_bf16 v[68:71], v[176:179], v[216:219], v[68:71]
	s_setprio 0
	s_barrier
	s_add_i32 s70, s72, s16
	v_lshl_add_u64 v[196:197], s[50:51], 0, v[2:3]
	s_mov_b32 m0, s70
	ds_read_b128 v[180:183], v147 offset:16384
	ds_read_b128 v[184:187], v147 offset:17408
	ds_read_b128 v[188:191], v147 offset:18432
	ds_read_b128 v[192:195], v147 offset:19456
	ds_read_b128 v[204:207], v147 offset:20480
	ds_read_b128 v[208:211], v147 offset:21504
	ds_read_b128 v[212:215], v147 offset:22528
	ds_read_b128 v[216:219], v147 offset:23552
	global_load_lds_dwordx4 v[196:197], off
	s_add_i32 m0, s70, 0x2000
	s_add_u32 s70, s50, 0x40000
	v_lshl_add_u64 v[198:199], s[50:51], 0, v[136:137]
	s_addc_u32 s71, s51, 0
	s_add_i32 s72, s73, s16
	global_load_lds_dwordx4 v[198:199], off
	v_lshl_add_u64 v[220:221], s[70:71], 0, v[2:3]
	s_mov_b32 m0, s72
	s_nop 0
	global_load_lds_dwordx4 v[220:221], off
	v_lshl_add_u64 v[220:221], s[70:71], 0, v[136:137]
	s_add_i32 m0, s72, 0x2000
	s_nop 0
	global_load_lds_dwordx4 v[220:221], off
	v_lshl_add_u64 v[220:221], s[4:5], 0, v[132:133]
	s_mov_b32 m0, s17
	s_nop 0
	global_load_lds_dwordx4 v[220:221], off
	v_lshl_add_u64 v[220:221], s[4:5], 0, v[134:135]
	s_mov_b32 m0, s21
	s_nop 0
	global_load_lds_dwordx4 v[220:221], off
	s_waitcnt vmcnt(8)
	s_waitcnt lgkmcnt(0)
	s_barrier
	s_setprio 1
	s_waitcnt lgkmcnt(0)
	v_mfma_f32_16x16x32_bf16 v[64:67], v[148:151], v[180:183], 0
	v_mfma_f32_16x16x32_bf16 v[60:63], v[156:159], v[180:183], 0
	v_mfma_f32_16x16x32_bf16 v[56:59], v[148:151], v[188:191], 0
	v_mfma_f32_16x16x32_bf16 v[52:55], v[156:159], v[188:191], 0
	v_mfma_f32_16x16x32_bf16 v[40:43], v[148:151], v[204:207], 0
	v_mfma_f32_16x16x32_bf16 v[36:39], v[156:159], v[204:207], 0
	v_mfma_f32_16x16x32_bf16 v[24:27], v[148:151], v[212:215], 0
	v_mfma_f32_16x16x32_bf16 v[20:23], v[156:159], v[212:215], 0
	v_mfma_f32_16x16x32_bf16 v[64:67], v[152:155], v[184:187], v[64:67]
	v_mfma_f32_16x16x32_bf16 v[60:63], v[160:163], v[184:187], v[60:63]
	v_mfma_f32_16x16x32_bf16 v[56:59], v[152:155], v[192:195], v[56:59]
	v_mfma_f32_16x16x32_bf16 v[52:55], v[160:163], v[192:195], v[52:55]
	v_mfma_f32_16x16x32_bf16 v[40:43], v[152:155], v[208:211], v[40:43]
	v_mfma_f32_16x16x32_bf16 v[36:39], v[160:163], v[208:211], v[36:39]
	v_mfma_f32_16x16x32_bf16 v[24:27], v[152:155], v[216:219], v[24:27]
	v_mfma_f32_16x16x32_bf16 v[20:23], v[160:163], v[216:219], v[20:23]
	s_setprio 0
	s_setprio 1
	v_mfma_f32_16x16x32_bf16 v[48:51], v[164:167], v[180:183], 0
	v_mfma_f32_16x16x32_bf16 v[44:47], v[172:175], v[180:183], 0
	v_mfma_f32_16x16x32_bf16 v[32:35], v[164:167], v[188:191], 0
	v_mfma_f32_16x16x32_bf16 v[28:31], v[172:175], v[188:191], 0
	v_mfma_f32_16x16x32_bf16 v[16:19], v[164:167], v[204:207], 0
	v_mfma_f32_16x16x32_bf16 v[12:15], v[172:175], v[204:207], 0
	v_mfma_f32_16x16x32_bf16 v[8:11], v[164:167], v[212:215], 0
	v_mfma_f32_16x16x32_bf16 v[4:7], v[172:175], v[212:215], 0
	v_mfma_f32_16x16x32_bf16 v[48:51], v[168:171], v[184:187], v[48:51]
	v_mfma_f32_16x16x32_bf16 v[44:47], v[176:179], v[184:187], v[44:47]
	v_mfma_f32_16x16x32_bf16 v[32:35], v[168:171], v[192:195], v[32:35]
	v_mfma_f32_16x16x32_bf16 v[28:31], v[176:179], v[192:195], v[28:31]
	v_mfma_f32_16x16x32_bf16 v[16:19], v[168:171], v[208:211], v[16:19]
	v_mfma_f32_16x16x32_bf16 v[12:15], v[176:179], v[208:211], v[12:15]
	v_mfma_f32_16x16x32_bf16 v[8:11], v[168:171], v[216:219], v[8:11]
	v_mfma_f32_16x16x32_bf16 v[4:7], v[176:179], v[216:219], v[4:7]
	s_setprio 0
	s_barrier
	s_add_i32 s70, 0, 0x18000
	s_add_i32 s71, 0, 0x1c000
	v_add_u32_e32 v160, s70, v146
	v_add_u32_e32 v176, s71, v146
	ds_read_b128 v[148:151], v160
	ds_read_b128 v[152:155], v160 offset:1024
	ds_read_b128 v[156:159], v160 offset:2048
	ds_read_b128 v[160:163], v160 offset:3072
	ds_read_b128 v[164:167], v176
	ds_read_b128 v[168:171], v176 offset:1024
	ds_read_b128 v[172:175], v176 offset:2048
	ds_read_b128 v[176:179], v176 offset:3072
	s_add_u32 s4, s4, 0x40000
	s_addc_u32 s5, s5, 0
	s_mov_b32 m0, s46
	v_lshl_add_u64 v[220:221], s[4:5], 0, v[132:133]
	ds_read_b128 v[180:183], v147 offset:32768
	ds_read_b128 v[184:187], v147 offset:33792
	ds_read_b128 v[188:191], v147 offset:34816
	ds_read_b128 v[192:195], v147 offset:35840
	ds_read_b128 v[204:207], v147 offset:36864
	ds_read_b128 v[208:211], v147 offset:37888
	ds_read_b128 v[212:215], v147 offset:38912
	ds_read_b128 v[216:219], v147 offset:39936
	global_load_lds_dwordx4 v[220:221], off
	v_lshl_add_u64 v[220:221], s[4:5], 0, v[134:135]
	s_mov_b32 m0, s47
	s_nop 0
	global_load_lds_dwordx4 v[220:221], off
	s_waitcnt vmcnt(8)
	s_waitcnt lgkmcnt(0)
	s_barrier
	s_setprio 1
	s_waitcnt lgkmcnt(0)
	v_mfma_f32_16x16x32_bf16 v[128:131], v[148:151], v[180:183], v[128:131]
	v_mfma_f32_16x16x32_bf16 v[124:127], v[156:159], v[180:183], v[124:127]
	v_mfma_f32_16x16x32_bf16 v[120:123], v[148:151], v[188:191], v[120:123]
	v_mfma_f32_16x16x32_bf16 v[116:119], v[156:159], v[188:191], v[116:119]
	v_mfma_f32_16x16x32_bf16 v[104:107], v[148:151], v[204:207], v[104:107]
	v_mfma_f32_16x16x32_bf16 v[100:103], v[156:159], v[204:207], v[100:103]
	v_mfma_f32_16x16x32_bf16 v[88:91], v[148:151], v[212:215], v[88:91]
	v_mfma_f32_16x16x32_bf16 v[84:87], v[156:159], v[212:215], v[84:87]
	v_mfma_f32_16x16x32_bf16 v[128:131], v[152:155], v[184:187], v[128:131]
	v_mfma_f32_16x16x32_bf16 v[124:127], v[160:163], v[184:187], v[124:127]
	v_mfma_f32_16x16x32_bf16 v[120:123], v[152:155], v[192:195], v[120:123]
	v_mfma_f32_16x16x32_bf16 v[116:119], v[160:163], v[192:195], v[116:119]
	v_mfma_f32_16x16x32_bf16 v[104:107], v[152:155], v[208:211], v[104:107]
	v_mfma_f32_16x16x32_bf16 v[100:103], v[160:163], v[208:211], v[100:103]
	v_mfma_f32_16x16x32_bf16 v[88:91], v[152:155], v[216:219], v[88:91]
	v_mfma_f32_16x16x32_bf16 v[84:87], v[160:163], v[216:219], v[84:87]
	s_setprio 0
	s_setprio 1
	v_mfma_f32_16x16x32_bf16 v[112:115], v[164:167], v[180:183], v[112:115]
	v_mfma_f32_16x16x32_bf16 v[108:111], v[172:175], v[180:183], v[108:111]
	v_mfma_f32_16x16x32_bf16 v[96:99], v[164:167], v[188:191], v[96:99]
	v_mfma_f32_16x16x32_bf16 v[92:95], v[172:175], v[188:191], v[92:95]
	v_mfma_f32_16x16x32_bf16 v[80:83], v[164:167], v[204:207], v[80:83]
	v_mfma_f32_16x16x32_bf16 v[76:79], v[172:175], v[204:207], v[76:79]
	v_mfma_f32_16x16x32_bf16 v[72:75], v[164:167], v[212:215], v[72:75]
	v_mfma_f32_16x16x32_bf16 v[68:71], v[172:175], v[212:215], v[68:71]
	v_mfma_f32_16x16x32_bf16 v[112:115], v[168:171], v[184:187], v[112:115]
	v_mfma_f32_16x16x32_bf16 v[108:111], v[176:179], v[184:187], v[108:111]
	v_mfma_f32_16x16x32_bf16 v[96:99], v[168:171], v[192:195], v[96:99]
	v_mfma_f32_16x16x32_bf16 v[92:95], v[176:179], v[192:195], v[92:95]
	v_mfma_f32_16x16x32_bf16 v[80:83], v[168:171], v[208:211], v[80:83]
	v_mfma_f32_16x16x32_bf16 v[76:79], v[176:179], v[208:211], v[76:79]
	v_mfma_f32_16x16x32_bf16 v[72:75], v[168:171], v[216:219], v[72:75]
	v_mfma_f32_16x16x32_bf16 v[68:71], v[176:179], v[216:219], v[68:71]
	s_setprio 0
	s_barrier
	s_add_i32 s4, s70, s16
	v_lshl_add_u64 v[196:197], v[196:197], 0, s[34:35]
	s_mov_b32 m0, s4
	ds_read_b128 v[180:183], v147 offset:49152
	ds_read_b128 v[184:187], v147 offset:50176
	ds_read_b128 v[188:191], v147 offset:51200
	ds_read_b128 v[192:195], v147 offset:52224
	ds_read_b128 v[204:207], v147 offset:53248
	ds_read_b128 v[208:211], v147 offset:54272
	ds_read_b128 v[212:215], v147 offset:55296
	ds_read_b128 v[216:219], v147 offset:56320
	global_load_lds_dwordx4 v[196:197], off
	s_add_i32 m0, s4, 0x2000
	s_add_u32 s4, s50, 0x40080
	v_lshl_add_u64 v[196:197], v[198:199], 0, s[34:35]
	s_addc_u32 s5, s51, 0
	s_add_i32 s50, s71, s16
	global_load_lds_dwordx4 v[196:197], off
	v_lshl_add_u64 v[196:197], s[4:5], 0, v[2:3]
	s_mov_b32 m0, s50
	s_nop 0
	global_load_lds_dwordx4 v[196:197], off
	v_lshl_add_u64 v[196:197], s[4:5], 0, v[136:137]
	s_add_i32 m0, s50, 0x2000
	s_nop 0
	global_load_lds_dwordx4 v[196:197], off
	v_lshl_add_u64 v[196:197], s[12:13], 0, v[132:133]
	s_mov_b32 m0, s56
	s_nop 0
	global_load_lds_dwordx4 v[196:197], off
	v_lshl_add_u64 v[196:197], s[12:13], 0, v[134:135]
	s_mov_b32 m0, s58
	s_nop 0
	global_load_lds_dwordx4 v[196:197], off
	s_waitcnt vmcnt(8)
	s_waitcnt lgkmcnt(0)
	s_barrier
	s_setprio 1
	s_waitcnt lgkmcnt(0)
	v_mfma_f32_16x16x32_bf16 v[64:67], v[148:151], v[180:183], v[64:67]
	v_mfma_f32_16x16x32_bf16 v[60:63], v[156:159], v[180:183], v[60:63]
	v_mfma_f32_16x16x32_bf16 v[56:59], v[148:151], v[188:191], v[56:59]
	v_mfma_f32_16x16x32_bf16 v[52:55], v[156:159], v[188:191], v[52:55]
	v_mfma_f32_16x16x32_bf16 v[40:43], v[148:151], v[204:207], v[40:43]
	v_mfma_f32_16x16x32_bf16 v[36:39], v[156:159], v[204:207], v[36:39]
	v_mfma_f32_16x16x32_bf16 v[24:27], v[148:151], v[212:215], v[24:27]
	v_mfma_f32_16x16x32_bf16 v[20:23], v[156:159], v[212:215], v[20:23]
	v_mfma_f32_16x16x32_bf16 v[64:67], v[152:155], v[184:187], v[64:67]
	v_mfma_f32_16x16x32_bf16 v[60:63], v[160:163], v[184:187], v[60:63]
	v_mfma_f32_16x16x32_bf16 v[56:59], v[152:155], v[192:195], v[56:59]
	v_mfma_f32_16x16x32_bf16 v[52:55], v[160:163], v[192:195], v[52:55]
	v_mfma_f32_16x16x32_bf16 v[40:43], v[152:155], v[208:211], v[40:43]
	v_mfma_f32_16x16x32_bf16 v[36:39], v[160:163], v[208:211], v[36:39]
	v_mfma_f32_16x16x32_bf16 v[24:27], v[152:155], v[216:219], v[24:27]
	v_mfma_f32_16x16x32_bf16 v[20:23], v[160:163], v[216:219], v[20:23]
	s_setprio 0
	s_setprio 1
	v_mfma_f32_16x16x32_bf16 v[48:51], v[164:167], v[180:183], v[48:51]
	v_mfma_f32_16x16x32_bf16 v[44:47], v[172:175], v[180:183], v[44:47]
	v_mfma_f32_16x16x32_bf16 v[32:35], v[164:167], v[188:191], v[32:35]
	v_mfma_f32_16x16x32_bf16 v[28:31], v[172:175], v[188:191], v[28:31]
	v_mfma_f32_16x16x32_bf16 v[16:19], v[164:167], v[204:207], v[16:19]
	v_mfma_f32_16x16x32_bf16 v[12:15], v[172:175], v[204:207], v[12:15]
	v_mfma_f32_16x16x32_bf16 v[8:11], v[164:167], v[212:215], v[8:11]
	v_mfma_f32_16x16x32_bf16 v[4:7], v[172:175], v[212:215], v[4:7]
	v_mfma_f32_16x16x32_bf16 v[48:51], v[168:171], v[184:187], v[48:51]
	v_mfma_f32_16x16x32_bf16 v[44:47], v[176:179], v[184:187], v[44:47]
	v_mfma_f32_16x16x32_bf16 v[32:35], v[168:171], v[192:195], v[32:35]
	v_mfma_f32_16x16x32_bf16 v[28:31], v[176:179], v[192:195], v[28:31]
	v_mfma_f32_16x16x32_bf16 v[16:19], v[168:171], v[208:211], v[16:19]
	v_mfma_f32_16x16x32_bf16 v[12:15], v[176:179], v[208:211], v[12:15]
	v_mfma_f32_16x16x32_bf16 v[8:11], v[168:171], v[216:219], v[8:11]
	v_mfma_f32_16x16x32_bf16 v[4:7], v[176:179], v[216:219], v[4:7]
	s_setprio 0
	s_barrier
	s_add_i32 s69, s69, 2
	s_add_u32 s48, s48, 0x100
	s_addc_u32 s49, s49, 0
	s_cmp_gt_u32 s69, 13

.LBB0_310:
	s_ashr_i32 s41, s40, 31
	s_lshl_b64 s[4:5], s[40:41], 19
	s_add_u32 s42, s6, s4
	s_addc_u32 s43, s7, s5
	s_and_b64 s[4:5], s[22:23], exec
	s_cselect_b32 s41, s43, s39
	s_cselect_b32 s60, s42, s38
	s_ashr_i32 s37, s36, 31
	s_lshl_b64 s[4:5], s[36:37], 19
	s_add_u32 s44, s8, s4
	s_addc_u32 s45, s9, s5
	s_and_b64 s[4:5], s[22:23], exec
	s_cselect_b32 s37, s45, s49
	s_cselect_b32 s61, s44, s48
	s_add_u32 s62, s60, 0x80
	s_addc_u32 s63, s41, 0
	s_add_u32 s4, s38, 0x40080
	s_addc_u32 s5, s39, 0
	s_add_u32 s64, s48, 0x100
	v_lshl_add_u64 v[144:145], s[4:5], 0, v[140:141]
	v_lshl_add_u64 v[146:147], s[4:5], 0, v[142:143]
	s_addc_u32 s65, s49, 0
	s_mov_b32 s68, -2
	s_mov_b64 s[48:49], 0
	s_add_u32 s4, s38, s48
	s_addc_u32 s5, s39, s49
	s_add_u32 s69, s4, 0x100
	s_addc_u32 s70, s5, 0
	s_add_u32 s50, s64, s48
	s_addc_u32 s51, s65, s49
	s_add_u32 s4, s4, 0x180
	s_addc_u32 s5, s5, 0
	s_add_i32 s71, 0, 0x10000
	s_add_i32 s72, 0, 0x14000
	v_add_u32_e32 v2, s71, v149
	ds_read_b128 v[152:155], v2
	s_waitcnt vmcnt(0)
	ds_read_b128 v[156:159], v2 offset:1024
	ds_read_b128 v[160:163], v2 offset:2048
	ds_read_b128 v[164:167], v2 offset:3072
	v_add_u32_e32 v2, s72, v149
	ds_read_b128 v[168:171], v2
	ds_read_b128 v[172:175], v2 offset:1024
	ds_read_b128 v[176:179], v2 offset:2048
	ds_read_b128 v[180:183], v2 offset:3072
	s_cmpk_eq_i32 s48, 0x700
	s_cselect_b32 s13, s63, s5
	s_cselect_b32 s12, s62, s4
	s_cselect_b32 s51, s37, s51
	s_cselect_b32 s50, s61, s50
	s_cselect_b32 s5, s41, s70
	s_cselect_b32 s4, s60, s69
	v_lshl_add_u64 v[196:197], v[144:145], 0, s[48:49]
	s_add_i32 m0, s17, 0xc000
	ds_read_b128 v[184:187], v151
	ds_read_b128 v[188:191], v151 offset:1024
	ds_read_b128 v[192:195], v151 offset:2048
	ds_read_b128 v[204:207], v151 offset:3072
	ds_read_b128 v[208:211], v151 offset:4096
	ds_read_b128 v[212:215], v151 offset:5120
	ds_read_b128 v[216:219], v151 offset:6144
	ds_read_b128 v[220:223], v151 offset:7168
	global_load_lds_dwordx4 v[196:197], off
	v_lshl_add_u64 v[196:197], v[146:147], 0, s[48:49]
	s_add_i32 m0, s17, 0xe000
	s_nop 0
	global_load_lds_dwordx4 v[196:197], off
	s_waitcnt vmcnt(8)
	s_waitcnt lgkmcnt(0)
	s_barrier
	s_setprio 1
	s_waitcnt lgkmcnt(0)
	v_mfma_f32_16x16x32_bf16 v[128:131], v[152:155], v[184:187], 0
	v_mfma_f32_16x16x32_bf16 v[124:127], v[160:163], v[184:187], 0
	v_mfma_f32_16x16x32_bf16 v[120:123], v[152:155], v[192:195], 0
	v_mfma_f32_16x16x32_bf16 v[116:119], v[160:163], v[192:195], 0
	v_mfma_f32_16x16x32_bf16 v[104:107], v[152:155], v[208:211], 0
	v_mfma_f32_16x16x32_bf16 v[100:103], v[160:163], v[208:211], 0
	v_mfma_f32_16x16x32_bf16 v[88:91], v[152:155], v[216:219], 0
	v_mfma_f32_16x16x32_bf16 v[84:87], v[160:163], v[216:219], 0
	v_mfma_f32_16x16x32_bf16 v[128:131], v[156:159], v[188:191], v[128:131]
	v_mfma_f32_16x16x32_bf16 v[124:127], v[164:167], v[188:191], v[124:127]
	v_mfma_f32_16x16x32_bf16 v[120:123], v[156:159], v[204:207], v[120:123]
	v_mfma_f32_16x16x32_bf16 v[116:119], v[164:167], v[204:207], v[116:119]
	v_mfma_f32_16x16x32_bf16 v[104:107], v[156:159], v[212:215], v[104:107]
	v_mfma_f32_16x16x32_bf16 v[100:103], v[164:167], v[212:215], v[100:103]
	v_mfma_f32_16x16x32_bf16 v[88:91], v[156:159], v[220:223], v[88:91]
	v_mfma_f32_16x16x32_bf16 v[84:87], v[164:167], v[220:223], v[84:87]
	s_setprio 0
	s_setprio 1
	v_mfma_f32_16x16x32_bf16 v[112:115], v[168:171], v[184:187], 0
	v_mfma_f32_16x16x32_bf16 v[108:111], v[176:179], v[184:187], 0
	v_mfma_f32_16x16x32_bf16 v[96:99], v[168:171], v[192:195], 0
	v_mfma_f32_16x16x32_bf16 v[92:95], v[176:179], v[192:195], 0
	v_mfma_f32_16x16x32_bf16 v[80:83], v[168:171], v[208:211], 0
	v_mfma_f32_16x16x32_bf16 v[76:79], v[176:179], v[208:211], 0
	v_mfma_f32_16x16x32_bf16 v[72:75], v[168:171], v[216:219], 0
	v_mfma_f32_16x16x32_bf16 v[68:71], v[176:179], v[216:219], 0
	v_mfma_f32_16x16x32_bf16 v[112:115], v[172:175], v[188:191], v[112:115]
	v_mfma_f32_16x16x32_bf16 v[108:111], v[180:183], v[188:191], v[108:111]
	v_mfma_f32_16x16x32_bf16 v[96:99], v[172:175], v[204:207], v[96:99]
	v_mfma_f32_16x16x32_bf16 v[92:95], v[180:183], v[204:207], v[92:95]
	v_mfma_f32_16x16x32_bf16 v[80:83], v[172:175], v[212:215], v[80:83]
	v_mfma_f32_16x16x32_bf16 v[76:79], v[180:183], v[212:215], v[76:79]
	v_mfma_f32_16x16x32_bf16 v[72:75], v[172:175], v[220:223], v[72:75]
	v_mfma_f32_16x16x32_bf16 v[68:71], v[180:183], v[220:223], v[68:71]
	s_setprio 0
	s_barrier
	s_add_i32 s69, s71, s16
	v_lshl_add_u64 v[196:197], s[50:51], 0, v[134:135]
	s_mov_b32 m0, s69
	ds_read_b128 v[184:187], v151 offset:16384
	ds_read_b128 v[188:191], v151 offset:17408
	ds_read_b128 v[192:195], v151 offset:18432
	ds_read_b128 v[204:207], v151 offset:19456
	ds_read_b128 v[208:211], v151 offset:20480
	ds_read_b128 v[212:215], v151 offset:21504
	ds_read_b128 v[216:219], v151 offset:22528
	ds_read_b128 v[220:223], v151 offset:23552
	global_load_lds_dwordx4 v[196:197], off
	s_add_i32 m0, s69, 0x2000
	s_add_u32 s70, s50, 0x40000
	v_lshl_add_u64 v[198:199], s[50:51], 0, v[138:139]
	s_addc_u32 s71, s51, 0
	s_add_i32 s69, s72, s16
	global_load_lds_dwordx4 v[198:199], off
	v_lshl_add_u64 v[224:225], s[70:71], 0, v[134:135]
	s_mov_b32 m0, s69
	s_nop 0
	global_load_lds_dwordx4 v[224:225], off
	v_lshl_add_u64 v[224:225], s[70:71], 0, v[138:139]
	s_add_i32 m0, s69, 0x2000
	s_nop 0
	global_load_lds_dwordx4 v[224:225], off
	v_lshl_add_u64 v[224:225], s[4:5], 0, v[132:133]
	s_mov_b32 m0, s17
	s_nop 0
	global_load_lds_dwordx4 v[224:225], off
	v_lshl_add_u64 v[224:225], s[4:5], 0, v[136:137]
	s_mov_b32 m0, s21
	s_nop 0
	global_load_lds_dwordx4 v[224:225], off
	s_waitcnt vmcnt(8)
	s_waitcnt lgkmcnt(0)
	s_barrier
	s_setprio 1
	s_waitcnt lgkmcnt(0)
	v_mfma_f32_16x16x32_bf16 v[64:67], v[152:155], v[184:187], 0
	v_mfma_f32_16x16x32_bf16 v[60:63], v[160:163], v[184:187], 0
	v_mfma_f32_16x16x32_bf16 v[56:59], v[152:155], v[192:195], 0
	v_mfma_f32_16x16x32_bf16 v[52:55], v[160:163], v[192:195], 0
	v_mfma_f32_16x16x32_bf16 v[40:43], v[152:155], v[208:211], 0
	v_mfma_f32_16x16x32_bf16 v[36:39], v[160:163], v[208:211], 0
	v_mfma_f32_16x16x32_bf16 v[24:27], v[152:155], v[216:219], 0
	v_mfma_f32_16x16x32_bf16 v[20:23], v[160:163], v[216:219], 0
	v_mfma_f32_16x16x32_bf16 v[64:67], v[156:159], v[188:191], v[64:67]
	v_mfma_f32_16x16x32_bf16 v[60:63], v[164:167], v[188:191], v[60:63]
	v_mfma_f32_16x16x32_bf16 v[56:59], v[156:159], v[204:207], v[56:59]
	v_mfma_f32_16x16x32_bf16 v[52:55], v[164:167], v[204:207], v[52:55]
	v_mfma_f32_16x16x32_bf16 v[40:43], v[156:159], v[212:215], v[40:43]
	v_mfma_f32_16x16x32_bf16 v[36:39], v[164:167], v[212:215], v[36:39]
	v_mfma_f32_16x16x32_bf16 v[24:27], v[156:159], v[220:223], v[24:27]
	v_mfma_f32_16x16x32_bf16 v[20:23], v[164:167], v[220:223], v[20:23]
	s_setprio 0
	s_setprio 1
	v_mfma_f32_16x16x32_bf16 v[48:51], v[168:171], v[184:187], 0
	v_mfma_f32_16x16x32_bf16 v[44:47], v[176:179], v[184:187], 0
	v_mfma_f32_16x16x32_bf16 v[32:35], v[168:171], v[192:195], 0
	v_mfma_f32_16x16x32_bf16 v[28:31], v[176:179], v[192:195], 0
	v_mfma_f32_16x16x32_bf16 v[16:19], v[168:171], v[208:211], 0
	v_mfma_f32_16x16x32_bf16 v[12:15], v[176:179], v[208:211], 0
	v_mfma_f32_16x16x32_bf16 v[8:11], v[168:171], v[216:219], 0
	v_mfma_f32_16x16x32_bf16 v[4:7], v[176:179], v[216:219], 0
	v_mfma_f32_16x16x32_bf16 v[48:51], v[172:175], v[188:191], v[48:51]
	v_mfma_f32_16x16x32_bf16 v[44:47], v[180:183], v[188:191], v[44:47]
	v_mfma_f32_16x16x32_bf16 v[32:35], v[172:175], v[204:207], v[32:35]
	v_mfma_f32_16x16x32_bf16 v[28:31], v[180:183], v[204:207], v[28:31]
	v_mfma_f32_16x16x32_bf16 v[16:19], v[172:175], v[212:215], v[16:19]
	v_mfma_f32_16x16x32_bf16 v[12:15], v[180:183], v[212:215], v[12:15]
	v_mfma_f32_16x16x32_bf16 v[8:11], v[172:175], v[220:223], v[8:11]
	v_mfma_f32_16x16x32_bf16 v[4:7], v[180:183], v[220:223], v[4:7]
	s_setprio 0
	s_barrier
	s_add_i32 s69, 0, 0x18000
	v_add_u32_e32 v2, s69, v149
	s_add_i32 s70, 0, 0x1c000
	ds_read_b128 v[152:155], v2
	ds_read_b128 v[156:159], v2 offset:1024
	ds_read_b128 v[160:163], v2 offset:2048
	ds_read_b128 v[164:167], v2 offset:3072
	v_add_u32_e32 v2, s70, v149
	ds_read_b128 v[168:171], v2
	ds_read_b128 v[172:175], v2 offset:1024
	ds_read_b128 v[176:179], v2 offset:2048
	ds_read_b128 v[180:183], v2 offset:3072
	s_add_u32 s4, s4, 0x40000
	s_addc_u32 s5, s5, 0
	s_mov_b32 m0, s46
	v_lshl_add_u64 v[224:225], s[4:5], 0, v[132:133]
	ds_read_b128 v[184:187], v151 offset:32768
	ds_read_b128 v[188:191], v151 offset:33792
	ds_read_b128 v[192:195], v151 offset:34816
	ds_read_b128 v[204:207], v151 offset:35840
	ds_read_b128 v[208:211], v151 offset:36864
	ds_read_b128 v[212:215], v151 offset:37888
	ds_read_b128 v[216:219], v151 offset:38912
	ds_read_b128 v[220:223], v151 offset:39936
	global_load_lds_dwordx4 v[224:225], off
	v_lshl_add_u64 v[224:225], s[4:5], 0, v[136:137]
	s_mov_b32 m0, s47
	s_nop 0
	global_load_lds_dwordx4 v[224:225], off
	s_waitcnt vmcnt(8)
	s_waitcnt lgkmcnt(0)
	s_barrier
	s_setprio 1
	s_waitcnt lgkmcnt(0)
	v_mfma_f32_16x16x32_bf16 v[128:131], v[152:155], v[184:187], v[128:131]
	v_mfma_f32_16x16x32_bf16 v[124:127], v[160:163], v[184:187], v[124:127]
	v_mfma_f32_16x16x32_bf16 v[120:123], v[152:155], v[192:195], v[120:123]
	v_mfma_f32_16x16x32_bf16 v[116:119], v[160:163], v[192:195], v[116:119]
	v_mfma_f32_16x16x32_bf16 v[104:107], v[152:155], v[208:211], v[104:107]
	v_mfma_f32_16x16x32_bf16 v[100:103], v[160:163], v[208:211], v[100:103]
	v_mfma_f32_16x16x32_bf16 v[88:91], v[152:155], v[216:219], v[88:91]
	v_mfma_f32_16x16x32_bf16 v[84:87], v[160:163], v[216:219], v[84:87]
	v_mfma_f32_16x16x32_bf16 v[128:131], v[156:159], v[188:191], v[128:131]
	v_mfma_f32_16x16x32_bf16 v[124:127], v[164:167], v[188:191], v[124:127]
	v_mfma_f32_16x16x32_bf16 v[120:123], v[156:159], v[204:207], v[120:123]
	v_mfma_f32_16x16x32_bf16 v[116:119], v[164:167], v[204:207], v[116:119]
	v_mfma_f32_16x16x32_bf16 v[104:107], v[156:159], v[212:215], v[104:107]
	v_mfma_f32_16x16x32_bf16 v[100:103], v[164:167], v[212:215], v[100:103]
	v_mfma_f32_16x16x32_bf16 v[88:91], v[156:159], v[220:223], v[88:91]
	v_mfma_f32_16x16x32_bf16 v[84:87], v[164:167], v[220:223], v[84:87]
	s_setprio 0
	s_setprio 1
	v_mfma_f32_16x16x32_bf16 v[112:115], v[168:171], v[184:187], v[112:115]
	v_mfma_f32_16x16x32_bf16 v[108:111], v[176:179], v[184:187], v[108:111]
	v_mfma_f32_16x16x32_bf16 v[96:99], v[168:171], v[192:195], v[96:99]
	v_mfma_f32_16x16x32_bf16 v[92:95], v[176:179], v[192:195], v[92:95]
	v_mfma_f32_16x16x32_bf16 v[80:83], v[168:171], v[208:211], v[80:83]
	v_mfma_f32_16x16x32_bf16 v[76:79], v[176:179], v[208:211], v[76:79]
	v_mfma_f32_16x16x32_bf16 v[72:75], v[168:171], v[216:219], v[72:75]
	v_mfma_f32_16x16x32_bf16 v[68:71], v[176:179], v[216:219], v[68:71]
	v_mfma_f32_16x16x32_bf16 v[112:115], v[172:175], v[188:191], v[112:115]
	v_mfma_f32_16x16x32_bf16 v[108:111], v[180:183], v[188:191], v[108:111]
	v_mfma_f32_16x16x32_bf16 v[96:99], v[172:175], v[204:207], v[96:99]
	v_mfma_f32_16x16x32_bf16 v[92:95], v[180:183], v[204:207], v[92:95]
	v_mfma_f32_16x16x32_bf16 v[80:83], v[172:175], v[212:215], v[80:83]
	v_mfma_f32_16x16x32_bf16 v[76:79], v[180:183], v[212:215], v[76:79]
	v_mfma_f32_16x16x32_bf16 v[72:75], v[172:175], v[220:223], v[72:75]
	v_mfma_f32_16x16x32_bf16 v[68:71], v[180:183], v[220:223], v[68:71]
	s_setprio 0
	s_barrier
	s_add_i32 s4, s69, s16
	v_lshl_add_u64 v[196:197], v[196:197], 0, s[34:35]
	s_mov_b32 m0, s4
	ds_read_b128 v[184:187], v151 offset:49152
	ds_read_b128 v[188:191], v151 offset:50176
	ds_read_b128 v[192:195], v151 offset:51200
	ds_read_b128 v[204:207], v151 offset:52224
	ds_read_b128 v[208:211], v151 offset:53248
	ds_read_b128 v[212:215], v151 offset:54272
	ds_read_b128 v[216:219], v151 offset:55296
	ds_read_b128 v[220:223], v151 offset:56320
	global_load_lds_dwordx4 v[196:197], off
	s_add_i32 m0, s4, 0x2000
	s_add_u32 s4, s50, 0x40080
	v_lshl_add_u64 v[196:197], v[198:199], 0, s[34:35]
	s_addc_u32 s5, s51, 0
	s_add_i32 s50, s70, s16
	global_load_lds_dwordx4 v[196:197], off
	v_lshl_add_u64 v[196:197], s[4:5], 0, v[134:135]
	s_mov_b32 m0, s50
	s_nop 0
	global_load_lds_dwordx4 v[196:197], off
	v_lshl_add_u64 v[196:197], s[4:5], 0, v[138:139]
	s_add_i32 m0, s50, 0x2000
	s_nop 0
	global_load_lds_dwordx4 v[196:197], off
	v_lshl_add_u64 v[196:197], s[12:13], 0, v[132:133]
	s_mov_b32 m0, s53
	s_nop 0
	global_load_lds_dwordx4 v[196:197], off
	v_lshl_add_u64 v[196:197], s[12:13], 0, v[136:137]
	s_mov_b32 m0, s56
	s_nop 0
	global_load_lds_dwordx4 v[196:197], off
	s_waitcnt vmcnt(8)
	s_waitcnt lgkmcnt(0)
	s_barrier
	s_setprio 1
	s_waitcnt lgkmcnt(0)
	v_mfma_f32_16x16x32_bf16 v[64:67], v[152:155], v[184:187], v[64:67]
	v_mfma_f32_16x16x32_bf16 v[60:63], v[160:163], v[184:187], v[60:63]
	v_mfma_f32_16x16x32_bf16 v[56:59], v[152:155], v[192:195], v[56:59]
	v_mfma_f32_16x16x32_bf16 v[52:55], v[160:163], v[192:195], v[52:55]
	v_mfma_f32_16x16x32_bf16 v[40:43], v[152:155], v[208:211], v[40:43]
	v_mfma_f32_16x16x32_bf16 v[36:39], v[160:163], v[208:211], v[36:39]
	v_mfma_f32_16x16x32_bf16 v[24:27], v[152:155], v[216:219], v[24:27]
	v_mfma_f32_16x16x32_bf16 v[20:23], v[160:163], v[216:219], v[20:23]
	v_mfma_f32_16x16x32_bf16 v[64:67], v[156:159], v[188:191], v[64:67]
	v_mfma_f32_16x16x32_bf16 v[60:63], v[164:167], v[188:191], v[60:63]
	v_mfma_f32_16x16x32_bf16 v[56:59], v[156:159], v[204:207], v[56:59]
	v_mfma_f32_16x16x32_bf16 v[52:55], v[164:167], v[204:207], v[52:55]
	v_mfma_f32_16x16x32_bf16 v[40:43], v[156:159], v[212:215], v[40:43]
	v_mfma_f32_16x16x32_bf16 v[36:39], v[164:167], v[212:215], v[36:39]
	v_mfma_f32_16x16x32_bf16 v[24:27], v[156:159], v[220:223], v[24:27]
	v_mfma_f32_16x16x32_bf16 v[20:23], v[164:167], v[220:223], v[20:23]
	s_setprio 0
	s_setprio 1
	v_mfma_f32_16x16x32_bf16 v[48:51], v[168:171], v[184:187], v[48:51]
	v_mfma_f32_16x16x32_bf16 v[44:47], v[176:179], v[184:187], v[44:47]
	v_mfma_f32_16x16x32_bf16 v[32:35], v[168:171], v[192:195], v[32:35]
	v_mfma_f32_16x16x32_bf16 v[28:31], v[176:179], v[192:195], v[28:31]
	v_mfma_f32_16x16x32_bf16 v[16:19], v[168:171], v[208:211], v[16:19]
	v_mfma_f32_16x16x32_bf16 v[12:15], v[176:179], v[208:211], v[12:15]
	v_mfma_f32_16x16x32_bf16 v[8:11], v[168:171], v[216:219], v[8:11]
	v_mfma_f32_16x16x32_bf16 v[4:7], v[176:179], v[216:219], v[4:7]
	v_mfma_f32_16x16x32_bf16 v[48:51], v[172:175], v[188:191], v[48:51]
	v_mfma_f32_16x16x32_bf16 v[44:47], v[180:183], v[188:191], v[44:47]
	v_mfma_f32_16x16x32_bf16 v[32:35], v[172:175], v[204:207], v[32:35]
	v_mfma_f32_16x16x32_bf16 v[28:31], v[180:183], v[204:207], v[28:31]
	v_mfma_f32_16x16x32_bf16 v[16:19], v[172:175], v[212:215], v[16:19]
	v_mfma_f32_16x16x32_bf16 v[12:15], v[180:183], v[212:215], v[12:15]
	v_mfma_f32_16x16x32_bf16 v[8:11], v[172:175], v[220:223], v[8:11]
	v_mfma_f32_16x16x32_bf16 v[4:7], v[180:183], v[220:223], v[4:7]
	s_setprio 0
	s_barrier
	s_add_i32 s68, s68, 2
	s_add_u32 s48, s48, 0x100
	s_addc_u32 s49, s49, 0
	s_cmp_gt_u32 s68, 13

.LBB0_382:
	s_ashr_i32 s51, s50, 31
	s_lshl_b64 s[4:5], s[50:51], 19
	s_add_u32 s64, s8, s4
	s_addc_u32 s65, s9, s5
	s_and_b64 s[4:5], s[38:39], exec
	s_cselect_b32 s51, s65, s41
	s_cselect_b32 s71, s64, s40
	s_ashr_i32 s11, s10, 31
	s_lshl_b64 s[4:5], s[10:11], 18
	s_add_u32 s36, s16, s4
	s_addc_u32 s37, s17, s5
	s_and_b64 s[4:5], s[38:39], exec
	s_cselect_b32 s11, s37, s43
	s_cselect_b32 s74, s36, s42
	s_add_u32 s75, s71, 0x80
	s_addc_u32 s76, s51, 0
	s_add_u32 s4, s40, 0x40080
	s_addc_u32 s5, s41, 0
	s_add_u32 s77, s42, 0x100
	v_lshl_add_u64 v[100:101], s[4:5], 0, v[176:177]
	v_lshl_add_u64 v[102:103], s[4:5], 0, v[178:179]
	s_addc_u32 s78, s43, 0
	s_mov_b32 s79, -2
	s_mov_b64 s[42:43], 0
	s_add_u32 s4, s40, s42
	s_addc_u32 s5, s41, s43
	s_add_u32 s80, s4, 0x100
	s_addc_u32 s81, s5, 0
	s_add_u32 s48, s77, s42
	s_addc_u32 s49, s78, s43
	s_add_u32 s4, s4, 0x180
	s_addc_u32 s5, s5, 0
	s_add_i32 s82, 0, 0x10000
	s_add_i32 s83, 0, 0x14000
	v_add_u32_e32 v2, s82, v203
	ds_read_b128 v[104:107], v2
	ds_read_b128 v[124:127], v2 offset:1024
	ds_read_b128 v[128:131], v2 offset:2048
	ds_read_b128 v[148:151], v2 offset:3072
	v_add_u32_e32 v2, s83, v203
	ds_read_b128 v[152:155], v2
	ds_read_b128 v[156:159], v2 offset:1024
	ds_read_b128 v[160:163], v2 offset:2048
	ds_read_b128 v[164:167], v2 offset:3072
	s_cmpk_eq_i32 s42, 0x300
	s_cselect_b32 s45, s76, s5
	s_cselect_b32 s44, s75, s4
	s_cselect_b32 s49, s11, s49
	s_cselect_b32 s48, s74, s48
	s_cselect_b32 s5, s51, s81
	s_cselect_b32 s4, s71, s80
	v_lshl_add_u64 v[196:197], v[100:101], 0, s[42:43]
	s_add_i32 m0, s47, 0xc000
	ds_read_b128 v[180:183], v210
	ds_read_b128 v[184:187], v210 offset:1024
	ds_read_b128 v[188:191], v210 offset:2048
	ds_read_b128 v[192:195], v210 offset:3072
	ds_read_b128 v[204:207], v210 offset:4096
	ds_read_b128 v[212:215], v210 offset:5120
	ds_read_b128 v[216:219], v210 offset:6144
	ds_read_b128 v[220:223], v210 offset:7168
	global_load_lds_dwordx4 v[196:197], off
	v_lshl_add_u64 v[196:197], v[102:103], 0, s[42:43]
	s_add_i32 m0, s47, 0xe000
	s_nop 0
	global_load_lds_dwordx4 v[196:197], off
	s_waitcnt vmcnt(8)
	s_waitcnt lgkmcnt(0)
	s_barrier
	s_setprio 1
	s_waitcnt lgkmcnt(0)
	v_mfma_f32_16x16x32_bf16 v[144:147], v[104:107], v[180:183], 0
	v_mfma_f32_16x16x32_bf16 v[140:143], v[128:131], v[180:183], 0
	v_mfma_f32_16x16x32_bf16 v[120:123], v[104:107], v[188:191], 0
	v_mfma_f32_16x16x32_bf16 v[116:119], v[128:131], v[188:191], 0
	v_mfma_f32_16x16x32_bf16 v[96:99], v[104:107], v[204:207], 0
	v_mfma_f32_16x16x32_bf16 v[92:95], v[128:131], v[204:207], 0
	v_mfma_f32_16x16x32_bf16 v[80:83], v[104:107], v[216:219], 0
	v_mfma_f32_16x16x32_bf16 v[76:79], v[128:131], v[216:219], 0
	v_mfma_f32_16x16x32_bf16 v[144:147], v[124:127], v[184:187], v[144:147]
	v_mfma_f32_16x16x32_bf16 v[140:143], v[148:151], v[184:187], v[140:143]
	v_mfma_f32_16x16x32_bf16 v[120:123], v[124:127], v[192:195], v[120:123]
	v_mfma_f32_16x16x32_bf16 v[116:119], v[148:151], v[192:195], v[116:119]
	v_mfma_f32_16x16x32_bf16 v[96:99], v[124:127], v[212:215], v[96:99]
	v_mfma_f32_16x16x32_bf16 v[92:95], v[148:151], v[212:215], v[92:95]
	v_mfma_f32_16x16x32_bf16 v[80:83], v[124:127], v[220:223], v[80:83]
	v_mfma_f32_16x16x32_bf16 v[76:79], v[148:151], v[220:223], v[76:79]
	s_setprio 0
	s_setprio 1
	v_mfma_f32_16x16x32_bf16 v[136:139], v[152:155], v[180:183], 0
	v_mfma_f32_16x16x32_bf16 v[132:135], v[160:163], v[180:183], 0
	v_mfma_f32_16x16x32_bf16 v[112:115], v[152:155], v[188:191], 0
	v_mfma_f32_16x16x32_bf16 v[108:111], v[160:163], v[188:191], 0
	v_mfma_f32_16x16x32_bf16 v[88:91], v[152:155], v[204:207], 0
	v_mfma_f32_16x16x32_bf16 v[84:87], v[160:163], v[204:207], 0
	v_mfma_f32_16x16x32_bf16 v[72:75], v[152:155], v[216:219], 0
	v_mfma_f32_16x16x32_bf16 v[68:71], v[160:163], v[216:219], 0
	v_mfma_f32_16x16x32_bf16 v[136:139], v[156:159], v[184:187], v[136:139]
	v_mfma_f32_16x16x32_bf16 v[132:135], v[164:167], v[184:187], v[132:135]
	v_mfma_f32_16x16x32_bf16 v[112:115], v[156:159], v[192:195], v[112:115]
	v_mfma_f32_16x16x32_bf16 v[108:111], v[164:167], v[192:195], v[108:111]
	v_mfma_f32_16x16x32_bf16 v[88:91], v[156:159], v[212:215], v[88:91]
	v_mfma_f32_16x16x32_bf16 v[84:87], v[164:167], v[212:215], v[84:87]
	v_mfma_f32_16x16x32_bf16 v[72:75], v[156:159], v[220:223], v[72:75]
	v_mfma_f32_16x16x32_bf16 v[68:71], v[164:167], v[220:223], v[68:71]
	s_setprio 0
	s_barrier
	s_add_i32 s80, s82, s46
	v_lshl_add_u64 v[196:197], s[48:49], 0, v[172:173]
	s_mov_b32 m0, s80
	ds_read_b128 v[180:183], v210 offset:16384
	ds_read_b128 v[184:187], v210 offset:17408
	ds_read_b128 v[188:191], v210 offset:18432
	ds_read_b128 v[192:195], v210 offset:19456
	ds_read_b128 v[204:207], v210 offset:20480
	ds_read_b128 v[212:215], v210 offset:21504
	ds_read_b128 v[216:219], v210 offset:22528
	ds_read_b128 v[220:223], v210 offset:23552
	global_load_lds_dwordx4 v[196:197], off
	s_add_i32 m0, s80, 0x2000
	s_add_u32 s80, s48, 0x20000
	v_lshl_add_u64 v[198:199], s[48:49], 0, v[168:169]
	s_addc_u32 s81, s49, 0
	s_add_i32 s82, s83, s46
	global_load_lds_dwordx4 v[198:199], off
	v_lshl_add_u64 v[208:209], s[80:81], 0, v[172:173]
	s_mov_b32 m0, s82
	s_nop 0
	global_load_lds_dwordx4 v[208:209], off
	v_lshl_add_u64 v[208:209], s[80:81], 0, v[168:169]
	s_add_i32 m0, s82, 0x2000
	s_nop 0
	global_load_lds_dwordx4 v[208:209], off
	v_lshl_add_u64 v[208:209], s[4:5], 0, v[174:175]
	s_mov_b32 m0, s47
	s_nop 0
	global_load_lds_dwordx4 v[208:209], off
	v_lshl_add_u64 v[208:209], s[4:5], 0, v[170:171]
	s_mov_b32 m0, s56
	s_nop 0
	global_load_lds_dwordx4 v[208:209], off
	s_waitcnt vmcnt(8)
	s_waitcnt lgkmcnt(0)
	s_barrier
	s_setprio 1
	s_waitcnt lgkmcnt(0)
	v_mfma_f32_16x16x32_bf16 v[64:67], v[104:107], v[180:183], 0
	v_mfma_f32_16x16x32_bf16 v[60:63], v[128:131], v[180:183], 0
	v_mfma_f32_16x16x32_bf16 v[48:51], v[104:107], v[188:191], 0
	v_mfma_f32_16x16x32_bf16 v[44:47], v[128:131], v[188:191], 0
	v_mfma_f32_16x16x32_bf16 v[32:35], v[104:107], v[204:207], 0
	v_mfma_f32_16x16x32_bf16 v[28:31], v[128:131], v[204:207], 0
	v_mfma_f32_16x16x32_bf16 v[16:19], v[104:107], v[216:219], 0
	v_mfma_f32_16x16x32_bf16 v[12:15], v[128:131], v[216:219], 0
	v_mfma_f32_16x16x32_bf16 v[64:67], v[124:127], v[184:187], v[64:67]
	v_mfma_f32_16x16x32_bf16 v[60:63], v[148:151], v[184:187], v[60:63]
	v_mfma_f32_16x16x32_bf16 v[48:51], v[124:127], v[192:195], v[48:51]
	v_mfma_f32_16x16x32_bf16 v[44:47], v[148:151], v[192:195], v[44:47]
	v_mfma_f32_16x16x32_bf16 v[32:35], v[124:127], v[212:215], v[32:35]
	v_mfma_f32_16x16x32_bf16 v[28:31], v[148:151], v[212:215], v[28:31]
	v_mfma_f32_16x16x32_bf16 v[16:19], v[124:127], v[220:223], v[16:19]
	v_mfma_f32_16x16x32_bf16 v[12:15], v[148:151], v[220:223], v[12:15]
	s_setprio 0
	s_setprio 1
	v_mfma_f32_16x16x32_bf16 v[56:59], v[152:155], v[180:183], 0
	v_mfma_f32_16x16x32_bf16 v[52:55], v[160:163], v[180:183], 0
	v_mfma_f32_16x16x32_bf16 v[40:43], v[152:155], v[188:191], 0
	v_mfma_f32_16x16x32_bf16 v[36:39], v[160:163], v[188:191], 0
	v_mfma_f32_16x16x32_bf16 v[24:27], v[152:155], v[204:207], 0
	v_mfma_f32_16x16x32_bf16 v[20:23], v[160:163], v[204:207], 0
	v_mfma_f32_16x16x32_bf16 v[8:11], v[152:155], v[216:219], 0
	v_mfma_f32_16x16x32_bf16 v[4:7], v[160:163], v[216:219], 0
	v_mfma_f32_16x16x32_bf16 v[56:59], v[156:159], v[184:187], v[56:59]
	v_mfma_f32_16x16x32_bf16 v[52:55], v[164:167], v[184:187], v[52:55]
	v_mfma_f32_16x16x32_bf16 v[40:43], v[156:159], v[192:195], v[40:43]
	v_mfma_f32_16x16x32_bf16 v[36:39], v[164:167], v[192:195], v[36:39]
	v_mfma_f32_16x16x32_bf16 v[24:27], v[156:159], v[212:215], v[24:27]
	v_mfma_f32_16x16x32_bf16 v[20:23], v[164:167], v[212:215], v[20:23]
	v_mfma_f32_16x16x32_bf16 v[8:11], v[156:159], v[220:223], v[8:11]
	v_mfma_f32_16x16x32_bf16 v[4:7], v[164:167], v[220:223], v[4:7]
	s_setprio 0
	s_barrier
	s_add_i32 s80, 0, 0x18000
	v_add_u32_e32 v2, s80, v203
	s_add_i32 s81, 0, 0x1c000
	ds_read_b128 v[104:107], v2
	ds_read_b128 v[124:127], v2 offset:1024
	ds_read_b128 v[128:131], v2 offset:2048
	ds_read_b128 v[148:151], v2 offset:3072
	v_add_u32_e32 v2, s81, v203
	ds_read_b128 v[152:155], v2
	ds_read_b128 v[156:159], v2 offset:1024
	ds_read_b128 v[160:163], v2 offset:2048
	ds_read_b128 v[164:167], v2 offset:3072
	s_add_u32 s4, s4, 0x40000
	s_addc_u32 s5, s5, 0
	s_mov_b32 m0, s58
	v_lshl_add_u64 v[208:209], s[4:5], 0, v[174:175]
	ds_read_b128 v[180:183], v210 offset:32768
	ds_read_b128 v[184:187], v210 offset:33792
	ds_read_b128 v[188:191], v210 offset:34816
	ds_read_b128 v[192:195], v210 offset:35840
	ds_read_b128 v[204:207], v210 offset:36864
	ds_read_b128 v[212:215], v210 offset:37888
	ds_read_b128 v[216:219], v210 offset:38912
	ds_read_b128 v[220:223], v210 offset:39936
	global_load_lds_dwordx4 v[208:209], off
	v_lshl_add_u64 v[208:209], s[4:5], 0, v[170:171]
	s_mov_b32 m0, s59
	s_nop 0
	global_load_lds_dwordx4 v[208:209], off
	s_waitcnt vmcnt(8)
	s_waitcnt lgkmcnt(0)
	s_barrier
	s_setprio 1
	s_waitcnt lgkmcnt(0)
	v_mfma_f32_16x16x32_bf16 v[144:147], v[104:107], v[180:183], v[144:147]
	v_mfma_f32_16x16x32_bf16 v[140:143], v[128:131], v[180:183], v[140:143]
	v_mfma_f32_16x16x32_bf16 v[120:123], v[104:107], v[188:191], v[120:123]
	v_mfma_f32_16x16x32_bf16 v[116:119], v[128:131], v[188:191], v[116:119]
	v_mfma_f32_16x16x32_bf16 v[96:99], v[104:107], v[204:207], v[96:99]
	v_mfma_f32_16x16x32_bf16 v[92:95], v[128:131], v[204:207], v[92:95]
	v_mfma_f32_16x16x32_bf16 v[80:83], v[104:107], v[216:219], v[80:83]
	v_mfma_f32_16x16x32_bf16 v[76:79], v[128:131], v[216:219], v[76:79]
	v_mfma_f32_16x16x32_bf16 v[144:147], v[124:127], v[184:187], v[144:147]
	v_mfma_f32_16x16x32_bf16 v[140:143], v[148:151], v[184:187], v[140:143]
	v_mfma_f32_16x16x32_bf16 v[120:123], v[124:127], v[192:195], v[120:123]
	v_mfma_f32_16x16x32_bf16 v[116:119], v[148:151], v[192:195], v[116:119]
	v_mfma_f32_16x16x32_bf16 v[96:99], v[124:127], v[212:215], v[96:99]
	v_mfma_f32_16x16x32_bf16 v[92:95], v[148:151], v[212:215], v[92:95]
	v_mfma_f32_16x16x32_bf16 v[80:83], v[124:127], v[220:223], v[80:83]
	v_mfma_f32_16x16x32_bf16 v[76:79], v[148:151], v[220:223], v[76:79]
	s_setprio 0
	s_setprio 1
	v_mfma_f32_16x16x32_bf16 v[136:139], v[152:155], v[180:183], v[136:139]
	v_mfma_f32_16x16x32_bf16 v[132:135], v[160:163], v[180:183], v[132:135]
	v_mfma_f32_16x16x32_bf16 v[112:115], v[152:155], v[188:191], v[112:115]
	v_mfma_f32_16x16x32_bf16 v[108:111], v[160:163], v[188:191], v[108:111]
	v_mfma_f32_16x16x32_bf16 v[88:91], v[152:155], v[204:207], v[88:91]
	v_mfma_f32_16x16x32_bf16 v[84:87], v[160:163], v[204:207], v[84:87]
	v_mfma_f32_16x16x32_bf16 v[72:75], v[152:155], v[216:219], v[72:75]
	v_mfma_f32_16x16x32_bf16 v[68:71], v[160:163], v[216:219], v[68:71]
	v_mfma_f32_16x16x32_bf16 v[136:139], v[156:159], v[184:187], v[136:139]
	v_mfma_f32_16x16x32_bf16 v[132:135], v[164:167], v[184:187], v[132:135]
	v_mfma_f32_16x16x32_bf16 v[112:115], v[156:159], v[192:195], v[112:115]
	v_mfma_f32_16x16x32_bf16 v[108:111], v[164:167], v[192:195], v[108:111]
	v_mfma_f32_16x16x32_bf16 v[88:91], v[156:159], v[212:215], v[88:91]
	v_mfma_f32_16x16x32_bf16 v[84:87], v[164:167], v[212:215], v[84:87]
	v_mfma_f32_16x16x32_bf16 v[72:75], v[156:159], v[220:223], v[72:75]
	v_mfma_f32_16x16x32_bf16 v[68:71], v[164:167], v[220:223], v[68:71]
	s_setprio 0
	s_barrier
	s_add_i32 s4, s80, s46
	v_lshl_add_u64 v[196:197], v[196:197], 0, s[34:35]
	s_mov_b32 m0, s4
	ds_read_b128 v[180:183], v210 offset:49152
	ds_read_b128 v[184:187], v210 offset:50176
	ds_read_b128 v[188:191], v210 offset:51200
	ds_read_b128 v[192:195], v210 offset:52224
	ds_read_b128 v[204:207], v210 offset:53248
	ds_read_b128 v[212:215], v210 offset:54272
	ds_read_b128 v[216:219], v210 offset:55296
	ds_read_b128 v[220:223], v210 offset:56320
	global_load_lds_dwordx4 v[196:197], off
	s_add_i32 m0, s4, 0x2000
	s_add_u32 s4, s48, 0x20080
	v_lshl_add_u64 v[196:197], v[198:199], 0, s[34:35]
	s_addc_u32 s5, s49, 0
	s_add_i32 s48, s81, s46
	global_load_lds_dwordx4 v[196:197], off
	v_lshl_add_u64 v[196:197], s[4:5], 0, v[172:173]
	s_mov_b32 m0, s48
	s_nop 0
	global_load_lds_dwordx4 v[196:197], off
	v_lshl_add_u64 v[196:197], s[4:5], 0, v[168:169]
	s_add_i32 m0, s48, 0x2000
	s_nop 0
	global_load_lds_dwordx4 v[196:197], off
	v_lshl_add_u64 v[196:197], s[44:45], 0, v[174:175]
	s_mov_b32 m0, s68
	s_nop 0
	global_load_lds_dwordx4 v[196:197], off
	v_lshl_add_u64 v[196:197], s[44:45], 0, v[170:171]
	s_mov_b32 m0, s69
	s_nop 0
	global_load_lds_dwordx4 v[196:197], off
	s_waitcnt vmcnt(8)
	s_waitcnt lgkmcnt(0)
	s_barrier
	s_setprio 1
	s_waitcnt lgkmcnt(0)
	v_mfma_f32_16x16x32_bf16 v[64:67], v[104:107], v[180:183], v[64:67]
	v_mfma_f32_16x16x32_bf16 v[60:63], v[128:131], v[180:183], v[60:63]
	v_mfma_f32_16x16x32_bf16 v[48:51], v[104:107], v[188:191], v[48:51]
	v_mfma_f32_16x16x32_bf16 v[44:47], v[128:131], v[188:191], v[44:47]
	v_mfma_f32_16x16x32_bf16 v[32:35], v[104:107], v[204:207], v[32:35]
	v_mfma_f32_16x16x32_bf16 v[28:31], v[128:131], v[204:207], v[28:31]
	v_mfma_f32_16x16x32_bf16 v[16:19], v[104:107], v[216:219], v[16:19]
	v_mfma_f32_16x16x32_bf16 v[12:15], v[128:131], v[216:219], v[12:15]
	v_mfma_f32_16x16x32_bf16 v[64:67], v[124:127], v[184:187], v[64:67]
	v_mfma_f32_16x16x32_bf16 v[60:63], v[148:151], v[184:187], v[60:63]
	v_mfma_f32_16x16x32_bf16 v[48:51], v[124:127], v[192:195], v[48:51]
	v_mfma_f32_16x16x32_bf16 v[44:47], v[148:151], v[192:195], v[44:47]
	v_mfma_f32_16x16x32_bf16 v[32:35], v[124:127], v[212:215], v[32:35]
	v_mfma_f32_16x16x32_bf16 v[28:31], v[148:151], v[212:215], v[28:31]
	v_mfma_f32_16x16x32_bf16 v[16:19], v[124:127], v[220:223], v[16:19]
	v_mfma_f32_16x16x32_bf16 v[12:15], v[148:151], v[220:223], v[12:15]
	s_setprio 0
	s_setprio 1
	v_mfma_f32_16x16x32_bf16 v[56:59], v[152:155], v[180:183], v[56:59]
	v_mfma_f32_16x16x32_bf16 v[52:55], v[160:163], v[180:183], v[52:55]
	v_mfma_f32_16x16x32_bf16 v[40:43], v[152:155], v[188:191], v[40:43]
	v_mfma_f32_16x16x32_bf16 v[36:39], v[160:163], v[188:191], v[36:39]
	v_mfma_f32_16x16x32_bf16 v[24:27], v[152:155], v[204:207], v[24:27]
	v_mfma_f32_16x16x32_bf16 v[20:23], v[160:163], v[204:207], v[20:23]
	v_mfma_f32_16x16x32_bf16 v[8:11], v[152:155], v[216:219], v[8:11]
	v_mfma_f32_16x16x32_bf16 v[4:7], v[160:163], v[216:219], v[4:7]
	v_mfma_f32_16x16x32_bf16 v[56:59], v[156:159], v[184:187], v[56:59]
	v_mfma_f32_16x16x32_bf16 v[52:55], v[164:167], v[184:187], v[52:55]
	v_mfma_f32_16x16x32_bf16 v[40:43], v[156:159], v[192:195], v[40:43]
	v_mfma_f32_16x16x32_bf16 v[36:39], v[164:167], v[192:195], v[36:39]
	v_mfma_f32_16x16x32_bf16 v[24:27], v[156:159], v[212:215], v[24:27]
	v_mfma_f32_16x16x32_bf16 v[20:23], v[164:167], v[212:215], v[20:23]
	v_mfma_f32_16x16x32_bf16 v[8:11], v[156:159], v[220:223], v[8:11]
	v_mfma_f32_16x16x32_bf16 v[4:7], v[164:167], v[220:223], v[4:7]
	s_setprio 0
	s_barrier
	s_add_i32 s79, s79, 2
	s_add_u32 s42, s42, 0x100
	s_addc_u32 s43, s43, 0
	s_cmp_gt_u32 s79, 5

.LBB0_1043:
	s_ashr_i32 s41, s40, 31
	s_lshl_b64 s[4:5], s[40:41], 19
	s_add_u32 s42, s6, s4
	s_addc_u32 s43, s7, s5
	s_and_b64 s[4:5], s[38:39], exec
	s_cselect_b32 s41, s43, s49
	s_cselect_b32 s65, s42, s48
	s_ashr_i32 s37, s36, 31
	s_lshl_b64 s[4:5], s[36:37], 19
	s_add_u32 s44, s8, s4
	s_addc_u32 s45, s9, s5
	s_and_b64 s[4:5], s[38:39], exec
	s_cselect_b32 s37, s45, s51
	s_cselect_b32 s68, s44, s50
	s_add_u32 s69, s65, 0x80
	s_addc_u32 s70, s41, 0
	s_add_u32 s4, s48, 0x40080
	s_addc_u32 s5, s49, 0
	s_add_u32 s71, s50, 0x100
	v_lshl_add_u64 v[140:141], s[4:5], 0, v[136:137]
	v_lshl_add_u64 v[142:143], s[4:5], 0, v[138:139]
	s_addc_u32 s72, s51, 0
	s_mov_b32 s73, -2
	s_mov_b64 s[50:51], 0
	s_waitcnt vmcnt(0)
	s_add_u32 s4, s48, s50
	s_addc_u32 s5, s49, s51
	s_add_u32 s74, s4, 0x100
	s_addc_u32 s75, s5, 0
	s_add_u32 s52, s71, s50
	s_addc_u32 s53, s72, s51
	s_add_u32 s4, s4, 0x180
	s_addc_u32 s5, s5, 0
	s_add_i32 s76, 0, 0x10000
	s_add_i32 s77, 0, 0x14000
	v_add_u32_e32 v2, s76, v203
	ds_read_b128 v[144:147], v2
	ds_read_b128 v[148:151], v2 offset:1024
	ds_read_b128 v[152:155], v2 offset:2048
	ds_read_b128 v[156:159], v2 offset:3072
	v_add_u32_e32 v2, s77, v203
	ds_read_b128 v[160:163], v2
	ds_read_b128 v[164:167], v2 offset:1024
	ds_read_b128 v[168:171], v2 offset:2048
	ds_read_b128 v[172:175], v2 offset:3072
	s_cmpk_eq_i32 s50, 0x700
	s_cselect_b32 s13, s70, s5
	s_cselect_b32 s12, s69, s4
	s_cselect_b32 s53, s37, s53
	s_cselect_b32 s52, s68, s52
	s_cselect_b32 s5, s41, s75
	s_cselect_b32 s4, s65, s74
	v_lshl_add_u64 v[212:213], v[140:141], 0, s[50:51]
	s_add_i32 m0, s17, 0xc000
	ds_read_b128 v[176:179], v224
	ds_read_b128 v[180:183], v224 offset:1024
	ds_read_b128 v[184:187], v224 offset:2048
	ds_read_b128 v[188:191], v224 offset:3072
	ds_read_b128 v[192:195], v224 offset:4096
	ds_read_b128 v[196:199], v224 offset:5120
	ds_read_b128 v[204:207], v224 offset:6144
	ds_read_b128 v[208:211], v224 offset:7168
	global_load_lds_dwordx4 v[212:213], off
	v_lshl_add_u64 v[212:213], v[142:143], 0, s[50:51]
	s_add_i32 m0, s17, 0xe000
	s_nop 0
	global_load_lds_dwordx4 v[212:213], off
	s_waitcnt vmcnt(8)
	s_waitcnt lgkmcnt(0)
	s_barrier
	s_setprio 1
	s_waitcnt lgkmcnt(0)
	v_mfma_f32_16x16x32_bf16 v[128:131], v[144:147], v[176:179], 0
	v_mfma_f32_16x16x32_bf16 v[124:127], v[152:155], v[176:179], 0
	v_mfma_f32_16x16x32_bf16 v[112:115], v[144:147], v[184:187], 0
	v_mfma_f32_16x16x32_bf16 v[108:111], v[152:155], v[184:187], 0
	v_mfma_f32_16x16x32_bf16 v[96:99], v[144:147], v[192:195], 0
	v_mfma_f32_16x16x32_bf16 v[92:95], v[152:155], v[192:195], 0
	v_mfma_f32_16x16x32_bf16 v[80:83], v[144:147], v[204:207], 0
	v_mfma_f32_16x16x32_bf16 v[76:79], v[152:155], v[204:207], 0
	v_mfma_f32_16x16x32_bf16 v[128:131], v[148:151], v[180:183], v[128:131]
	v_mfma_f32_16x16x32_bf16 v[124:127], v[156:159], v[180:183], v[124:127]
	v_mfma_f32_16x16x32_bf16 v[112:115], v[148:151], v[188:191], v[112:115]
	v_mfma_f32_16x16x32_bf16 v[108:111], v[156:159], v[188:191], v[108:111]
	v_mfma_f32_16x16x32_bf16 v[96:99], v[148:151], v[196:199], v[96:99]
	v_mfma_f32_16x16x32_bf16 v[92:95], v[156:159], v[196:199], v[92:95]
	v_mfma_f32_16x16x32_bf16 v[80:83], v[148:151], v[208:211], v[80:83]
	v_mfma_f32_16x16x32_bf16 v[76:79], v[156:159], v[208:211], v[76:79]
	s_setprio 0
	s_setprio 1
	v_mfma_f32_16x16x32_bf16 v[120:123], v[160:163], v[176:179], 0
	v_mfma_f32_16x16x32_bf16 v[116:119], v[168:171], v[176:179], 0
	v_mfma_f32_16x16x32_bf16 v[104:107], v[160:163], v[184:187], 0
	v_mfma_f32_16x16x32_bf16 v[100:103], v[168:171], v[184:187], 0
	v_mfma_f32_16x16x32_bf16 v[88:91], v[160:163], v[192:195], 0
	v_mfma_f32_16x16x32_bf16 v[84:87], v[168:171], v[192:195], 0
	v_mfma_f32_16x16x32_bf16 v[72:75], v[160:163], v[204:207], 0
	v_mfma_f32_16x16x32_bf16 v[68:71], v[168:171], v[204:207], 0
	v_mfma_f32_16x16x32_bf16 v[120:123], v[164:167], v[180:183], v[120:123]
	v_mfma_f32_16x16x32_bf16 v[116:119], v[172:175], v[180:183], v[116:119]
	v_mfma_f32_16x16x32_bf16 v[104:107], v[164:167], v[188:191], v[104:107]
	v_mfma_f32_16x16x32_bf16 v[100:103], v[172:175], v[188:191], v[100:103]
	v_mfma_f32_16x16x32_bf16 v[88:91], v[164:167], v[196:199], v[88:91]
	v_mfma_f32_16x16x32_bf16 v[84:87], v[172:175], v[196:199], v[84:87]
	v_mfma_f32_16x16x32_bf16 v[72:75], v[164:167], v[208:211], v[72:75]
	v_mfma_f32_16x16x32_bf16 v[68:71], v[172:175], v[208:211], v[68:71]
	s_setprio 0
	s_barrier
	s_add_i32 s74, s76, s16
	v_lshl_add_u64 v[212:213], s[52:53], 0, v[134:135]
	s_mov_b32 m0, s74
	ds_read_b128 v[176:179], v224 offset:16384
	ds_read_b128 v[180:183], v224 offset:17408
	ds_read_b128 v[184:187], v224 offset:18432
	ds_read_b128 v[188:191], v224 offset:19456
	ds_read_b128 v[192:195], v224 offset:20480
	ds_read_b128 v[196:199], v224 offset:21504
	ds_read_b128 v[204:207], v224 offset:22528
	ds_read_b128 v[208:211], v224 offset:23552
	global_load_lds_dwordx4 v[212:213], off
	s_add_i32 m0, s74, 0x2000
	s_add_u32 s74, s52, 0x40000
	v_lshl_add_u64 v[214:215], s[52:53], 0, v[132:133]
	s_addc_u32 s75, s53, 0
	s_add_i32 s76, s77, s16
	global_load_lds_dwordx4 v[214:215], off
	v_lshl_add_u64 v[216:217], s[74:75], 0, v[134:135]
	s_mov_b32 m0, s76
	s_nop 0
	global_load_lds_dwordx4 v[216:217], off
	v_lshl_add_u64 v[216:217], s[74:75], 0, v[132:133]
	s_add_i32 m0, s76, 0x2000
	s_nop 0
	global_load_lds_dwordx4 v[216:217], off
	v_lshl_add_u64 v[216:217], s[4:5], 0, v[134:135]
	s_mov_b32 m0, s17
	s_nop 0
	global_load_lds_dwordx4 v[216:217], off
	v_lshl_add_u64 v[216:217], s[4:5], 0, v[132:133]
	s_mov_b32 m0, s46
	s_nop 0
	global_load_lds_dwordx4 v[216:217], off
	s_waitcnt vmcnt(8)
	s_waitcnt lgkmcnt(0)
	s_barrier
	s_setprio 1
	s_waitcnt lgkmcnt(0)
	v_mfma_f32_16x16x32_bf16 v[64:67], v[144:147], v[176:179], 0
	v_mfma_f32_16x16x32_bf16 v[60:63], v[152:155], v[176:179], 0
	v_mfma_f32_16x16x32_bf16 v[48:51], v[144:147], v[184:187], 0
	v_mfma_f32_16x16x32_bf16 v[44:47], v[152:155], v[184:187], 0
	v_mfma_f32_16x16x32_bf16 v[32:35], v[144:147], v[192:195], 0
	v_mfma_f32_16x16x32_bf16 v[28:31], v[152:155], v[192:195], 0
	v_mfma_f32_16x16x32_bf16 v[16:19], v[144:147], v[204:207], 0
	v_mfma_f32_16x16x32_bf16 v[12:15], v[152:155], v[204:207], 0
	v_mfma_f32_16x16x32_bf16 v[64:67], v[148:151], v[180:183], v[64:67]
	v_mfma_f32_16x16x32_bf16 v[60:63], v[156:159], v[180:183], v[60:63]
	v_mfma_f32_16x16x32_bf16 v[48:51], v[148:151], v[188:191], v[48:51]
	v_mfma_f32_16x16x32_bf16 v[44:47], v[156:159], v[188:191], v[44:47]
	v_mfma_f32_16x16x32_bf16 v[32:35], v[148:151], v[196:199], v[32:35]
	v_mfma_f32_16x16x32_bf16 v[28:31], v[156:159], v[196:199], v[28:31]
	v_mfma_f32_16x16x32_bf16 v[16:19], v[148:151], v[208:211], v[16:19]
	v_mfma_f32_16x16x32_bf16 v[12:15], v[156:159], v[208:211], v[12:15]
	s_setprio 0
	s_setprio 1
	v_mfma_f32_16x16x32_bf16 v[56:59], v[160:163], v[176:179], 0
	v_mfma_f32_16x16x32_bf16 v[52:55], v[168:171], v[176:179], 0
	v_mfma_f32_16x16x32_bf16 v[40:43], v[160:163], v[184:187], 0
	v_mfma_f32_16x16x32_bf16 v[36:39], v[168:171], v[184:187], 0
	v_mfma_f32_16x16x32_bf16 v[24:27], v[160:163], v[192:195], 0
	v_mfma_f32_16x16x32_bf16 v[20:23], v[168:171], v[192:195], 0
	v_mfma_f32_16x16x32_bf16 v[8:11], v[160:163], v[204:207], 0
	v_mfma_f32_16x16x32_bf16 v[4:7], v[168:171], v[204:207], 0
	v_mfma_f32_16x16x32_bf16 v[56:59], v[164:167], v[180:183], v[56:59]
	v_mfma_f32_16x16x32_bf16 v[52:55], v[172:175], v[180:183], v[52:55]
	v_mfma_f32_16x16x32_bf16 v[40:43], v[164:167], v[188:191], v[40:43]
	v_mfma_f32_16x16x32_bf16 v[36:39], v[172:175], v[188:191], v[36:39]
	v_mfma_f32_16x16x32_bf16 v[24:27], v[164:167], v[196:199], v[24:27]
	v_mfma_f32_16x16x32_bf16 v[20:23], v[172:175], v[196:199], v[20:23]
	v_mfma_f32_16x16x32_bf16 v[8:11], v[164:167], v[208:211], v[8:11]
	v_mfma_f32_16x16x32_bf16 v[4:7], v[172:175], v[208:211], v[4:7]
	s_setprio 0
	s_barrier
	s_add_i32 s74, 0, 0x18000
	v_add_u32_e32 v2, s74, v203
	s_add_i32 s75, 0, 0x1c000
	ds_read_b128 v[144:147], v2
	ds_read_b128 v[148:151], v2 offset:1024
	ds_read_b128 v[152:155], v2 offset:2048
	ds_read_b128 v[156:159], v2 offset:3072
	v_add_u32_e32 v2, s75, v203
	ds_read_b128 v[160:163], v2
	ds_read_b128 v[164:167], v2 offset:1024
	ds_read_b128 v[168:171], v2 offset:2048
	ds_read_b128 v[172:175], v2 offset:3072
	s_add_u32 s4, s4, 0x40000
	s_addc_u32 s5, s5, 0
	s_mov_b32 m0, s47
	v_lshl_add_u64 v[216:217], s[4:5], 0, v[134:135]
	ds_read_b128 v[176:179], v224 offset:32768
	ds_read_b128 v[180:183], v224 offset:33792
	ds_read_b128 v[184:187], v224 offset:34816
	ds_read_b128 v[188:191], v224 offset:35840
	ds_read_b128 v[192:195], v224 offset:36864
	ds_read_b128 v[196:199], v224 offset:37888
	ds_read_b128 v[204:207], v224 offset:38912
	ds_read_b128 v[208:211], v224 offset:39936
	global_load_lds_dwordx4 v[216:217], off
	v_lshl_add_u64 v[216:217], s[4:5], 0, v[132:133]
	s_mov_b32 m0, s56
	s_nop 0
	global_load_lds_dwordx4 v[216:217], off
	s_waitcnt vmcnt(8)
	s_waitcnt lgkmcnt(0)
	s_barrier
	s_setprio 1
	s_waitcnt lgkmcnt(0)
	v_mfma_f32_16x16x32_bf16 v[128:131], v[144:147], v[176:179], v[128:131]
	v_mfma_f32_16x16x32_bf16 v[124:127], v[152:155], v[176:179], v[124:127]
	v_mfma_f32_16x16x32_bf16 v[112:115], v[144:147], v[184:187], v[112:115]
	v_mfma_f32_16x16x32_bf16 v[108:111], v[152:155], v[184:187], v[108:111]
	v_mfma_f32_16x16x32_bf16 v[96:99], v[144:147], v[192:195], v[96:99]
	v_mfma_f32_16x16x32_bf16 v[92:95], v[152:155], v[192:195], v[92:95]
	v_mfma_f32_16x16x32_bf16 v[80:83], v[144:147], v[204:207], v[80:83]
	v_mfma_f32_16x16x32_bf16 v[76:79], v[152:155], v[204:207], v[76:79]
	v_mfma_f32_16x16x32_bf16 v[128:131], v[148:151], v[180:183], v[128:131]
	v_mfma_f32_16x16x32_bf16 v[124:127], v[156:159], v[180:183], v[124:127]
	v_mfma_f32_16x16x32_bf16 v[112:115], v[148:151], v[188:191], v[112:115]
	v_mfma_f32_16x16x32_bf16 v[108:111], v[156:159], v[188:191], v[108:111]
	v_mfma_f32_16x16x32_bf16 v[96:99], v[148:151], v[196:199], v[96:99]
	v_mfma_f32_16x16x32_bf16 v[92:95], v[156:159], v[196:199], v[92:95]
	v_mfma_f32_16x16x32_bf16 v[80:83], v[148:151], v[208:211], v[80:83]
	v_mfma_f32_16x16x32_bf16 v[76:79], v[156:159], v[208:211], v[76:79]
	s_setprio 0
	s_setprio 1
	v_mfma_f32_16x16x32_bf16 v[120:123], v[160:163], v[176:179], v[120:123]
	v_mfma_f32_16x16x32_bf16 v[116:119], v[168:171], v[176:179], v[116:119]
	v_mfma_f32_16x16x32_bf16 v[104:107], v[160:163], v[184:187], v[104:107]
	v_mfma_f32_16x16x32_bf16 v[100:103], v[168:171], v[184:187], v[100:103]
	v_mfma_f32_16x16x32_bf16 v[88:91], v[160:163], v[192:195], v[88:91]
	v_mfma_f32_16x16x32_bf16 v[84:87], v[168:171], v[192:195], v[84:87]
	v_mfma_f32_16x16x32_bf16 v[72:75], v[160:163], v[204:207], v[72:75]
	v_mfma_f32_16x16x32_bf16 v[68:71], v[168:171], v[204:207], v[68:71]
	v_mfma_f32_16x16x32_bf16 v[120:123], v[164:167], v[180:183], v[120:123]
	v_mfma_f32_16x16x32_bf16 v[116:119], v[172:175], v[180:183], v[116:119]
	v_mfma_f32_16x16x32_bf16 v[104:107], v[164:167], v[188:191], v[104:107]
	v_mfma_f32_16x16x32_bf16 v[100:103], v[172:175], v[188:191], v[100:103]
	v_mfma_f32_16x16x32_bf16 v[88:91], v[164:167], v[196:199], v[88:91]
	v_mfma_f32_16x16x32_bf16 v[84:87], v[172:175], v[196:199], v[84:87]
	v_mfma_f32_16x16x32_bf16 v[72:75], v[164:167], v[208:211], v[72:75]
	v_mfma_f32_16x16x32_bf16 v[68:71], v[172:175], v[208:211], v[68:71]
	s_setprio 0
	s_barrier
	s_add_i32 s4, s74, s16
	v_lshl_add_u64 v[212:213], v[212:213], 0, s[34:35]
	s_mov_b32 m0, s4
	ds_read_b128 v[176:179], v224 offset:49152
	ds_read_b128 v[180:183], v224 offset:50176
	ds_read_b128 v[184:187], v224 offset:51200
	ds_read_b128 v[188:191], v224 offset:52224
	ds_read_b128 v[192:195], v224 offset:53248
	ds_read_b128 v[196:199], v224 offset:54272
	ds_read_b128 v[204:207], v224 offset:55296
	ds_read_b128 v[208:211], v224 offset:56320
	global_load_lds_dwordx4 v[212:213], off
	s_add_i32 m0, s4, 0x2000
	s_add_u32 s4, s52, 0x40080
	v_lshl_add_u64 v[212:213], v[214:215], 0, s[34:35]
	s_addc_u32 s5, s53, 0
	s_add_i32 s52, s75, s16
	global_load_lds_dwordx4 v[212:213], off
	v_lshl_add_u64 v[212:213], s[4:5], 0, v[134:135]
	s_mov_b32 m0, s52
	s_nop 0
	global_load_lds_dwordx4 v[212:213], off
	v_lshl_add_u64 v[212:213], s[4:5], 0, v[132:133]
	s_add_i32 m0, s52, 0x2000
	s_nop 0
	global_load_lds_dwordx4 v[212:213], off
	v_lshl_add_u64 v[212:213], s[12:13], 0, v[134:135]
	s_mov_b32 m0, s59
	s_nop 0
	global_load_lds_dwordx4 v[212:213], off
	v_lshl_add_u64 v[212:213], s[12:13], 0, v[132:133]
	s_mov_b32 m0, s60
	s_nop 0
	global_load_lds_dwordx4 v[212:213], off
	s_waitcnt vmcnt(8)
	s_waitcnt lgkmcnt(0)
	s_barrier
	s_setprio 1
	s_waitcnt lgkmcnt(0)
	v_mfma_f32_16x16x32_bf16 v[64:67], v[144:147], v[176:179], v[64:67]
	v_mfma_f32_16x16x32_bf16 v[60:63], v[152:155], v[176:179], v[60:63]
	v_mfma_f32_16x16x32_bf16 v[48:51], v[144:147], v[184:187], v[48:51]
	v_mfma_f32_16x16x32_bf16 v[44:47], v[152:155], v[184:187], v[44:47]
	v_mfma_f32_16x16x32_bf16 v[32:35], v[144:147], v[192:195], v[32:35]
	v_mfma_f32_16x16x32_bf16 v[28:31], v[152:155], v[192:195], v[28:31]
	v_mfma_f32_16x16x32_bf16 v[16:19], v[144:147], v[204:207], v[16:19]
	v_mfma_f32_16x16x32_bf16 v[12:15], v[152:155], v[204:207], v[12:15]
	v_mfma_f32_16x16x32_bf16 v[64:67], v[148:151], v[180:183], v[64:67]
	v_mfma_f32_16x16x32_bf16 v[60:63], v[156:159], v[180:183], v[60:63]
	v_mfma_f32_16x16x32_bf16 v[48:51], v[148:151], v[188:191], v[48:51]
	v_mfma_f32_16x16x32_bf16 v[44:47], v[156:159], v[188:191], v[44:47]
	v_mfma_f32_16x16x32_bf16 v[32:35], v[148:151], v[196:199], v[32:35]
	v_mfma_f32_16x16x32_bf16 v[28:31], v[156:159], v[196:199], v[28:31]
	v_mfma_f32_16x16x32_bf16 v[16:19], v[148:151], v[208:211], v[16:19]
	v_mfma_f32_16x16x32_bf16 v[12:15], v[156:159], v[208:211], v[12:15]
	s_setprio 0
	s_setprio 1
	v_mfma_f32_16x16x32_bf16 v[56:59], v[160:163], v[176:179], v[56:59]
	v_mfma_f32_16x16x32_bf16 v[52:55], v[168:171], v[176:179], v[52:55]
	v_mfma_f32_16x16x32_bf16 v[40:43], v[160:163], v[184:187], v[40:43]
	v_mfma_f32_16x16x32_bf16 v[36:39], v[168:171], v[184:187], v[36:39]
	v_mfma_f32_16x16x32_bf16 v[24:27], v[160:163], v[192:195], v[24:27]
	v_mfma_f32_16x16x32_bf16 v[20:23], v[168:171], v[192:195], v[20:23]
	v_mfma_f32_16x16x32_bf16 v[8:11], v[160:163], v[204:207], v[8:11]
	v_mfma_f32_16x16x32_bf16 v[4:7], v[168:171], v[204:207], v[4:7]
	v_mfma_f32_16x16x32_bf16 v[56:59], v[164:167], v[180:183], v[56:59]
	v_mfma_f32_16x16x32_bf16 v[52:55], v[172:175], v[180:183], v[52:55]
	v_mfma_f32_16x16x32_bf16 v[40:43], v[164:167], v[188:191], v[40:43]
	v_mfma_f32_16x16x32_bf16 v[36:39], v[172:175], v[188:191], v[36:39]
	v_mfma_f32_16x16x32_bf16 v[24:27], v[164:167], v[196:199], v[24:27]
	v_mfma_f32_16x16x32_bf16 v[20:23], v[172:175], v[196:199], v[20:23]
	v_mfma_f32_16x16x32_bf16 v[8:11], v[164:167], v[208:211], v[8:11]
	v_mfma_f32_16x16x32_bf16 v[4:7], v[172:175], v[208:211], v[4:7]
	s_setprio 0
	s_barrier
	s_add_i32 s73, s73, 2
	s_add_u32 s50, s50, 0x100
	s_addc_u32 s51, s51, 0
	s_cmp_gt_u32 s73, 13

.LBB0_1117:
	s_ashr_i32 s37, s36, 31
	s_lshl_b64 s[4:5], s[36:37], 19
	s_add_u32 s40, s6, s4
	s_addc_u32 s41, s7, s5
	s_and_b64 s[4:5], s[38:39], exec
	s_cselect_b32 s37, s41, s45
	s_cselect_b32 s64, s40, s44
	s_ashr_i32 s23, s22, 31
	s_lshl_b64 s[4:5], s[22:23], 19
	s_add_u32 s42, s8, s4
	s_addc_u32 s43, s9, s5
	s_and_b64 s[4:5], s[38:39], exec
	s_cselect_b32 s23, s43, s49
	s_cselect_b32 s65, s42, s48
	s_add_u32 s68, s64, 0x80
	s_addc_u32 s69, s37, 0
	s_add_u32 s70, s48, 0x100
	s_addc_u32 s71, s49, 0
	s_add_u32 s4, s44, 0x40080
	s_addc_u32 s5, s45, 0
	v_lshl_add_u64 v[108:109], s[4:5], 0, v[210:211]
	v_lshl_add_u64 v[110:111], s[4:5], 0, v[212:213]
	s_mov_b32 s72, -2
	s_mov_b64 s[48:49], 0
	s_waitcnt lgkmcnt(0)
	s_waitcnt vmcnt(0)
	s_add_u32 s4, s44, s48
	s_addc_u32 s5, s45, s49
	s_add_u32 s73, s4, 0x100
	s_addc_u32 s74, s5, 0
	s_add_u32 s50, s70, s48
	s_addc_u32 s51, s71, s49
	s_add_u32 s4, s4, 0x180
	s_addc_u32 s5, s5, 0
	s_add_i32 s75, 0, 0x10000
	s_add_i32 s76, 0, 0x14000
	v_add_u32_e32 v148, s75, v203
	v_add_u32_e32 v164, s76, v203
	ds_read_b128 v[116:119], v148
	ds_read_b128 v[128:131], v148 offset:1024
	ds_read_b128 v[136:139], v148 offset:2048
	ds_read_b128 v[148:151], v148 offset:3072
	ds_read_b128 v[152:155], v164
	ds_read_b128 v[156:159], v164 offset:1024
	ds_read_b128 v[160:163], v164 offset:2048
	ds_read_b128 v[164:167], v164 offset:3072
	s_cmpk_eq_i32 s48, 0x700
	s_cselect_b32 s13, s69, s5
	s_cselect_b32 s12, s68, s4
	s_cselect_b32 s51, s23, s51
	s_cselect_b32 s50, s65, s50
	s_cselect_b32 s5, s37, s74
	s_cselect_b32 s4, s64, s73
	v_lshl_add_u64 v[214:215], v[108:109], 0, s[48:49]
	s_add_i32 m0, s17, 0xc000
	ds_read_b128 v[168:171], v236
	ds_read_b128 v[172:175], v236 offset:1024
	ds_read_b128 v[176:179], v236 offset:2048
	ds_read_b128 v[180:183], v236 offset:3072
	ds_read_b128 v[184:187], v236 offset:4096
	ds_read_b128 v[188:191], v236 offset:5120
	ds_read_b128 v[192:195], v236 offset:6144
	ds_read_b128 v[196:199], v236 offset:7168
	global_load_lds_dwordx4 v[214:215], off
	v_lshl_add_u64 v[214:215], v[110:111], 0, s[48:49]
	s_add_i32 m0, s17, 0xe000
	s_nop 0
	global_load_lds_dwordx4 v[214:215], off
	s_waitcnt vmcnt(8)
	s_waitcnt lgkmcnt(0)
	s_barrier
	s_setprio 1
	s_waitcnt lgkmcnt(0)
	v_mfma_f32_16x16x32_bf16 v[144:147], v[116:119], v[168:171], 0
	v_mfma_f32_16x16x32_bf16 v[140:143], v[136:139], v[168:171], 0
	v_mfma_f32_16x16x32_bf16 v[120:123], v[116:119], v[176:179], 0
	v_mfma_f32_16x16x32_bf16 v[112:115], v[136:139], v[176:179], 0
	v_mfma_f32_16x16x32_bf16 v[96:99], v[116:119], v[184:187], 0
	v_mfma_f32_16x16x32_bf16 v[92:95], v[136:139], v[184:187], 0
	v_mfma_f32_16x16x32_bf16 v[80:83], v[116:119], v[192:195], 0
	v_mfma_f32_16x16x32_bf16 v[76:79], v[136:139], v[192:195], 0
	v_mfma_f32_16x16x32_bf16 v[144:147], v[128:131], v[172:175], v[144:147]
	v_mfma_f32_16x16x32_bf16 v[140:143], v[148:151], v[172:175], v[140:143]
	v_mfma_f32_16x16x32_bf16 v[120:123], v[128:131], v[180:183], v[120:123]
	v_mfma_f32_16x16x32_bf16 v[112:115], v[148:151], v[180:183], v[112:115]
	v_mfma_f32_16x16x32_bf16 v[96:99], v[128:131], v[188:191], v[96:99]
	v_mfma_f32_16x16x32_bf16 v[92:95], v[148:151], v[188:191], v[92:95]
	v_mfma_f32_16x16x32_bf16 v[80:83], v[128:131], v[196:199], v[80:83]
	v_mfma_f32_16x16x32_bf16 v[76:79], v[148:151], v[196:199], v[76:79]
	s_setprio 0
	s_setprio 1
	v_mfma_f32_16x16x32_bf16 v[132:135], v[152:155], v[168:171], 0
	v_mfma_f32_16x16x32_bf16 v[124:127], v[160:163], v[168:171], 0
	v_mfma_f32_16x16x32_bf16 v[104:107], v[152:155], v[176:179], 0
	v_mfma_f32_16x16x32_bf16 v[100:103], v[160:163], v[176:179], 0
	v_mfma_f32_16x16x32_bf16 v[88:91], v[152:155], v[184:187], 0
	v_mfma_f32_16x16x32_bf16 v[84:87], v[160:163], v[184:187], 0
	v_mfma_f32_16x16x32_bf16 v[72:75], v[152:155], v[192:195], 0
	v_mfma_f32_16x16x32_bf16 v[68:71], v[160:163], v[192:195], 0
	v_mfma_f32_16x16x32_bf16 v[132:135], v[156:159], v[172:175], v[132:135]
	v_mfma_f32_16x16x32_bf16 v[124:127], v[164:167], v[172:175], v[124:127]
	v_mfma_f32_16x16x32_bf16 v[104:107], v[156:159], v[180:183], v[104:107]
	v_mfma_f32_16x16x32_bf16 v[100:103], v[164:167], v[180:183], v[100:103]
	v_mfma_f32_16x16x32_bf16 v[88:91], v[156:159], v[188:191], v[88:91]
	v_mfma_f32_16x16x32_bf16 v[84:87], v[164:167], v[188:191], v[84:87]
	v_mfma_f32_16x16x32_bf16 v[72:75], v[156:159], v[196:199], v[72:75]
	v_mfma_f32_16x16x32_bf16 v[68:71], v[164:167], v[196:199], v[68:71]
	s_setprio 0
	s_barrier
	s_add_i32 s73, s75, s16
	v_lshl_add_u64 v[214:215], s[50:51], 0, v[2:3]
	s_mov_b32 m0, s73
	ds_read_b128 v[168:171], v236 offset:16384
	ds_read_b128 v[172:175], v236 offset:17408
	ds_read_b128 v[176:179], v236 offset:18432
	ds_read_b128 v[180:183], v236 offset:19456
	ds_read_b128 v[184:187], v236 offset:20480
	ds_read_b128 v[188:191], v236 offset:21504
	ds_read_b128 v[192:195], v236 offset:22528
	ds_read_b128 v[196:199], v236 offset:23552
	global_load_lds_dwordx4 v[214:215], off
	s_add_i32 m0, s73, 0x2000
	s_add_u32 s74, s50, 0x40000
	v_lshl_add_u64 v[216:217], s[50:51], 0, v[204:205]
	s_addc_u32 s75, s51, 0
	s_add_i32 s73, s76, s16
	global_load_lds_dwordx4 v[216:217], off
	v_lshl_add_u64 v[218:219], s[74:75], 0, v[2:3]
	s_mov_b32 m0, s73
	s_nop 0
	global_load_lds_dwordx4 v[218:219], off
	v_lshl_add_u64 v[218:219], s[74:75], 0, v[204:205]
	s_add_i32 m0, s73, 0x2000
	s_nop 0
	global_load_lds_dwordx4 v[218:219], off
	v_lshl_add_u64 v[218:219], s[4:5], 0, v[208:209]
	s_mov_b32 m0, s17
	s_nop 0
	global_load_lds_dwordx4 v[218:219], off
	v_lshl_add_u64 v[218:219], s[4:5], 0, v[206:207]
	s_mov_b32 m0, s46
	s_nop 0
	global_load_lds_dwordx4 v[218:219], off
	s_waitcnt vmcnt(8)
	s_waitcnt lgkmcnt(0)
	s_barrier
	s_setprio 1
	s_waitcnt lgkmcnt(0)
	v_mfma_f32_16x16x32_bf16 v[64:67], v[116:119], v[168:171], 0
	v_mfma_f32_16x16x32_bf16 v[60:63], v[136:139], v[168:171], 0
	v_mfma_f32_16x16x32_bf16 v[48:51], v[116:119], v[176:179], 0
	v_mfma_f32_16x16x32_bf16 v[44:47], v[136:139], v[176:179], 0
	v_mfma_f32_16x16x32_bf16 v[32:35], v[116:119], v[184:187], 0
	v_mfma_f32_16x16x32_bf16 v[28:31], v[136:139], v[184:187], 0
	v_mfma_f32_16x16x32_bf16 v[16:19], v[116:119], v[192:195], 0
	v_mfma_f32_16x16x32_bf16 v[12:15], v[136:139], v[192:195], 0
	v_mfma_f32_16x16x32_bf16 v[64:67], v[128:131], v[172:175], v[64:67]
	v_mfma_f32_16x16x32_bf16 v[60:63], v[148:151], v[172:175], v[60:63]
	v_mfma_f32_16x16x32_bf16 v[48:51], v[128:131], v[180:183], v[48:51]
	v_mfma_f32_16x16x32_bf16 v[44:47], v[148:151], v[180:183], v[44:47]
	v_mfma_f32_16x16x32_bf16 v[32:35], v[128:131], v[188:191], v[32:35]
	v_mfma_f32_16x16x32_bf16 v[28:31], v[148:151], v[188:191], v[28:31]
	v_mfma_f32_16x16x32_bf16 v[16:19], v[128:131], v[196:199], v[16:19]
	v_mfma_f32_16x16x32_bf16 v[12:15], v[148:151], v[196:199], v[12:15]
	s_setprio 0
	s_setprio 1
	v_mfma_f32_16x16x32_bf16 v[56:59], v[152:155], v[168:171], 0
	v_mfma_f32_16x16x32_bf16 v[52:55], v[160:163], v[168:171], 0
	v_mfma_f32_16x16x32_bf16 v[40:43], v[152:155], v[176:179], 0
	v_mfma_f32_16x16x32_bf16 v[36:39], v[160:163], v[176:179], 0
	v_mfma_f32_16x16x32_bf16 v[24:27], v[152:155], v[184:187], 0
	v_mfma_f32_16x16x32_bf16 v[20:23], v[160:163], v[184:187], 0
	v_mfma_f32_16x16x32_bf16 v[8:11], v[152:155], v[192:195], 0
	v_mfma_f32_16x16x32_bf16 v[4:7], v[160:163], v[192:195], 0
	v_mfma_f32_16x16x32_bf16 v[56:59], v[156:159], v[172:175], v[56:59]
	v_mfma_f32_16x16x32_bf16 v[52:55], v[164:167], v[172:175], v[52:55]
	v_mfma_f32_16x16x32_bf16 v[40:43], v[156:159], v[180:183], v[40:43]
	v_mfma_f32_16x16x32_bf16 v[36:39], v[164:167], v[180:183], v[36:39]
	v_mfma_f32_16x16x32_bf16 v[24:27], v[156:159], v[188:191], v[24:27]
	v_mfma_f32_16x16x32_bf16 v[20:23], v[164:167], v[188:191], v[20:23]
	v_mfma_f32_16x16x32_bf16 v[8:11], v[156:159], v[196:199], v[8:11]
	v_mfma_f32_16x16x32_bf16 v[4:7], v[164:167], v[196:199], v[4:7]
	s_setprio 0
	s_barrier
	s_add_i32 s73, 0, 0x18000
	s_add_i32 s74, 0, 0x1c000
	v_add_u32_e32 v148, s73, v203
	v_add_u32_e32 v164, s74, v203
	ds_read_b128 v[116:119], v148
	ds_read_b128 v[128:131], v148 offset:1024
	ds_read_b128 v[136:139], v148 offset:2048
	ds_read_b128 v[148:151], v148 offset:3072
	ds_read_b128 v[152:155], v164
	ds_read_b128 v[156:159], v164 offset:1024
	ds_read_b128 v[160:163], v164 offset:2048
	ds_read_b128 v[164:167], v164 offset:3072
	s_add_u32 s4, s4, 0x40000
	s_addc_u32 s5, s5, 0
	s_mov_b32 m0, s47
	v_lshl_add_u64 v[218:219], s[4:5], 0, v[208:209]
	ds_read_b128 v[168:171], v236 offset:32768
	ds_read_b128 v[172:175], v236 offset:33792
	ds_read_b128 v[176:179], v236 offset:34816
	ds_read_b128 v[180:183], v236 offset:35840
	ds_read_b128 v[184:187], v236 offset:36864
	ds_read_b128 v[188:191], v236 offset:37888
	ds_read_b128 v[192:195], v236 offset:38912
	ds_read_b128 v[196:199], v236 offset:39936
	global_load_lds_dwordx4 v[218:219], off
	v_lshl_add_u64 v[218:219], s[4:5], 0, v[206:207]
	s_mov_b32 m0, s52
	s_nop 0
	global_load_lds_dwordx4 v[218:219], off
	s_waitcnt vmcnt(8)
	s_waitcnt lgkmcnt(0)
	s_barrier
	s_setprio 1
	s_waitcnt lgkmcnt(0)
	v_mfma_f32_16x16x32_bf16 v[144:147], v[116:119], v[168:171], v[144:147]
	v_mfma_f32_16x16x32_bf16 v[140:143], v[136:139], v[168:171], v[140:143]
	v_mfma_f32_16x16x32_bf16 v[120:123], v[116:119], v[176:179], v[120:123]
	v_mfma_f32_16x16x32_bf16 v[112:115], v[136:139], v[176:179], v[112:115]
	v_mfma_f32_16x16x32_bf16 v[96:99], v[116:119], v[184:187], v[96:99]
	v_mfma_f32_16x16x32_bf16 v[92:95], v[136:139], v[184:187], v[92:95]
	v_mfma_f32_16x16x32_bf16 v[80:83], v[116:119], v[192:195], v[80:83]
	v_mfma_f32_16x16x32_bf16 v[76:79], v[136:139], v[192:195], v[76:79]
	v_mfma_f32_16x16x32_bf16 v[144:147], v[128:131], v[172:175], v[144:147]
	v_mfma_f32_16x16x32_bf16 v[140:143], v[148:151], v[172:175], v[140:143]
	v_mfma_f32_16x16x32_bf16 v[120:123], v[128:131], v[180:183], v[120:123]
	v_mfma_f32_16x16x32_bf16 v[112:115], v[148:151], v[180:183], v[112:115]
	v_mfma_f32_16x16x32_bf16 v[96:99], v[128:131], v[188:191], v[96:99]
	v_mfma_f32_16x16x32_bf16 v[92:95], v[148:151], v[188:191], v[92:95]
	v_mfma_f32_16x16x32_bf16 v[80:83], v[128:131], v[196:199], v[80:83]
	v_mfma_f32_16x16x32_bf16 v[76:79], v[148:151], v[196:199], v[76:79]
	s_setprio 0
	s_setprio 1
	v_mfma_f32_16x16x32_bf16 v[132:135], v[152:155], v[168:171], v[132:135]
	v_mfma_f32_16x16x32_bf16 v[124:127], v[160:163], v[168:171], v[124:127]
	v_mfma_f32_16x16x32_bf16 v[104:107], v[152:155], v[176:179], v[104:107]
	v_mfma_f32_16x16x32_bf16 v[100:103], v[160:163], v[176:179], v[100:103]
	v_mfma_f32_16x16x32_bf16 v[88:91], v[152:155], v[184:187], v[88:91]
	v_mfma_f32_16x16x32_bf16 v[84:87], v[160:163], v[184:187], v[84:87]
	v_mfma_f32_16x16x32_bf16 v[72:75], v[152:155], v[192:195], v[72:75]
	v_mfma_f32_16x16x32_bf16 v[68:71], v[160:163], v[192:195], v[68:71]
	v_mfma_f32_16x16x32_bf16 v[132:135], v[156:159], v[172:175], v[132:135]
	v_mfma_f32_16x16x32_bf16 v[124:127], v[164:167], v[172:175], v[124:127]
	v_mfma_f32_16x16x32_bf16 v[104:107], v[156:159], v[180:183], v[104:107]
	v_mfma_f32_16x16x32_bf16 v[100:103], v[164:167], v[180:183], v[100:103]
	v_mfma_f32_16x16x32_bf16 v[88:91], v[156:159], v[188:191], v[88:91]
	v_mfma_f32_16x16x32_bf16 v[84:87], v[164:167], v[188:191], v[84:87]
	v_mfma_f32_16x16x32_bf16 v[72:75], v[156:159], v[196:199], v[72:75]
	v_mfma_f32_16x16x32_bf16 v[68:71], v[164:167], v[196:199], v[68:71]
	s_setprio 0
	s_barrier
	s_add_i32 s4, s73, s16
	v_lshl_add_u64 v[214:215], v[214:215], 0, s[34:35]
	s_mov_b32 m0, s4
	ds_read_b128 v[168:171], v236 offset:49152
	ds_read_b128 v[172:175], v236 offset:50176
	ds_read_b128 v[176:179], v236 offset:51200
	ds_read_b128 v[180:183], v236 offset:52224
	ds_read_b128 v[184:187], v236 offset:53248
	ds_read_b128 v[188:191], v236 offset:54272
	ds_read_b128 v[192:195], v236 offset:55296
	ds_read_b128 v[196:199], v236 offset:56320
	global_load_lds_dwordx4 v[214:215], off
	s_add_i32 m0, s4, 0x2000
	s_add_u32 s4, s50, 0x40080
	v_lshl_add_u64 v[214:215], v[216:217], 0, s[34:35]
	s_addc_u32 s5, s51, 0
	s_add_i32 s50, s74, s16
	global_load_lds_dwordx4 v[214:215], off
	v_lshl_add_u64 v[214:215], s[4:5], 0, v[2:3]
	s_mov_b32 m0, s50
	s_nop 0
	global_load_lds_dwordx4 v[214:215], off
	v_lshl_add_u64 v[214:215], s[4:5], 0, v[204:205]
	s_add_i32 m0, s50, 0x2000
	s_nop 0
	global_load_lds_dwordx4 v[214:215], off
	v_lshl_add_u64 v[214:215], s[12:13], 0, v[208:209]
	s_mov_b32 m0, s60
	s_nop 0
	global_load_lds_dwordx4 v[214:215], off
	v_lshl_add_u64 v[214:215], s[12:13], 0, v[206:207]
	s_mov_b32 m0, s61
	s_nop 0
	global_load_lds_dwordx4 v[214:215], off
	s_waitcnt vmcnt(8)
	s_waitcnt lgkmcnt(0)
	s_barrier
	s_setprio 1
	s_waitcnt lgkmcnt(0)
	v_mfma_f32_16x16x32_bf16 v[64:67], v[116:119], v[168:171], v[64:67]
	v_mfma_f32_16x16x32_bf16 v[60:63], v[136:139], v[168:171], v[60:63]
	v_mfma_f32_16x16x32_bf16 v[48:51], v[116:119], v[176:179], v[48:51]
	v_mfma_f32_16x16x32_bf16 v[44:47], v[136:139], v[176:179], v[44:47]
	v_mfma_f32_16x16x32_bf16 v[32:35], v[116:119], v[184:187], v[32:35]
	v_mfma_f32_16x16x32_bf16 v[28:31], v[136:139], v[184:187], v[28:31]
	v_mfma_f32_16x16x32_bf16 v[16:19], v[116:119], v[192:195], v[16:19]
	v_mfma_f32_16x16x32_bf16 v[12:15], v[136:139], v[192:195], v[12:15]
	v_mfma_f32_16x16x32_bf16 v[64:67], v[128:131], v[172:175], v[64:67]
	v_mfma_f32_16x16x32_bf16 v[60:63], v[148:151], v[172:175], v[60:63]
	v_mfma_f32_16x16x32_bf16 v[48:51], v[128:131], v[180:183], v[48:51]
	v_mfma_f32_16x16x32_bf16 v[44:47], v[148:151], v[180:183], v[44:47]
	v_mfma_f32_16x16x32_bf16 v[32:35], v[128:131], v[188:191], v[32:35]
	v_mfma_f32_16x16x32_bf16 v[28:31], v[148:151], v[188:191], v[28:31]
	v_mfma_f32_16x16x32_bf16 v[16:19], v[128:131], v[196:199], v[16:19]
	v_mfma_f32_16x16x32_bf16 v[12:15], v[148:151], v[196:199], v[12:15]
	s_setprio 0
	s_setprio 1
	v_mfma_f32_16x16x32_bf16 v[56:59], v[152:155], v[168:171], v[56:59]
	v_mfma_f32_16x16x32_bf16 v[52:55], v[160:163], v[168:171], v[52:55]
	v_mfma_f32_16x16x32_bf16 v[40:43], v[152:155], v[176:179], v[40:43]
	v_mfma_f32_16x16x32_bf16 v[36:39], v[160:163], v[176:179], v[36:39]
	v_mfma_f32_16x16x32_bf16 v[24:27], v[152:155], v[184:187], v[24:27]
	v_mfma_f32_16x16x32_bf16 v[20:23], v[160:163], v[184:187], v[20:23]
	v_mfma_f32_16x16x32_bf16 v[8:11], v[152:155], v[192:195], v[8:11]
	v_mfma_f32_16x16x32_bf16 v[4:7], v[160:163], v[192:195], v[4:7]
	v_mfma_f32_16x16x32_bf16 v[56:59], v[156:159], v[172:175], v[56:59]
	v_mfma_f32_16x16x32_bf16 v[52:55], v[164:167], v[172:175], v[52:55]
	v_mfma_f32_16x16x32_bf16 v[40:43], v[156:159], v[180:183], v[40:43]
	v_mfma_f32_16x16x32_bf16 v[36:39], v[164:167], v[180:183], v[36:39]
	v_mfma_f32_16x16x32_bf16 v[24:27], v[156:159], v[188:191], v[24:27]
	v_mfma_f32_16x16x32_bf16 v[20:23], v[164:167], v[188:191], v[20:23]
	v_mfma_f32_16x16x32_bf16 v[8:11], v[156:159], v[196:199], v[8:11]
	v_mfma_f32_16x16x32_bf16 v[4:7], v[164:167], v[196:199], v[4:7]
	s_setprio 0
	s_barrier
	s_add_i32 s72, s72, 2
	s_add_u32 s48, s48, 0x100
	s_addc_u32 s49, s49, 0
	s_cmp_gt_u32 s72, 13

.LBB0_1205:
	s_ashr_i32 s37, s36, 31
	s_lshl_b64 s[4:5], s[36:37], 19
	s_add_u32 s40, s6, s4
	s_addc_u32 s41, s7, s5
	s_and_b64 s[4:5], s[38:39], exec
	s_cselect_b32 s37, s41, s23
	s_cselect_b32 s61, s40, s22
	s_ashr_i32 s21, s20, 31
	s_lshl_b64 s[4:5], s[20:21], 19
	s_add_u32 s42, s8, s4
	s_addc_u32 s43, s9, s5
	s_and_b64 s[4:5], s[38:39], exec
	s_cselect_b32 s21, s43, s45
	s_cselect_b32 s62, s42, s44
	s_add_u32 s63, s61, 0x80
	s_addc_u32 s64, s37, 0
	s_add_u32 s4, s22, 0x40080
	s_addc_u32 s5, s23, 0
	s_add_u32 s65, s44, 0x100
	v_lshl_add_u64 v[142:143], s[4:5], 0, v[138:139]
	v_lshl_add_u64 v[144:145], s[4:5], 0, v[140:141]
	s_addc_u32 s68, s45, 0
	s_mov_b32 s69, -2
	s_mov_b64 s[44:45], 0
	s_add_u32 s4, s22, s44
	s_addc_u32 s5, s23, s45
	s_add_u32 s70, s4, 0x100
	s_addc_u32 s71, s5, 0
	s_add_u32 s48, s65, s44
	s_addc_u32 s49, s68, s45
	s_add_u32 s4, s4, 0x180
	s_addc_u32 s5, s5, 0
	s_add_i32 s72, 0, 0x10000
	s_add_i32 s73, 0, 0x14000
	v_add_u32_e32 v160, s72, v146
	v_add_u32_e32 v176, s73, v146
	ds_read_b128 v[148:151], v160
	ds_read_b128 v[152:155], v160 offset:1024
	ds_read_b128 v[156:159], v160 offset:2048
	ds_read_b128 v[160:163], v160 offset:3072
	ds_read_b128 v[164:167], v176
	ds_read_b128 v[168:171], v176 offset:1024
	ds_read_b128 v[172:175], v176 offset:2048
	ds_read_b128 v[176:179], v176 offset:3072
	s_cmpk_eq_i32 s44, 0x700
	s_cselect_b32 s13, s64, s5
	s_cselect_b32 s12, s63, s4
	s_cselect_b32 s49, s21, s49
	s_cselect_b32 s48, s62, s48
	s_cselect_b32 s5, s37, s71
	s_cselect_b32 s4, s61, s70
	v_lshl_add_u64 v[216:217], v[142:143], 0, s[44:45]
	s_add_i32 m0, s17, 0xc000
	ds_read_b128 v[180:183], v147
	ds_read_b128 v[184:187], v147 offset:1024
	ds_read_b128 v[188:191], v147 offset:2048
	ds_read_b128 v[192:195], v147 offset:3072
	ds_read_b128 v[196:199], v147 offset:4096
	ds_read_b128 v[204:207], v147 offset:5120
	ds_read_b128 v[208:211], v147 offset:6144
	ds_read_b128 v[212:215], v147 offset:7168
	global_load_lds_dwordx4 v[216:217], off
	v_lshl_add_u64 v[216:217], v[144:145], 0, s[44:45]
	s_add_i32 m0, s17, 0xe000
	s_nop 0
	global_load_lds_dwordx4 v[216:217], off
	s_waitcnt vmcnt(8)
	s_waitcnt lgkmcnt(0)
	s_barrier
	s_setprio 1
	s_waitcnt lgkmcnt(0)
	v_mfma_f32_16x16x32_bf16 v[128:131], v[148:151], v[180:183], 0
	v_mfma_f32_16x16x32_bf16 v[124:127], v[156:159], v[180:183], 0
	v_mfma_f32_16x16x32_bf16 v[120:123], v[148:151], v[188:191], 0
	v_mfma_f32_16x16x32_bf16 v[116:119], v[156:159], v[188:191], 0
	v_mfma_f32_16x16x32_bf16 v[104:107], v[148:151], v[196:199], 0
	v_mfma_f32_16x16x32_bf16 v[100:103], v[156:159], v[196:199], 0
	v_mfma_f32_16x16x32_bf16 v[88:91], v[148:151], v[208:211], 0
	v_mfma_f32_16x16x32_bf16 v[84:87], v[156:159], v[208:211], 0
	v_mfma_f32_16x16x32_bf16 v[128:131], v[152:155], v[184:187], v[128:131]
	v_mfma_f32_16x16x32_bf16 v[124:127], v[160:163], v[184:187], v[124:127]
	v_mfma_f32_16x16x32_bf16 v[120:123], v[152:155], v[192:195], v[120:123]
	v_mfma_f32_16x16x32_bf16 v[116:119], v[160:163], v[192:195], v[116:119]
	v_mfma_f32_16x16x32_bf16 v[104:107], v[152:155], v[204:207], v[104:107]
	v_mfma_f32_16x16x32_bf16 v[100:103], v[160:163], v[204:207], v[100:103]
	v_mfma_f32_16x16x32_bf16 v[88:91], v[152:155], v[212:215], v[88:91]
	v_mfma_f32_16x16x32_bf16 v[84:87], v[160:163], v[212:215], v[84:87]
	s_setprio 0
	s_setprio 1
	v_mfma_f32_16x16x32_bf16 v[112:115], v[164:167], v[180:183], 0
	v_mfma_f32_16x16x32_bf16 v[108:111], v[172:175], v[180:183], 0
	v_mfma_f32_16x16x32_bf16 v[96:99], v[164:167], v[188:191], 0
	v_mfma_f32_16x16x32_bf16 v[92:95], v[172:175], v[188:191], 0
	v_mfma_f32_16x16x32_bf16 v[80:83], v[164:167], v[196:199], 0
	v_mfma_f32_16x16x32_bf16 v[76:79], v[172:175], v[196:199], 0
	v_mfma_f32_16x16x32_bf16 v[72:75], v[164:167], v[208:211], 0
	v_mfma_f32_16x16x32_bf16 v[68:71], v[172:175], v[208:211], 0
	v_mfma_f32_16x16x32_bf16 v[112:115], v[168:171], v[184:187], v[112:115]
	v_mfma_f32_16x16x32_bf16 v[108:111], v[176:179], v[184:187], v[108:111]
	v_mfma_f32_16x16x32_bf16 v[96:99], v[168:171], v[192:195], v[96:99]
	v_mfma_f32_16x16x32_bf16 v[92:95], v[176:179], v[192:195], v[92:95]
	v_mfma_f32_16x16x32_bf16 v[80:83], v[168:171], v[204:207], v[80:83]
	v_mfma_f32_16x16x32_bf16 v[76:79], v[176:179], v[204:207], v[76:79]
	v_mfma_f32_16x16x32_bf16 v[72:75], v[168:171], v[212:215], v[72:75]
	v_mfma_f32_16x16x32_bf16 v[68:71], v[176:179], v[212:215], v[68:71]
	s_setprio 0
	s_barrier
	s_add_i32 s70, s72, s16
	v_lshl_add_u64 v[216:217], s[48:49], 0, v[2:3]
	s_mov_b32 m0, s70
	ds_read_b128 v[180:183], v147 offset:16384
	ds_read_b128 v[184:187], v147 offset:17408
	ds_read_b128 v[188:191], v147 offset:18432
	ds_read_b128 v[192:195], v147 offset:19456
	ds_read_b128 v[196:199], v147 offset:20480
	ds_read_b128 v[204:207], v147 offset:21504
	ds_read_b128 v[208:211], v147 offset:22528
	ds_read_b128 v[212:215], v147 offset:23552
	global_load_lds_dwordx4 v[216:217], off
	s_add_i32 m0, s70, 0x2000
	s_add_u32 s70, s48, 0x40000
	v_lshl_add_u64 v[218:219], s[48:49], 0, v[132:133]
	s_addc_u32 s71, s49, 0
	s_add_i32 s72, s73, s16
	global_load_lds_dwordx4 v[218:219], off
	v_lshl_add_u64 v[220:221], s[70:71], 0, v[2:3]
	s_mov_b32 m0, s72
	s_nop 0
	global_load_lds_dwordx4 v[220:221], off
	v_lshl_add_u64 v[220:221], s[70:71], 0, v[132:133]
	s_add_i32 m0, s72, 0x2000
	s_nop 0
	global_load_lds_dwordx4 v[220:221], off
	v_lshl_add_u64 v[220:221], s[4:5], 0, v[136:137]
	s_mov_b32 m0, s17
	s_nop 0
	global_load_lds_dwordx4 v[220:221], off
	v_lshl_add_u64 v[220:221], s[4:5], 0, v[134:135]
	s_mov_b32 m0, s46
	s_nop 0
	global_load_lds_dwordx4 v[220:221], off
	s_waitcnt vmcnt(8)
	s_waitcnt lgkmcnt(0)
	s_barrier
	s_setprio 1
	s_waitcnt lgkmcnt(0)
	v_mfma_f32_16x16x32_bf16 v[64:67], v[148:151], v[180:183], 0
	v_mfma_f32_16x16x32_bf16 v[60:63], v[156:159], v[180:183], 0
	v_mfma_f32_16x16x32_bf16 v[56:59], v[148:151], v[188:191], 0
	v_mfma_f32_16x16x32_bf16 v[52:55], v[156:159], v[188:191], 0
	v_mfma_f32_16x16x32_bf16 v[40:43], v[148:151], v[196:199], 0
	v_mfma_f32_16x16x32_bf16 v[36:39], v[156:159], v[196:199], 0
	v_mfma_f32_16x16x32_bf16 v[24:27], v[148:151], v[208:211], 0
	v_mfma_f32_16x16x32_bf16 v[20:23], v[156:159], v[208:211], 0
	v_mfma_f32_16x16x32_bf16 v[64:67], v[152:155], v[184:187], v[64:67]
	v_mfma_f32_16x16x32_bf16 v[60:63], v[160:163], v[184:187], v[60:63]
	v_mfma_f32_16x16x32_bf16 v[56:59], v[152:155], v[192:195], v[56:59]
	v_mfma_f32_16x16x32_bf16 v[52:55], v[160:163], v[192:195], v[52:55]
	v_mfma_f32_16x16x32_bf16 v[40:43], v[152:155], v[204:207], v[40:43]
	v_mfma_f32_16x16x32_bf16 v[36:39], v[160:163], v[204:207], v[36:39]
	v_mfma_f32_16x16x32_bf16 v[24:27], v[152:155], v[212:215], v[24:27]
	v_mfma_f32_16x16x32_bf16 v[20:23], v[160:163], v[212:215], v[20:23]
	s_setprio 0
	s_setprio 1
	v_mfma_f32_16x16x32_bf16 v[48:51], v[164:167], v[180:183], 0
	v_mfma_f32_16x16x32_bf16 v[44:47], v[172:175], v[180:183], 0
	v_mfma_f32_16x16x32_bf16 v[32:35], v[164:167], v[188:191], 0
	v_mfma_f32_16x16x32_bf16 v[28:31], v[172:175], v[188:191], 0
	v_mfma_f32_16x16x32_bf16 v[16:19], v[164:167], v[196:199], 0
	v_mfma_f32_16x16x32_bf16 v[12:15], v[172:175], v[196:199], 0
	v_mfma_f32_16x16x32_bf16 v[8:11], v[164:167], v[208:211], 0
	v_mfma_f32_16x16x32_bf16 v[4:7], v[172:175], v[208:211], 0
	v_mfma_f32_16x16x32_bf16 v[48:51], v[168:171], v[184:187], v[48:51]
	v_mfma_f32_16x16x32_bf16 v[44:47], v[176:179], v[184:187], v[44:47]
	v_mfma_f32_16x16x32_bf16 v[32:35], v[168:171], v[192:195], v[32:35]
	v_mfma_f32_16x16x32_bf16 v[28:31], v[176:179], v[192:195], v[28:31]
	v_mfma_f32_16x16x32_bf16 v[16:19], v[168:171], v[204:207], v[16:19]
	v_mfma_f32_16x16x32_bf16 v[12:15], v[176:179], v[204:207], v[12:15]
	v_mfma_f32_16x16x32_bf16 v[8:11], v[168:171], v[212:215], v[8:11]
	v_mfma_f32_16x16x32_bf16 v[4:7], v[176:179], v[212:215], v[4:7]
	s_setprio 0
	s_barrier
	s_add_i32 s70, 0, 0x18000
	s_add_i32 s71, 0, 0x1c000
	v_add_u32_e32 v160, s70, v146
	v_add_u32_e32 v176, s71, v146
	ds_read_b128 v[148:151], v160
	ds_read_b128 v[152:155], v160 offset:1024
	ds_read_b128 v[156:159], v160 offset:2048
	ds_read_b128 v[160:163], v160 offset:3072
	ds_read_b128 v[164:167], v176
	ds_read_b128 v[168:171], v176 offset:1024
	ds_read_b128 v[172:175], v176 offset:2048
	ds_read_b128 v[176:179], v176 offset:3072
	s_add_u32 s4, s4, 0x40000
	s_addc_u32 s5, s5, 0
	s_mov_b32 m0, s47
	v_lshl_add_u64 v[220:221], s[4:5], 0, v[136:137]
	ds_read_b128 v[180:183], v147 offset:32768
	ds_read_b128 v[184:187], v147 offset:33792
	ds_read_b128 v[188:191], v147 offset:34816
	ds_read_b128 v[192:195], v147 offset:35840
	ds_read_b128 v[196:199], v147 offset:36864
	ds_read_b128 v[204:207], v147 offset:37888
	ds_read_b128 v[208:211], v147 offset:38912
	ds_read_b128 v[212:215], v147 offset:39936
	global_load_lds_dwordx4 v[220:221], off
	v_lshl_add_u64 v[220:221], s[4:5], 0, v[134:135]
	s_mov_b32 m0, s50
	s_nop 0
	global_load_lds_dwordx4 v[220:221], off
	s_waitcnt vmcnt(8)
	s_waitcnt lgkmcnt(0)
	s_barrier
	s_setprio 1
	s_waitcnt lgkmcnt(0)
	v_mfma_f32_16x16x32_bf16 v[128:131], v[148:151], v[180:183], v[128:131]
	v_mfma_f32_16x16x32_bf16 v[124:127], v[156:159], v[180:183], v[124:127]
	v_mfma_f32_16x16x32_bf16 v[120:123], v[148:151], v[188:191], v[120:123]
	v_mfma_f32_16x16x32_bf16 v[116:119], v[156:159], v[188:191], v[116:119]
	v_mfma_f32_16x16x32_bf16 v[104:107], v[148:151], v[196:199], v[104:107]
	v_mfma_f32_16x16x32_bf16 v[100:103], v[156:159], v[196:199], v[100:103]
	v_mfma_f32_16x16x32_bf16 v[88:91], v[148:151], v[208:211], v[88:91]
	v_mfma_f32_16x16x32_bf16 v[84:87], v[156:159], v[208:211], v[84:87]
	v_mfma_f32_16x16x32_bf16 v[128:131], v[152:155], v[184:187], v[128:131]
	v_mfma_f32_16x16x32_bf16 v[124:127], v[160:163], v[184:187], v[124:127]
	v_mfma_f32_16x16x32_bf16 v[120:123], v[152:155], v[192:195], v[120:123]
	v_mfma_f32_16x16x32_bf16 v[116:119], v[160:163], v[192:195], v[116:119]
	v_mfma_f32_16x16x32_bf16 v[104:107], v[152:155], v[204:207], v[104:107]
	v_mfma_f32_16x16x32_bf16 v[100:103], v[160:163], v[204:207], v[100:103]
	v_mfma_f32_16x16x32_bf16 v[88:91], v[152:155], v[212:215], v[88:91]
	v_mfma_f32_16x16x32_bf16 v[84:87], v[160:163], v[212:215], v[84:87]
	s_setprio 0
	s_setprio 1
	v_mfma_f32_16x16x32_bf16 v[112:115], v[164:167], v[180:183], v[112:115]
	v_mfma_f32_16x16x32_bf16 v[108:111], v[172:175], v[180:183], v[108:111]
	v_mfma_f32_16x16x32_bf16 v[96:99], v[164:167], v[188:191], v[96:99]
	v_mfma_f32_16x16x32_bf16 v[92:95], v[172:175], v[188:191], v[92:95]
	v_mfma_f32_16x16x32_bf16 v[80:83], v[164:167], v[196:199], v[80:83]
	v_mfma_f32_16x16x32_bf16 v[76:79], v[172:175], v[196:199], v[76:79]
	v_mfma_f32_16x16x32_bf16 v[72:75], v[164:167], v[208:211], v[72:75]
	v_mfma_f32_16x16x32_bf16 v[68:71], v[172:175], v[208:211], v[68:71]
	v_mfma_f32_16x16x32_bf16 v[112:115], v[168:171], v[184:187], v[112:115]
	v_mfma_f32_16x16x32_bf16 v[108:111], v[176:179], v[184:187], v[108:111]
	v_mfma_f32_16x16x32_bf16 v[96:99], v[168:171], v[192:195], v[96:99]
	v_mfma_f32_16x16x32_bf16 v[92:95], v[176:179], v[192:195], v[92:95]
	v_mfma_f32_16x16x32_bf16 v[80:83], v[168:171], v[204:207], v[80:83]
	v_mfma_f32_16x16x32_bf16 v[76:79], v[176:179], v[204:207], v[76:79]
	v_mfma_f32_16x16x32_bf16 v[72:75], v[168:171], v[212:215], v[72:75]
	v_mfma_f32_16x16x32_bf16 v[68:71], v[176:179], v[212:215], v[68:71]
	s_setprio 0
	s_barrier
	s_add_i32 s4, s70, s16
	v_lshl_add_u64 v[216:217], v[216:217], 0, s[34:35]
	s_mov_b32 m0, s4
	ds_read_b128 v[180:183], v147 offset:49152
	ds_read_b128 v[184:187], v147 offset:50176
	ds_read_b128 v[188:191], v147 offset:51200
	ds_read_b128 v[192:195], v147 offset:52224
	ds_read_b128 v[196:199], v147 offset:53248
	ds_read_b128 v[204:207], v147 offset:54272
	ds_read_b128 v[208:211], v147 offset:55296
	ds_read_b128 v[212:215], v147 offset:56320
	global_load_lds_dwordx4 v[216:217], off
	s_add_i32 m0, s4, 0x2000
	s_add_u32 s4, s48, 0x40080
	v_lshl_add_u64 v[216:217], v[218:219], 0, s[34:35]
	s_addc_u32 s5, s49, 0
	s_add_i32 s48, s71, s16
	global_load_lds_dwordx4 v[216:217], off
	v_lshl_add_u64 v[216:217], s[4:5], 0, v[2:3]
	s_mov_b32 m0, s48
	s_nop 0
	global_load_lds_dwordx4 v[216:217], off
	v_lshl_add_u64 v[216:217], s[4:5], 0, v[132:133]
	s_add_i32 m0, s48, 0x2000
	s_nop 0
	global_load_lds_dwordx4 v[216:217], off
	v_lshl_add_u64 v[216:217], s[12:13], 0, v[136:137]
	s_mov_b32 m0, s53
	s_nop 0
	global_load_lds_dwordx4 v[216:217], off
	v_lshl_add_u64 v[216:217], s[12:13], 0, v[134:135]
	s_mov_b32 m0, s56
	s_nop 0
	global_load_lds_dwordx4 v[216:217], off
	s_waitcnt vmcnt(8)
	s_waitcnt lgkmcnt(0)
	s_barrier
	s_setprio 1
	s_waitcnt lgkmcnt(0)
	v_mfma_f32_16x16x32_bf16 v[64:67], v[148:151], v[180:183], v[64:67]
	v_mfma_f32_16x16x32_bf16 v[60:63], v[156:159], v[180:183], v[60:63]
	v_mfma_f32_16x16x32_bf16 v[56:59], v[148:151], v[188:191], v[56:59]
	v_mfma_f32_16x16x32_bf16 v[52:55], v[156:159], v[188:191], v[52:55]
	v_mfma_f32_16x16x32_bf16 v[40:43], v[148:151], v[196:199], v[40:43]
	v_mfma_f32_16x16x32_bf16 v[36:39], v[156:159], v[196:199], v[36:39]
	v_mfma_f32_16x16x32_bf16 v[24:27], v[148:151], v[208:211], v[24:27]
	v_mfma_f32_16x16x32_bf16 v[20:23], v[156:159], v[208:211], v[20:23]
	v_mfma_f32_16x16x32_bf16 v[64:67], v[152:155], v[184:187], v[64:67]
	v_mfma_f32_16x16x32_bf16 v[60:63], v[160:163], v[184:187], v[60:63]
	v_mfma_f32_16x16x32_bf16 v[56:59], v[152:155], v[192:195], v[56:59]
	v_mfma_f32_16x16x32_bf16 v[52:55], v[160:163], v[192:195], v[52:55]
	v_mfma_f32_16x16x32_bf16 v[40:43], v[152:155], v[204:207], v[40:43]
	v_mfma_f32_16x16x32_bf16 v[36:39], v[160:163], v[204:207], v[36:39]
	v_mfma_f32_16x16x32_bf16 v[24:27], v[152:155], v[212:215], v[24:27]
	v_mfma_f32_16x16x32_bf16 v[20:23], v[160:163], v[212:215], v[20:23]
	s_setprio 0
	s_setprio 1
	v_mfma_f32_16x16x32_bf16 v[48:51], v[164:167], v[180:183], v[48:51]
	v_mfma_f32_16x16x32_bf16 v[44:47], v[172:175], v[180:183], v[44:47]
	v_mfma_f32_16x16x32_bf16 v[32:35], v[164:167], v[188:191], v[32:35]
	v_mfma_f32_16x16x32_bf16 v[28:31], v[172:175], v[188:191], v[28:31]
	v_mfma_f32_16x16x32_bf16 v[16:19], v[164:167], v[196:199], v[16:19]
	v_mfma_f32_16x16x32_bf16 v[12:15], v[172:175], v[196:199], v[12:15]
	v_mfma_f32_16x16x32_bf16 v[8:11], v[164:167], v[208:211], v[8:11]
	v_mfma_f32_16x16x32_bf16 v[4:7], v[172:175], v[208:211], v[4:7]
	v_mfma_f32_16x16x32_bf16 v[48:51], v[168:171], v[184:187], v[48:51]
	v_mfma_f32_16x16x32_bf16 v[44:47], v[176:179], v[184:187], v[44:47]
	v_mfma_f32_16x16x32_bf16 v[32:35], v[168:171], v[192:195], v[32:35]
	v_mfma_f32_16x16x32_bf16 v[28:31], v[176:179], v[192:195], v[28:31]
	v_mfma_f32_16x16x32_bf16 v[16:19], v[168:171], v[204:207], v[16:19]
	v_mfma_f32_16x16x32_bf16 v[12:15], v[176:179], v[204:207], v[12:15]
	v_mfma_f32_16x16x32_bf16 v[8:11], v[168:171], v[212:215], v[8:11]
	v_mfma_f32_16x16x32_bf16 v[4:7], v[176:179], v[212:215], v[4:7]
	s_setprio 0
	s_barrier
	s_add_i32 s69, s69, 2
	s_add_u32 s44, s44, 0x100
	s_addc_u32 s45, s45, 0
	s_cmp_gt_u32 s69, 13

.LBB0_1379:
	s_ashr_i32 s43, s42, 31
	s_lshl_b64 s[4:5], s[42:43], 19
	s_add_u32 s44, s6, s4
	s_addc_u32 s45, s7, s5
	s_and_b64 s[4:5], s[38:39], exec
	s_cselect_b32 s43, s45, s41
	s_cselect_b32 s68, s44, s40
	s_ashr_i32 s37, s36, 31
	s_lshl_b64 s[4:5], s[36:37], 19
	s_add_u32 s48, s8, s4
	s_addc_u32 s49, s9, s5
	s_and_b64 s[4:5], s[38:39], exec
	s_cselect_b32 s37, s49, s51
	s_cselect_b32 s69, s48, s50
	s_add_u32 s70, s68, 0x80
	s_addc_u32 s71, s43, 0
	s_add_u32 s4, s40, 0x40080
	s_addc_u32 s5, s41, 0
	s_add_u32 s72, s50, 0x100
	v_lshl_add_u64 v[144:145], s[4:5], 0, v[140:141]
	v_lshl_add_u64 v[146:147], s[4:5], 0, v[142:143]
	s_addc_u32 s73, s51, 0
	s_mov_b32 s74, -2
	s_mov_b64 s[50:51], 0
	s_waitcnt vmcnt(0)
	s_add_u32 s4, s40, s50
	s_addc_u32 s5, s41, s51
	s_add_u32 s75, s4, 0x100
	s_addc_u32 s76, s5, 0
	s_add_u32 s52, s72, s50
	s_addc_u32 s53, s73, s51
	s_add_u32 s4, s4, 0x180
	s_addc_u32 s5, s5, 0
	s_add_i32 s77, 0, 0x10000
	s_add_i32 s78, 0, 0x14000
	v_add_u32_e32 v2, s77, v160
	ds_read_b128 v[148:151], v2
	ds_read_b128 v[152:155], v2 offset:1024
	ds_read_b128 v[156:159], v2 offset:2048
	ds_read_b128 v[162:165], v2 offset:3072
	v_add_u32_e32 v2, s78, v160
	ds_read_b128 v[166:169], v2
	s_waitcnt lgkmcnt(0)
	ds_read_b128 v[170:173], v2 offset:1024
	ds_read_b128 v[174:177], v2 offset:2048
	ds_read_b128 v[178:181], v2 offset:3072
	s_cmpk_eq_i32 s50, 0x700
	s_cselect_b32 s13, s71, s5
	s_cselect_b32 s12, s70, s4
	s_cselect_b32 s53, s37, s53
	s_cselect_b32 s52, s69, s52
	s_cselect_b32 s5, s43, s76
	s_cselect_b32 s4, s68, s75
	v_lshl_add_u64 v[198:199], v[144:145], 0, s[50:51]
	s_add_i32 m0, s17, 0xc000
	ds_read_b128 v[182:185], v161
	ds_read_b128 v[186:189], v161 offset:1024
	ds_read_b128 v[190:193], v161 offset:2048
	ds_read_b128 v[194:197], v161 offset:3072
	ds_read_b128 v[204:207], v161 offset:4096
	ds_read_b128 v[208:211], v161 offset:5120
	ds_read_b128 v[212:215], v161 offset:6144
	ds_read_b128 v[216:219], v161 offset:7168
	global_load_lds_dwordx4 v[198:199], off
	v_lshl_add_u64 v[198:199], v[146:147], 0, s[50:51]
	s_add_i32 m0, s17, 0xe000
	s_nop 0
	global_load_lds_dwordx4 v[198:199], off
	s_waitcnt vmcnt(8)
	s_waitcnt lgkmcnt(0)
	s_barrier
	s_setprio 1
	s_waitcnt lgkmcnt(0)
	v_mfma_f32_16x16x32_bf16 v[128:131], v[148:151], v[182:185], 0
	v_mfma_f32_16x16x32_bf16 v[124:127], v[156:159], v[182:185], 0
	v_mfma_f32_16x16x32_bf16 v[112:115], v[148:151], v[190:193], 0
	v_mfma_f32_16x16x32_bf16 v[108:111], v[156:159], v[190:193], 0
	v_mfma_f32_16x16x32_bf16 v[96:99], v[148:151], v[204:207], 0
	v_mfma_f32_16x16x32_bf16 v[92:95], v[156:159], v[204:207], 0
	v_mfma_f32_16x16x32_bf16 v[80:83], v[148:151], v[212:215], 0
	v_mfma_f32_16x16x32_bf16 v[76:79], v[156:159], v[212:215], 0
	v_mfma_f32_16x16x32_bf16 v[128:131], v[152:155], v[186:189], v[128:131]
	v_mfma_f32_16x16x32_bf16 v[124:127], v[162:165], v[186:189], v[124:127]
	v_mfma_f32_16x16x32_bf16 v[112:115], v[152:155], v[194:197], v[112:115]
	v_mfma_f32_16x16x32_bf16 v[108:111], v[162:165], v[194:197], v[108:111]
	v_mfma_f32_16x16x32_bf16 v[96:99], v[152:155], v[208:211], v[96:99]
	v_mfma_f32_16x16x32_bf16 v[92:95], v[162:165], v[208:211], v[92:95]
	v_mfma_f32_16x16x32_bf16 v[80:83], v[152:155], v[216:219], v[80:83]
	v_mfma_f32_16x16x32_bf16 v[76:79], v[162:165], v[216:219], v[76:79]
	s_setprio 0
	s_setprio 1
	v_mfma_f32_16x16x32_bf16 v[120:123], v[166:169], v[182:185], 0
	v_mfma_f32_16x16x32_bf16 v[116:119], v[174:177], v[182:185], 0
	v_mfma_f32_16x16x32_bf16 v[104:107], v[166:169], v[190:193], 0
	v_mfma_f32_16x16x32_bf16 v[100:103], v[174:177], v[190:193], 0
	v_mfma_f32_16x16x32_bf16 v[88:91], v[166:169], v[204:207], 0
	v_mfma_f32_16x16x32_bf16 v[84:87], v[174:177], v[204:207], 0
	v_mfma_f32_16x16x32_bf16 v[72:75], v[166:169], v[212:215], 0
	v_mfma_f32_16x16x32_bf16 v[68:71], v[174:177], v[212:215], 0
	v_mfma_f32_16x16x32_bf16 v[120:123], v[170:173], v[186:189], v[120:123]
	v_mfma_f32_16x16x32_bf16 v[116:119], v[178:181], v[186:189], v[116:119]
	v_mfma_f32_16x16x32_bf16 v[104:107], v[170:173], v[194:197], v[104:107]
	v_mfma_f32_16x16x32_bf16 v[100:103], v[178:181], v[194:197], v[100:103]
	v_mfma_f32_16x16x32_bf16 v[88:91], v[170:173], v[208:211], v[88:91]
	v_mfma_f32_16x16x32_bf16 v[84:87], v[178:181], v[208:211], v[84:87]
	v_mfma_f32_16x16x32_bf16 v[72:75], v[170:173], v[216:219], v[72:75]
	v_mfma_f32_16x16x32_bf16 v[68:71], v[178:181], v[216:219], v[68:71]
	s_setprio 0
	s_barrier
	s_add_i32 s75, s77, s16
	v_lshl_add_u64 v[198:199], s[52:53], 0, v[136:137]
	s_mov_b32 m0, s75
	ds_read_b128 v[182:185], v161 offset:16384
	ds_read_b128 v[186:189], v161 offset:17408
	ds_read_b128 v[190:193], v161 offset:18432
	ds_read_b128 v[194:197], v161 offset:19456
	ds_read_b128 v[204:207], v161 offset:20480
	ds_read_b128 v[208:211], v161 offset:21504
	ds_read_b128 v[212:215], v161 offset:22528
	ds_read_b128 v[216:219], v161 offset:23552
	global_load_lds_dwordx4 v[198:199], off
	s_add_i32 m0, s75, 0x2000
	s_add_u32 s76, s52, 0x40000
	v_lshl_add_u64 v[220:221], s[52:53], 0, v[132:133]
	s_addc_u32 s77, s53, 0
	s_add_i32 s75, s78, s16
	global_load_lds_dwordx4 v[220:221], off
	v_lshl_add_u64 v[222:223], s[76:77], 0, v[136:137]
	s_mov_b32 m0, s75
	s_nop 0
	global_load_lds_dwordx4 v[222:223], off
	v_lshl_add_u64 v[222:223], s[76:77], 0, v[132:133]
	s_add_i32 m0, s75, 0x2000
	s_nop 0
	global_load_lds_dwordx4 v[222:223], off
	v_lshl_add_u64 v[222:223], s[4:5], 0, v[138:139]
	s_mov_b32 m0, s17
	s_nop 0
	global_load_lds_dwordx4 v[222:223], off
	v_lshl_add_u64 v[222:223], s[4:5], 0, v[134:135]
	s_mov_b32 m0, s46
	s_nop 0
	global_load_lds_dwordx4 v[222:223], off
	s_waitcnt vmcnt(8)
	s_waitcnt lgkmcnt(0)
	s_barrier
	s_setprio 1
	s_waitcnt lgkmcnt(0)
	v_mfma_f32_16x16x32_bf16 v[64:67], v[148:151], v[182:185], 0
	v_mfma_f32_16x16x32_bf16 v[60:63], v[156:159], v[182:185], 0
	v_mfma_f32_16x16x32_bf16 v[48:51], v[148:151], v[190:193], 0
	v_mfma_f32_16x16x32_bf16 v[44:47], v[156:159], v[190:193], 0
	v_mfma_f32_16x16x32_bf16 v[32:35], v[148:151], v[204:207], 0
	v_mfma_f32_16x16x32_bf16 v[28:31], v[156:159], v[204:207], 0
	v_mfma_f32_16x16x32_bf16 v[16:19], v[148:151], v[212:215], 0
	v_mfma_f32_16x16x32_bf16 v[12:15], v[156:159], v[212:215], 0
	v_mfma_f32_16x16x32_bf16 v[64:67], v[152:155], v[186:189], v[64:67]
	v_mfma_f32_16x16x32_bf16 v[60:63], v[162:165], v[186:189], v[60:63]
	v_mfma_f32_16x16x32_bf16 v[48:51], v[152:155], v[194:197], v[48:51]
	v_mfma_f32_16x16x32_bf16 v[44:47], v[162:165], v[194:197], v[44:47]
	v_mfma_f32_16x16x32_bf16 v[32:35], v[152:155], v[208:211], v[32:35]
	v_mfma_f32_16x16x32_bf16 v[28:31], v[162:165], v[208:211], v[28:31]
	v_mfma_f32_16x16x32_bf16 v[16:19], v[152:155], v[216:219], v[16:19]
	v_mfma_f32_16x16x32_bf16 v[12:15], v[162:165], v[216:219], v[12:15]
	s_setprio 0
	s_setprio 1
	v_mfma_f32_16x16x32_bf16 v[56:59], v[166:169], v[182:185], 0
	v_mfma_f32_16x16x32_bf16 v[52:55], v[174:177], v[182:185], 0
	v_mfma_f32_16x16x32_bf16 v[40:43], v[166:169], v[190:193], 0
	v_mfma_f32_16x16x32_bf16 v[36:39], v[174:177], v[190:193], 0
	v_mfma_f32_16x16x32_bf16 v[24:27], v[166:169], v[204:207], 0
	v_mfma_f32_16x16x32_bf16 v[20:23], v[174:177], v[204:207], 0
	v_mfma_f32_16x16x32_bf16 v[8:11], v[166:169], v[212:215], 0
	v_mfma_f32_16x16x32_bf16 v[4:7], v[174:177], v[212:215], 0
	v_mfma_f32_16x16x32_bf16 v[56:59], v[170:173], v[186:189], v[56:59]
	v_mfma_f32_16x16x32_bf16 v[52:55], v[178:181], v[186:189], v[52:55]
	v_mfma_f32_16x16x32_bf16 v[40:43], v[170:173], v[194:197], v[40:43]
	v_mfma_f32_16x16x32_bf16 v[36:39], v[178:181], v[194:197], v[36:39]
	v_mfma_f32_16x16x32_bf16 v[24:27], v[170:173], v[208:211], v[24:27]
	v_mfma_f32_16x16x32_bf16 v[20:23], v[178:181], v[208:211], v[20:23]
	v_mfma_f32_16x16x32_bf16 v[8:11], v[170:173], v[216:219], v[8:11]
	v_mfma_f32_16x16x32_bf16 v[4:7], v[178:181], v[216:219], v[4:7]
	s_setprio 0
	s_barrier
	s_add_i32 s75, 0, 0x18000
	v_add_u32_e32 v2, s75, v160
	s_add_i32 s76, 0, 0x1c000
	ds_read_b128 v[148:151], v2
	ds_read_b128 v[152:155], v2 offset:1024
	ds_read_b128 v[156:159], v2 offset:2048
	ds_read_b128 v[162:165], v2 offset:3072
	v_add_u32_e32 v2, s76, v160
	ds_read_b128 v[166:169], v2
	ds_read_b128 v[170:173], v2 offset:1024
	ds_read_b128 v[174:177], v2 offset:2048
	ds_read_b128 v[178:181], v2 offset:3072
	s_add_u32 s4, s4, 0x40000
	s_addc_u32 s5, s5, 0
	s_mov_b32 m0, s47
	v_lshl_add_u64 v[222:223], s[4:5], 0, v[138:139]
	ds_read_b128 v[182:185], v161 offset:32768
	ds_read_b128 v[186:189], v161 offset:33792
	ds_read_b128 v[190:193], v161 offset:34816
	ds_read_b128 v[194:197], v161 offset:35840
	ds_read_b128 v[204:207], v161 offset:36864
	ds_read_b128 v[208:211], v161 offset:37888
	ds_read_b128 v[212:215], v161 offset:38912
	ds_read_b128 v[216:219], v161 offset:39936
	global_load_lds_dwordx4 v[222:223], off
	v_lshl_add_u64 v[222:223], s[4:5], 0, v[134:135]
	s_mov_b32 m0, s56
	s_nop 0
	global_load_lds_dwordx4 v[222:223], off
	s_waitcnt vmcnt(8)
	s_waitcnt lgkmcnt(0)
	s_barrier
	s_setprio 1
	s_waitcnt lgkmcnt(0)
	v_mfma_f32_16x16x32_bf16 v[128:131], v[148:151], v[182:185], v[128:131]
	v_mfma_f32_16x16x32_bf16 v[124:127], v[156:159], v[182:185], v[124:127]
	v_mfma_f32_16x16x32_bf16 v[112:115], v[148:151], v[190:193], v[112:115]
	v_mfma_f32_16x16x32_bf16 v[108:111], v[156:159], v[190:193], v[108:111]
	v_mfma_f32_16x16x32_bf16 v[96:99], v[148:151], v[204:207], v[96:99]
	v_mfma_f32_16x16x32_bf16 v[92:95], v[156:159], v[204:207], v[92:95]
	v_mfma_f32_16x16x32_bf16 v[80:83], v[148:151], v[212:215], v[80:83]
	v_mfma_f32_16x16x32_bf16 v[76:79], v[156:159], v[212:215], v[76:79]
	v_mfma_f32_16x16x32_bf16 v[128:131], v[152:155], v[186:189], v[128:131]
	v_mfma_f32_16x16x32_bf16 v[124:127], v[162:165], v[186:189], v[124:127]
	v_mfma_f32_16x16x32_bf16 v[112:115], v[152:155], v[194:197], v[112:115]
	v_mfma_f32_16x16x32_bf16 v[108:111], v[162:165], v[194:197], v[108:111]
	v_mfma_f32_16x16x32_bf16 v[96:99], v[152:155], v[208:211], v[96:99]
	v_mfma_f32_16x16x32_bf16 v[92:95], v[162:165], v[208:211], v[92:95]
	v_mfma_f32_16x16x32_bf16 v[80:83], v[152:155], v[216:219], v[80:83]
	v_mfma_f32_16x16x32_bf16 v[76:79], v[162:165], v[216:219], v[76:79]
	s_setprio 0
	s_setprio 1
	v_mfma_f32_16x16x32_bf16 v[120:123], v[166:169], v[182:185], v[120:123]
	v_mfma_f32_16x16x32_bf16 v[116:119], v[174:177], v[182:185], v[116:119]
	v_mfma_f32_16x16x32_bf16 v[104:107], v[166:169], v[190:193], v[104:107]
	v_mfma_f32_16x16x32_bf16 v[100:103], v[174:177], v[190:193], v[100:103]
	v_mfma_f32_16x16x32_bf16 v[88:91], v[166:169], v[204:207], v[88:91]
	v_mfma_f32_16x16x32_bf16 v[84:87], v[174:177], v[204:207], v[84:87]
	v_mfma_f32_16x16x32_bf16 v[72:75], v[166:169], v[212:215], v[72:75]
	v_mfma_f32_16x16x32_bf16 v[68:71], v[174:177], v[212:215], v[68:71]
	v_mfma_f32_16x16x32_bf16 v[120:123], v[170:173], v[186:189], v[120:123]
	v_mfma_f32_16x16x32_bf16 v[116:119], v[178:181], v[186:189], v[116:119]
	v_mfma_f32_16x16x32_bf16 v[104:107], v[170:173], v[194:197], v[104:107]
	v_mfma_f32_16x16x32_bf16 v[100:103], v[178:181], v[194:197], v[100:103]
	v_mfma_f32_16x16x32_bf16 v[88:91], v[170:173], v[208:211], v[88:91]
	v_mfma_f32_16x16x32_bf16 v[84:87], v[178:181], v[208:211], v[84:87]
	v_mfma_f32_16x16x32_bf16 v[72:75], v[170:173], v[216:219], v[72:75]
	v_mfma_f32_16x16x32_bf16 v[68:71], v[178:181], v[216:219], v[68:71]
	s_setprio 0
	s_barrier
	s_add_i32 s4, s75, s16
	v_lshl_add_u64 v[198:199], v[198:199], 0, s[34:35]
	s_mov_b32 m0, s4
	ds_read_b128 v[182:185], v161 offset:49152
	ds_read_b128 v[186:189], v161 offset:50176
	ds_read_b128 v[190:193], v161 offset:51200
	ds_read_b128 v[194:197], v161 offset:52224
	ds_read_b128 v[204:207], v161 offset:53248
	ds_read_b128 v[208:211], v161 offset:54272
	ds_read_b128 v[212:215], v161 offset:55296
	ds_read_b128 v[216:219], v161 offset:56320
	global_load_lds_dwordx4 v[198:199], off
	s_add_i32 m0, s4, 0x2000
	s_add_u32 s4, s52, 0x40080
	v_lshl_add_u64 v[198:199], v[220:221], 0, s[34:35]
	s_addc_u32 s5, s53, 0
	s_add_i32 s52, s76, s16
	global_load_lds_dwordx4 v[198:199], off
	v_lshl_add_u64 v[198:199], s[4:5], 0, v[136:137]
	s_mov_b32 m0, s52
	s_nop 0
	global_load_lds_dwordx4 v[198:199], off
	v_lshl_add_u64 v[198:199], s[4:5], 0, v[132:133]
	s_add_i32 m0, s52, 0x2000
	s_nop 0
	global_load_lds_dwordx4 v[198:199], off
	v_lshl_add_u64 v[198:199], s[12:13], 0, v[138:139]
	s_mov_b32 m0, s61
	s_nop 0
	global_load_lds_dwordx4 v[198:199], off
	v_lshl_add_u64 v[198:199], s[12:13], 0, v[134:135]
	s_mov_b32 m0, s62
	s_nop 0
	global_load_lds_dwordx4 v[198:199], off
	s_waitcnt vmcnt(8)
	s_waitcnt lgkmcnt(0)
	s_barrier
	s_setprio 1
	s_waitcnt lgkmcnt(0)
	v_mfma_f32_16x16x32_bf16 v[64:67], v[148:151], v[182:185], v[64:67]
	v_mfma_f32_16x16x32_bf16 v[60:63], v[156:159], v[182:185], v[60:63]
	v_mfma_f32_16x16x32_bf16 v[48:51], v[148:151], v[190:193], v[48:51]
	v_mfma_f32_16x16x32_bf16 v[44:47], v[156:159], v[190:193], v[44:47]
	v_mfma_f32_16x16x32_bf16 v[32:35], v[148:151], v[204:207], v[32:35]
	v_mfma_f32_16x16x32_bf16 v[28:31], v[156:159], v[204:207], v[28:31]
	v_mfma_f32_16x16x32_bf16 v[16:19], v[148:151], v[212:215], v[16:19]
	v_mfma_f32_16x16x32_bf16 v[12:15], v[156:159], v[212:215], v[12:15]
	v_mfma_f32_16x16x32_bf16 v[64:67], v[152:155], v[186:189], v[64:67]
	v_mfma_f32_16x16x32_bf16 v[60:63], v[162:165], v[186:189], v[60:63]
	v_mfma_f32_16x16x32_bf16 v[48:51], v[152:155], v[194:197], v[48:51]
	v_mfma_f32_16x16x32_bf16 v[44:47], v[162:165], v[194:197], v[44:47]
	v_mfma_f32_16x16x32_bf16 v[32:35], v[152:155], v[208:211], v[32:35]
	v_mfma_f32_16x16x32_bf16 v[28:31], v[162:165], v[208:211], v[28:31]
	v_mfma_f32_16x16x32_bf16 v[16:19], v[152:155], v[216:219], v[16:19]
	v_mfma_f32_16x16x32_bf16 v[12:15], v[162:165], v[216:219], v[12:15]
	s_setprio 0
	s_setprio 1
	v_mfma_f32_16x16x32_bf16 v[56:59], v[166:169], v[182:185], v[56:59]
	v_mfma_f32_16x16x32_bf16 v[52:55], v[174:177], v[182:185], v[52:55]
	v_mfma_f32_16x16x32_bf16 v[40:43], v[166:169], v[190:193], v[40:43]
	v_mfma_f32_16x16x32_bf16 v[36:39], v[174:177], v[190:193], v[36:39]
	v_mfma_f32_16x16x32_bf16 v[24:27], v[166:169], v[204:207], v[24:27]
	v_mfma_f32_16x16x32_bf16 v[20:23], v[174:177], v[204:207], v[20:23]
	v_mfma_f32_16x16x32_bf16 v[8:11], v[166:169], v[212:215], v[8:11]
	v_mfma_f32_16x16x32_bf16 v[4:7], v[174:177], v[212:215], v[4:7]
	v_mfma_f32_16x16x32_bf16 v[56:59], v[170:173], v[186:189], v[56:59]
	v_mfma_f32_16x16x32_bf16 v[52:55], v[178:181], v[186:189], v[52:55]
	v_mfma_f32_16x16x32_bf16 v[40:43], v[170:173], v[194:197], v[40:43]
	v_mfma_f32_16x16x32_bf16 v[36:39], v[178:181], v[194:197], v[36:39]
	v_mfma_f32_16x16x32_bf16 v[24:27], v[170:173], v[208:211], v[24:27]
	v_mfma_f32_16x16x32_bf16 v[20:23], v[178:181], v[208:211], v[20:23]
	v_mfma_f32_16x16x32_bf16 v[8:11], v[170:173], v[216:219], v[8:11]
	v_mfma_f32_16x16x32_bf16 v[4:7], v[178:181], v[216:219], v[4:7]
	s_setprio 0
	s_barrier
	s_add_i32 s74, s74, 2
	s_add_u32 s50, s50, 0x100
	s_addc_u32 s51, s51, 0
	s_cmp_gt_u32 s74, 13

.LBB0_1458:
	s_ashr_i32 s41, s40, 31
	s_lshl_b64 s[4:5], s[40:41], 21
	s_add_u32 s42, s6, s4
	s_addc_u32 s43, s7, s5
	s_and_b64 s[4:5], s[38:39], exec
	s_cselect_b32 s41, s43, s49
	s_cselect_b32 s68, s42, s48
	s_ashr_i32 s37, s36, 31
	s_lshl_b64 s[4:5], s[36:37], 21
	s_add_u32 s44, s8, s4
	s_addc_u32 s45, s9, s5
	s_and_b64 s[4:5], s[38:39], exec
	s_cselect_b32 s37, s45, s51
	s_cselect_b32 s69, s44, s50
	s_add_u32 s70, s68, 0x80
	s_addc_u32 s71, s41, 0
	s_add_u32 s72, s50, 0x100
	s_addc_u32 s73, s51, 0
	s_add_u32 s4, s48, 0x100080
	s_addc_u32 s5, s49, 0
	v_lshl_add_u64 v[112:113], s[4:5], 0, v[210:211]
	v_lshl_add_u64 v[114:115], s[4:5], 0, v[212:213]
	s_mov_b32 s74, -2
	s_mov_b64 s[50:51], 0
	s_waitcnt lgkmcnt(0)
	s_waitcnt vmcnt(0)
	s_add_u32 s4, s48, s50
	s_addc_u32 s5, s49, s51
	s_add_u32 s75, s4, 0x100
	s_addc_u32 s76, s5, 0
	s_add_u32 s52, s72, s50
	s_addc_u32 s53, s73, s51
	s_add_u32 s4, s4, 0x180
	s_addc_u32 s5, s5, 0
	s_add_i32 s77, 0, 0x10000
	s_add_i32 s78, 0, 0x14000
	v_add_u32_e32 v148, s77, v203
	v_add_u32_e32 v164, s78, v203
	ds_read_b128 v[120:123], v148
	ds_read_b128 v[132:135], v148 offset:1024
	ds_read_b128 v[144:147], v148 offset:2048
	ds_read_b128 v[148:151], v148 offset:3072
	ds_read_b128 v[152:155], v164
	ds_read_b128 v[156:159], v164 offset:1024
	ds_read_b128 v[160:163], v164 offset:2048
	ds_read_b128 v[164:167], v164 offset:3072
	s_cmpk_eq_i32 s50, 0x1f00
	s_cselect_b32 s13, s71, s5
	s_cselect_b32 s12, s70, s4
	s_cselect_b32 s53, s37, s53
	s_cselect_b32 s52, s69, s52
	s_cselect_b32 s5, s41, s76
	s_cselect_b32 s4, s68, s75
	v_lshl_add_u64 v[214:215], v[112:113], 0, s[50:51]
	s_add_i32 m0, s17, 0xc000
	ds_read_b128 v[168:171], v233
	ds_read_b128 v[172:175], v233 offset:1024
	ds_read_b128 v[176:179], v233 offset:2048
	ds_read_b128 v[180:183], v233 offset:3072
	ds_read_b128 v[184:187], v233 offset:4096
	ds_read_b128 v[188:191], v233 offset:5120
	ds_read_b128 v[192:195], v233 offset:6144
	ds_read_b128 v[196:199], v233 offset:7168
	global_load_lds_dwordx4 v[214:215], off
	v_lshl_add_u64 v[214:215], v[114:115], 0, s[50:51]
	s_add_i32 m0, s17, 0xe000
	s_nop 0
	global_load_lds_dwordx4 v[214:215], off
	s_waitcnt vmcnt(8)
	s_waitcnt lgkmcnt(0)
	s_barrier
	s_setprio 1
	s_waitcnt lgkmcnt(0)
	v_mfma_f32_16x16x32_bf16 v[140:143], v[120:123], v[168:171], 0
	v_mfma_f32_16x16x32_bf16 v[136:139], v[144:147], v[168:171], 0
	v_mfma_f32_16x16x32_bf16 v[116:119], v[120:123], v[176:179], 0
	v_mfma_f32_16x16x32_bf16 v[108:111], v[144:147], v[176:179], 0
	v_mfma_f32_16x16x32_bf16 v[96:99], v[120:123], v[184:187], 0
	v_mfma_f32_16x16x32_bf16 v[92:95], v[144:147], v[184:187], 0
	v_mfma_f32_16x16x32_bf16 v[80:83], v[120:123], v[192:195], 0
	v_mfma_f32_16x16x32_bf16 v[76:79], v[144:147], v[192:195], 0
	v_mfma_f32_16x16x32_bf16 v[140:143], v[132:135], v[172:175], v[140:143]
	v_mfma_f32_16x16x32_bf16 v[136:139], v[148:151], v[172:175], v[136:139]
	v_mfma_f32_16x16x32_bf16 v[116:119], v[132:135], v[180:183], v[116:119]
	v_mfma_f32_16x16x32_bf16 v[108:111], v[148:151], v[180:183], v[108:111]
	v_mfma_f32_16x16x32_bf16 v[96:99], v[132:135], v[188:191], v[96:99]
	v_mfma_f32_16x16x32_bf16 v[92:95], v[148:151], v[188:191], v[92:95]
	v_mfma_f32_16x16x32_bf16 v[80:83], v[132:135], v[196:199], v[80:83]
	v_mfma_f32_16x16x32_bf16 v[76:79], v[148:151], v[196:199], v[76:79]
	s_setprio 0
	s_setprio 1
	v_mfma_f32_16x16x32_bf16 v[128:131], v[152:155], v[168:171], 0
	v_mfma_f32_16x16x32_bf16 v[124:127], v[160:163], v[168:171], 0
	v_mfma_f32_16x16x32_bf16 v[104:107], v[152:155], v[176:179], 0
	v_mfma_f32_16x16x32_bf16 v[100:103], v[160:163], v[176:179], 0
	v_mfma_f32_16x16x32_bf16 v[88:91], v[152:155], v[184:187], 0
	v_mfma_f32_16x16x32_bf16 v[84:87], v[160:163], v[184:187], 0
	v_mfma_f32_16x16x32_bf16 v[72:75], v[152:155], v[192:195], 0
	v_mfma_f32_16x16x32_bf16 v[68:71], v[160:163], v[192:195], 0
	v_mfma_f32_16x16x32_bf16 v[128:131], v[156:159], v[172:175], v[128:131]
	v_mfma_f32_16x16x32_bf16 v[124:127], v[164:167], v[172:175], v[124:127]
	v_mfma_f32_16x16x32_bf16 v[104:107], v[156:159], v[180:183], v[104:107]
	v_mfma_f32_16x16x32_bf16 v[100:103], v[164:167], v[180:183], v[100:103]
	v_mfma_f32_16x16x32_bf16 v[88:91], v[156:159], v[188:191], v[88:91]
	v_mfma_f32_16x16x32_bf16 v[84:87], v[164:167], v[188:191], v[84:87]
	v_mfma_f32_16x16x32_bf16 v[72:75], v[156:159], v[196:199], v[72:75]
	v_mfma_f32_16x16x32_bf16 v[68:71], v[164:167], v[196:199], v[68:71]
	s_setprio 0
	s_barrier
	s_add_i32 s75, s77, s16
	v_lshl_add_u64 v[214:215], s[52:53], 0, v[2:3]
	s_mov_b32 m0, s75
	ds_read_b128 v[168:171], v233 offset:16384
	ds_read_b128 v[172:175], v233 offset:17408
	ds_read_b128 v[176:179], v233 offset:18432
	ds_read_b128 v[180:183], v233 offset:19456
	ds_read_b128 v[184:187], v233 offset:20480
	ds_read_b128 v[188:191], v233 offset:21504
	ds_read_b128 v[192:195], v233 offset:22528
	ds_read_b128 v[196:199], v233 offset:23552
	global_load_lds_dwordx4 v[214:215], off
	s_add_i32 m0, s75, 0x2000
	s_add_u32 s76, s52, 0x100000
	v_lshl_add_u64 v[216:217], s[52:53], 0, v[204:205]
	s_addc_u32 s77, s53, 0
	s_add_i32 s75, s78, s16
	global_load_lds_dwordx4 v[216:217], off
	v_lshl_add_u64 v[218:219], s[76:77], 0, v[2:3]
	s_mov_b32 m0, s75
	s_nop 0
	global_load_lds_dwordx4 v[218:219], off
	v_lshl_add_u64 v[218:219], s[76:77], 0, v[204:205]
	s_add_i32 m0, s75, 0x2000
	s_nop 0
	global_load_lds_dwordx4 v[218:219], off
	v_lshl_add_u64 v[218:219], s[4:5], 0, v[208:209]
	s_mov_b32 m0, s17
	s_nop 0
	global_load_lds_dwordx4 v[218:219], off
	v_lshl_add_u64 v[218:219], s[4:5], 0, v[206:207]
	s_mov_b32 m0, s46
	s_nop 0
	global_load_lds_dwordx4 v[218:219], off
	s_waitcnt vmcnt(8)
	s_waitcnt lgkmcnt(0)
	s_barrier
	s_setprio 1
	s_waitcnt lgkmcnt(0)
	v_mfma_f32_16x16x32_bf16 v[64:67], v[120:123], v[168:171], 0
	v_mfma_f32_16x16x32_bf16 v[60:63], v[144:147], v[168:171], 0
	v_mfma_f32_16x16x32_bf16 v[48:51], v[120:123], v[176:179], 0
	v_mfma_f32_16x16x32_bf16 v[44:47], v[144:147], v[176:179], 0
	v_mfma_f32_16x16x32_bf16 v[32:35], v[120:123], v[184:187], 0
	v_mfma_f32_16x16x32_bf16 v[28:31], v[144:147], v[184:187], 0
	v_mfma_f32_16x16x32_bf16 v[16:19], v[120:123], v[192:195], 0
	v_mfma_f32_16x16x32_bf16 v[12:15], v[144:147], v[192:195], 0
	v_mfma_f32_16x16x32_bf16 v[64:67], v[132:135], v[172:175], v[64:67]
	v_mfma_f32_16x16x32_bf16 v[60:63], v[148:151], v[172:175], v[60:63]
	v_mfma_f32_16x16x32_bf16 v[48:51], v[132:135], v[180:183], v[48:51]
	v_mfma_f32_16x16x32_bf16 v[44:47], v[148:151], v[180:183], v[44:47]
	v_mfma_f32_16x16x32_bf16 v[32:35], v[132:135], v[188:191], v[32:35]
	v_mfma_f32_16x16x32_bf16 v[28:31], v[148:151], v[188:191], v[28:31]
	v_mfma_f32_16x16x32_bf16 v[16:19], v[132:135], v[196:199], v[16:19]
	v_mfma_f32_16x16x32_bf16 v[12:15], v[148:151], v[196:199], v[12:15]
	s_setprio 0
	s_setprio 1
	v_mfma_f32_16x16x32_bf16 v[56:59], v[152:155], v[168:171], 0
	v_mfma_f32_16x16x32_bf16 v[52:55], v[160:163], v[168:171], 0
	v_mfma_f32_16x16x32_bf16 v[40:43], v[152:155], v[176:179], 0
	v_mfma_f32_16x16x32_bf16 v[36:39], v[160:163], v[176:179], 0
	v_mfma_f32_16x16x32_bf16 v[24:27], v[152:155], v[184:187], 0
	v_mfma_f32_16x16x32_bf16 v[20:23], v[160:163], v[184:187], 0
	v_mfma_f32_16x16x32_bf16 v[8:11], v[152:155], v[192:195], 0
	v_mfma_f32_16x16x32_bf16 v[4:7], v[160:163], v[192:195], 0
	v_mfma_f32_16x16x32_bf16 v[56:59], v[156:159], v[172:175], v[56:59]
	v_mfma_f32_16x16x32_bf16 v[52:55], v[164:167], v[172:175], v[52:55]
	v_mfma_f32_16x16x32_bf16 v[40:43], v[156:159], v[180:183], v[40:43]
	v_mfma_f32_16x16x32_bf16 v[36:39], v[164:167], v[180:183], v[36:39]
	v_mfma_f32_16x16x32_bf16 v[24:27], v[156:159], v[188:191], v[24:27]
	v_mfma_f32_16x16x32_bf16 v[20:23], v[164:167], v[188:191], v[20:23]
	v_mfma_f32_16x16x32_bf16 v[8:11], v[156:159], v[196:199], v[8:11]
	v_mfma_f32_16x16x32_bf16 v[4:7], v[164:167], v[196:199], v[4:7]
	s_setprio 0
	s_barrier
	s_add_i32 s75, 0, 0x18000
	s_add_i32 s76, 0, 0x1c000
	v_add_u32_e32 v148, s75, v203
	v_add_u32_e32 v164, s76, v203
	ds_read_b128 v[120:123], v148
	ds_read_b128 v[132:135], v148 offset:1024
	ds_read_b128 v[144:147], v148 offset:2048
	ds_read_b128 v[148:151], v148 offset:3072
	ds_read_b128 v[152:155], v164
	ds_read_b128 v[156:159], v164 offset:1024
	ds_read_b128 v[160:163], v164 offset:2048
	ds_read_b128 v[164:167], v164 offset:3072
	s_add_u32 s4, s4, 0x100000
	s_addc_u32 s5, s5, 0
	s_mov_b32 m0, s47
	v_lshl_add_u64 v[218:219], s[4:5], 0, v[208:209]
	ds_read_b128 v[168:171], v233 offset:32768
	ds_read_b128 v[172:175], v233 offset:33792
	ds_read_b128 v[176:179], v233 offset:34816
	ds_read_b128 v[180:183], v233 offset:35840
	ds_read_b128 v[184:187], v233 offset:36864
	ds_read_b128 v[188:191], v233 offset:37888
	ds_read_b128 v[192:195], v233 offset:38912
	ds_read_b128 v[196:199], v233 offset:39936
	global_load_lds_dwordx4 v[218:219], off
	v_lshl_add_u64 v[218:219], s[4:5], 0, v[206:207]
	s_mov_b32 m0, s58
	s_nop 0
	global_load_lds_dwordx4 v[218:219], off
	s_waitcnt vmcnt(8)
	s_waitcnt lgkmcnt(0)
	s_barrier
	s_setprio 1
	s_waitcnt lgkmcnt(0)
	v_mfma_f32_16x16x32_bf16 v[140:143], v[120:123], v[168:171], v[140:143]
	v_mfma_f32_16x16x32_bf16 v[136:139], v[144:147], v[168:171], v[136:139]
	v_mfma_f32_16x16x32_bf16 v[116:119], v[120:123], v[176:179], v[116:119]
	v_mfma_f32_16x16x32_bf16 v[108:111], v[144:147], v[176:179], v[108:111]
	v_mfma_f32_16x16x32_bf16 v[96:99], v[120:123], v[184:187], v[96:99]
	v_mfma_f32_16x16x32_bf16 v[92:95], v[144:147], v[184:187], v[92:95]
	v_mfma_f32_16x16x32_bf16 v[80:83], v[120:123], v[192:195], v[80:83]
	v_mfma_f32_16x16x32_bf16 v[76:79], v[144:147], v[192:195], v[76:79]
	v_mfma_f32_16x16x32_bf16 v[140:143], v[132:135], v[172:175], v[140:143]
	v_mfma_f32_16x16x32_bf16 v[136:139], v[148:151], v[172:175], v[136:139]
	v_mfma_f32_16x16x32_bf16 v[116:119], v[132:135], v[180:183], v[116:119]
	v_mfma_f32_16x16x32_bf16 v[108:111], v[148:151], v[180:183], v[108:111]
	v_mfma_f32_16x16x32_bf16 v[96:99], v[132:135], v[188:191], v[96:99]
	v_mfma_f32_16x16x32_bf16 v[92:95], v[148:151], v[188:191], v[92:95]
	v_mfma_f32_16x16x32_bf16 v[80:83], v[132:135], v[196:199], v[80:83]
	v_mfma_f32_16x16x32_bf16 v[76:79], v[148:151], v[196:199], v[76:79]
	s_setprio 0
	s_setprio 1
	v_mfma_f32_16x16x32_bf16 v[128:131], v[152:155], v[168:171], v[128:131]
	v_mfma_f32_16x16x32_bf16 v[124:127], v[160:163], v[168:171], v[124:127]
	v_mfma_f32_16x16x32_bf16 v[104:107], v[152:155], v[176:179], v[104:107]
	v_mfma_f32_16x16x32_bf16 v[100:103], v[160:163], v[176:179], v[100:103]
	v_mfma_f32_16x16x32_bf16 v[88:91], v[152:155], v[184:187], v[88:91]
	v_mfma_f32_16x16x32_bf16 v[84:87], v[160:163], v[184:187], v[84:87]
	v_mfma_f32_16x16x32_bf16 v[72:75], v[152:155], v[192:195], v[72:75]
	v_mfma_f32_16x16x32_bf16 v[68:71], v[160:163], v[192:195], v[68:71]
	v_mfma_f32_16x16x32_bf16 v[128:131], v[156:159], v[172:175], v[128:131]
	v_mfma_f32_16x16x32_bf16 v[124:127], v[164:167], v[172:175], v[124:127]
	v_mfma_f32_16x16x32_bf16 v[104:107], v[156:159], v[180:183], v[104:107]
	v_mfma_f32_16x16x32_bf16 v[100:103], v[164:167], v[180:183], v[100:103]
	v_mfma_f32_16x16x32_bf16 v[88:91], v[156:159], v[188:191], v[88:91]
	v_mfma_f32_16x16x32_bf16 v[84:87], v[164:167], v[188:191], v[84:87]
	v_mfma_f32_16x16x32_bf16 v[72:75], v[156:159], v[196:199], v[72:75]
	v_mfma_f32_16x16x32_bf16 v[68:71], v[164:167], v[196:199], v[68:71]
	s_setprio 0
	s_barrier
	s_add_i32 s4, s75, s16
	v_lshl_add_u64 v[214:215], v[214:215], 0, s[34:35]
	s_mov_b32 m0, s4
	ds_read_b128 v[168:171], v233 offset:49152
	ds_read_b128 v[172:175], v233 offset:50176
	ds_read_b128 v[176:179], v233 offset:51200
	ds_read_b128 v[180:183], v233 offset:52224
	ds_read_b128 v[184:187], v233 offset:53248
	ds_read_b128 v[188:191], v233 offset:54272
	ds_read_b128 v[192:195], v233 offset:55296
	ds_read_b128 v[196:199], v233 offset:56320
	global_load_lds_dwordx4 v[214:215], off
	s_add_i32 m0, s4, 0x2000
	s_add_u32 s4, s52, 0x100080
	v_lshl_add_u64 v[214:215], v[216:217], 0, s[34:35]
	s_addc_u32 s5, s53, 0
	s_add_i32 s52, s76, s16
	global_load_lds_dwordx4 v[214:215], off
	v_lshl_add_u64 v[214:215], s[4:5], 0, v[2:3]
	s_mov_b32 m0, s52
	s_nop 0
	global_load_lds_dwordx4 v[214:215], off
	v_lshl_add_u64 v[214:215], s[4:5], 0, v[204:205]
	s_add_i32 m0, s52, 0x2000
	s_nop 0
	global_load_lds_dwordx4 v[214:215], off
	v_lshl_add_u64 v[214:215], s[12:13], 0, v[208:209]
	s_mov_b32 m0, s62
	s_nop 0
	global_load_lds_dwordx4 v[214:215], off
	v_lshl_add_u64 v[214:215], s[12:13], 0, v[206:207]
	s_mov_b32 m0, s63
	s_nop 0
	global_load_lds_dwordx4 v[214:215], off
	s_waitcnt vmcnt(8)
	s_waitcnt lgkmcnt(0)
	s_barrier
	s_setprio 1
	s_waitcnt lgkmcnt(0)
	v_mfma_f32_16x16x32_bf16 v[64:67], v[120:123], v[168:171], v[64:67]
	v_mfma_f32_16x16x32_bf16 v[60:63], v[144:147], v[168:171], v[60:63]
	v_mfma_f32_16x16x32_bf16 v[48:51], v[120:123], v[176:179], v[48:51]
	v_mfma_f32_16x16x32_bf16 v[44:47], v[144:147], v[176:179], v[44:47]
	v_mfma_f32_16x16x32_bf16 v[32:35], v[120:123], v[184:187], v[32:35]
	v_mfma_f32_16x16x32_bf16 v[28:31], v[144:147], v[184:187], v[28:31]
	v_mfma_f32_16x16x32_bf16 v[16:19], v[120:123], v[192:195], v[16:19]
	v_mfma_f32_16x16x32_bf16 v[12:15], v[144:147], v[192:195], v[12:15]
	v_mfma_f32_16x16x32_bf16 v[64:67], v[132:135], v[172:175], v[64:67]
	v_mfma_f32_16x16x32_bf16 v[60:63], v[148:151], v[172:175], v[60:63]
	v_mfma_f32_16x16x32_bf16 v[48:51], v[132:135], v[180:183], v[48:51]
	v_mfma_f32_16x16x32_bf16 v[44:47], v[148:151], v[180:183], v[44:47]
	v_mfma_f32_16x16x32_bf16 v[32:35], v[132:135], v[188:191], v[32:35]
	v_mfma_f32_16x16x32_bf16 v[28:31], v[148:151], v[188:191], v[28:31]
	v_mfma_f32_16x16x32_bf16 v[16:19], v[132:135], v[196:199], v[16:19]
	v_mfma_f32_16x16x32_bf16 v[12:15], v[148:151], v[196:199], v[12:15]
	s_setprio 0
	s_setprio 1
	v_mfma_f32_16x16x32_bf16 v[56:59], v[152:155], v[168:171], v[56:59]
	v_mfma_f32_16x16x32_bf16 v[52:55], v[160:163], v[168:171], v[52:55]
	v_mfma_f32_16x16x32_bf16 v[40:43], v[152:155], v[176:179], v[40:43]
	v_mfma_f32_16x16x32_bf16 v[36:39], v[160:163], v[176:179], v[36:39]
	v_mfma_f32_16x16x32_bf16 v[24:27], v[152:155], v[184:187], v[24:27]
	v_mfma_f32_16x16x32_bf16 v[20:23], v[160:163], v[184:187], v[20:23]
	v_mfma_f32_16x16x32_bf16 v[8:11], v[152:155], v[192:195], v[8:11]
	v_mfma_f32_16x16x32_bf16 v[4:7], v[160:163], v[192:195], v[4:7]
	v_mfma_f32_16x16x32_bf16 v[56:59], v[156:159], v[172:175], v[56:59]
	v_mfma_f32_16x16x32_bf16 v[52:55], v[164:167], v[172:175], v[52:55]
	v_mfma_f32_16x16x32_bf16 v[40:43], v[156:159], v[180:183], v[40:43]
	v_mfma_f32_16x16x32_bf16 v[36:39], v[164:167], v[180:183], v[36:39]
	v_mfma_f32_16x16x32_bf16 v[24:27], v[156:159], v[188:191], v[24:27]
	v_mfma_f32_16x16x32_bf16 v[20:23], v[164:167], v[188:191], v[20:23]
	v_mfma_f32_16x16x32_bf16 v[8:11], v[156:159], v[196:199], v[8:11]
	v_mfma_f32_16x16x32_bf16 v[4:7], v[164:167], v[196:199], v[4:7]
	s_setprio 0
	s_barrier
	s_add_i32 s74, s74, 2
	s_add_u32 s50, s50, 0x100
	s_addc_u32 s51, s51, 0
	s_cmp_gt_u32 s74, 61
